# GEMM K-loops: each load segment issues its LDS-DMA loads before its ds_read fragment loads (was after)
# baseline (speedup 1.0000x reference)
; #define PG8_STAGE(bufoff, gbase, voff) do { _Pragma("unroll") for (int _i = 0; _i < 2; ++_i) \
;         __builtin_amdgcn_global_load_lds((const unsigned*)((const char*)(gbase) + (voff)[_i]), (LAS unsigned*)(lds + (bufoff) + ldsw + _i * 8192), 16, 0, 0); } while (0)
; #define PG8_LDA(dst, b, h) do { _Pragma("unroll") for (int m = 0; m < 4; ++m) _Pragma("unroll") for (int k = 0; k < 2; ++k) dst[m][k] = *(const LAS bf16x8*)(lds + PG8_SA(b, h) + aoff + m * 2048 + k * 1024); } while (0)
; #define PG8_LDB(dst, b, h) do { _Pragma("unroll") for (int n = 0; n < 2; ++n) _Pragma("unroll") for (int k = 0; k < 2; ++k) dst[n][k] = *(const LAS bf16x8*)(lds + PG8_SB(b, h) + boff + n * 2048 + k * 1024); } while (0)
; #define PG8_WAIT_V(n) asm volatile("s_waitcnt vmcnt(" #n ")" ::: "memory")
; #define PG8_WAIT_L(n) asm volatile("s_waitcnt lgkmcnt(" #n ")" ::: "memory")
; #define PG8_BAR __builtin_amdgcn_s_barrier()
; #define PG8_SCHED __builtin_amdgcn_sched_barrier(0)
; template <class Epi, class Sched, bool ALIGN_EPI = true, bool SP2 = true, class Side = NoSide>
; __device__ __forceinline__ void gemm_phase(LAS unsigned char* lds, const Gemm g, const Sched& S, const Epi& E, const Side side = Side()) {
;     ...
;             PG8_WAIT_L(0); PG8_BAR; PG8_MMA(0, 0, At, B0); PG8_MMA(0, 1, At, B1); PG8_BAR; PG8_SCHED;
;             PG8_LDA(At, 0, 1); PG8_STAGE(PG8_SB(0, 0), b2, voffB); PG8_STAGE(PG8_SB(0, 1), b2 + hstepB, voffB); PG8_STAGE(PG8_SA(0, 0), a2, voffA);
;             if (!after_epi) PG8_WAIT_V(8);
;             PG8_WAIT_L(0); PG8_BAR; PG8_MMA(1, 0, At, B0); PG8_MMA(1, 1, At, B1); PG8_BAR; PG8_SCHED;
;             PG8_LDB(B0, 1, 0); PG8_LDB(B1, 1, 1); PG8_SCHED; PG8_LDA(At, 1, 0); PG8_STAGE(PG8_SA(0, 1), a2 + hstepA, voffA);
;             PG8_WAIT_V(8); PG8_WAIT_L(0); PG8_BAR; PG8_MMA(0, 0, At, B0); PG8_MMA(0, 1, At, B1); PG8_BAR; PG8_SCHED;
.LBB0_160:
	s_waitcnt lgkmcnt(0)
	s_barrier
	s_setprio 1
	s_waitcnt lgkmcnt(0)
	v_mfma_i32_16x16x64_i8 v[62:65], v[146:149], v[186:189], v[62:65]
	v_mfma_i32_16x16x64_i8 v[58:61], v[154:157], v[186:189], v[58:61]
	v_mfma_i32_16x16x64_i8 v[46:49], v[146:149], v[178:181], v[46:49]
	v_mfma_i32_16x16x64_i8 v[42:45], v[154:157], v[178:181], v[42:45]
	v_mfma_i32_16x16x64_i8 v[30:33], v[146:149], v[170:173], v[30:33]
	v_mfma_i32_16x16x64_i8 v[26:29], v[154:157], v[170:173], v[26:29]
	v_mfma_i32_16x16x64_i8 v[14:17], v[146:149], v[162:165], v[14:17]
	v_mfma_i32_16x16x64_i8 v[10:13], v[154:157], v[162:165], v[10:13]
	v_mfma_i32_16x16x64_i8 v[62:65], v[150:153], v[190:193], v[62:65]
	v_mfma_i32_16x16x64_i8 v[58:61], v[158:161], v[190:193], v[58:61]
	v_mfma_i32_16x16x64_i8 v[46:49], v[150:153], v[182:185], v[46:49]
	v_mfma_i32_16x16x64_i8 v[42:45], v[158:161], v[182:185], v[42:45]
	v_mfma_i32_16x16x64_i8 v[30:33], v[150:153], v[174:177], v[30:33]
	v_mfma_i32_16x16x64_i8 v[26:29], v[158:161], v[174:177], v[26:29]
	v_mfma_i32_16x16x64_i8 v[14:17], v[150:153], v[166:169], v[14:17]
	v_mfma_i32_16x16x64_i8 v[10:13], v[158:161], v[166:169], v[10:13]
	s_setprio 0
	s_setprio 1
	v_mfma_i32_16x16x64_i8 v[54:57], v[130:133], v[186:189], v[54:57]
	v_mfma_i32_16x16x64_i8 v[50:53], v[138:141], v[186:189], v[50:53]
	v_mfma_i32_16x16x64_i8 v[38:41], v[130:133], v[178:181], v[38:41]
	v_mfma_i32_16x16x64_i8 v[34:37], v[138:141], v[178:181], v[34:37]
	v_mfma_i32_16x16x64_i8 v[22:25], v[130:133], v[170:173], v[22:25]
	v_mfma_i32_16x16x64_i8 v[18:21], v[138:141], v[170:173], v[18:21]
	v_mfma_i32_16x16x64_i8 v[6:9], v[130:133], v[162:165], v[6:9]
	v_mfma_i32_16x16x64_i8 v[2:5], v[138:141], v[162:165], v[2:5]
	v_mfma_i32_16x16x64_i8 v[54:57], v[134:137], v[190:193], v[54:57]
	v_mfma_i32_16x16x64_i8 v[50:53], v[142:145], v[190:193], v[50:53]
	v_mfma_i32_16x16x64_i8 v[38:41], v[134:137], v[182:185], v[38:41]
	v_mfma_i32_16x16x64_i8 v[34:37], v[142:145], v[182:185], v[34:37]
	v_mfma_i32_16x16x64_i8 v[22:25], v[134:137], v[174:177], v[22:25]
	v_mfma_i32_16x16x64_i8 v[18:21], v[142:145], v[174:177], v[18:21]
	v_mfma_i32_16x16x64_i8 v[6:9], v[134:137], v[166:169], v[6:9]
	v_mfma_i32_16x16x64_i8 v[2:5], v[142:145], v[166:169], v[2:5]
	s_setprio 0
	s_barrier
	s_add_i32 s44, 0, 0x18000
	s_add_i32 s45, 0, 0x1c000
	v_add_u32_e32 v142, s44, v195
	v_add_u32_e32 v158, s45, v195
	s_add_u32 s42, s42, 0x80000
	s_addc_u32 s43, s43, 0
	s_mov_b32 m0, s58
	v_lshl_add_u64 v[234:235], s[42:43], 0, v[198:199]
	global_load_lds_dwordx4 v[234:235], off
	v_lshl_add_u64 v[234:235], s[42:43], 0, v[200:201]
	s_mov_b32 m0, s59
	s_nop 0
	global_load_lds_dwordx4 v[234:235], off
	ds_read_b128 v[130:133], v142
	ds_read_b128 v[134:137], v142 offset:1024
	ds_read_b128 v[138:141], v142 offset:2048
	ds_read_b128 v[142:145], v142 offset:3072
	ds_read_b128 v[146:149], v158
	ds_read_b128 v[150:153], v158 offset:1024
	ds_read_b128 v[154:157], v158 offset:2048
	ds_read_b128 v[158:161], v158 offset:3072
	ds_read_b128 v[162:165], v231 offset:32768
	ds_read_b128 v[166:169], v231 offset:33792
	ds_read_b128 v[170:173], v231 offset:34816
	ds_read_b128 v[174:177], v231 offset:35840
	ds_read_b128 v[178:181], v231 offset:36864
	ds_read_b128 v[182:185], v231 offset:37888
	ds_read_b128 v[186:189], v231 offset:38912
	ds_read_b128 v[190:193], v231 offset:39936
	s_waitcnt vmcnt(8)
	s_waitcnt lgkmcnt(0)
	s_barrier
	s_setprio 1
	s_waitcnt lgkmcnt(0)
	v_mfma_i32_16x16x64_i8 v[126:129], v[130:133], v[162:165], v[126:129]
	v_mfma_i32_16x16x64_i8 v[122:125], v[138:141], v[162:165], v[122:125]
	v_mfma_i32_16x16x64_i8 v[110:113], v[130:133], v[170:173], v[110:113]
	v_mfma_i32_16x16x64_i8 v[106:109], v[138:141], v[170:173], v[106:109]
	v_mfma_i32_16x16x64_i8 v[94:97], v[130:133], v[178:181], v[94:97]
	v_mfma_i32_16x16x64_i8 v[90:93], v[138:141], v[178:181], v[90:93]
	v_mfma_i32_16x16x64_i8 v[78:81], v[130:133], v[186:189], v[78:81]
	v_mfma_i32_16x16x64_i8 v[74:77], v[138:141], v[186:189], v[74:77]
	v_mfma_i32_16x16x64_i8 v[126:129], v[134:137], v[166:169], v[126:129]
	v_mfma_i32_16x16x64_i8 v[122:125], v[142:145], v[166:169], v[122:125]
	v_mfma_i32_16x16x64_i8 v[110:113], v[134:137], v[174:177], v[110:113]
	v_mfma_i32_16x16x64_i8 v[106:109], v[142:145], v[174:177], v[106:109]
	v_mfma_i32_16x16x64_i8 v[94:97], v[134:137], v[182:185], v[94:97]
	v_mfma_i32_16x16x64_i8 v[90:93], v[142:145], v[182:185], v[90:93]
	v_mfma_i32_16x16x64_i8 v[78:81], v[134:137], v[190:193], v[78:81]
	v_mfma_i32_16x16x64_i8 v[74:77], v[142:145], v[190:193], v[74:77]
	s_setprio 0
	s_setprio 1
	v_mfma_i32_16x16x64_i8 v[118:121], v[146:149], v[162:165], v[118:121]
	v_mfma_i32_16x16x64_i8 v[114:117], v[154:157], v[162:165], v[114:117]
	v_mfma_i32_16x16x64_i8 v[102:105], v[146:149], v[170:173], v[102:105]
	v_mfma_i32_16x16x64_i8 v[98:101], v[154:157], v[170:173], v[98:101]
	v_mfma_i32_16x16x64_i8 v[86:89], v[146:149], v[178:181], v[86:89]
	v_mfma_i32_16x16x64_i8 v[82:85], v[154:157], v[178:181], v[82:85]
	v_mfma_i32_16x16x64_i8 v[70:73], v[146:149], v[186:189], v[70:73]
	v_mfma_i32_16x16x64_i8 v[66:69], v[154:157], v[186:189], v[66:69]
	v_mfma_i32_16x16x64_i8 v[118:121], v[150:153], v[166:169], v[118:121]
	v_mfma_i32_16x16x64_i8 v[114:117], v[158:161], v[166:169], v[114:117]
	v_mfma_i32_16x16x64_i8 v[102:105], v[150:153], v[174:177], v[102:105]
	v_mfma_i32_16x16x64_i8 v[98:101], v[158:161], v[174:177], v[98:101]
	v_mfma_i32_16x16x64_i8 v[86:89], v[150:153], v[182:185], v[86:89]
	v_mfma_i32_16x16x64_i8 v[82:85], v[158:161], v[182:185], v[82:85]
	v_mfma_i32_16x16x64_i8 v[70:73], v[150:153], v[190:193], v[70:73]
	v_mfma_i32_16x16x64_i8 v[66:69], v[158:161], v[190:193], v[66:69]
	s_setprio 0
	s_barrier
; #define PG8_STAGE(bufoff, gbase, voff) do { _Pragma("unroll") for (int _i = 0; _i < 2; ++_i) \
;         __builtin_amdgcn_global_load_lds((const unsigned*)((const char*)(gbase) + (voff)[_i]), (LAS unsigned*)(lds + (bufoff) + ldsw + _i * 8192), 16, 0, 0); } while (0)
; #define PG8_LDA(dst, b, h) do { _Pragma("unroll") for (int m = 0; m < 4; ++m) _Pragma("unroll") for (int k = 0; k < 2; ++k) dst[m][k] = *(const LAS bf16x8*)(lds + PG8_SA(b, h) + aoff + m * 2048 + k * 1024); } while (0)
; #define PG8_LDB(dst, b, h) do { _Pragma("unroll") for (int n = 0; n < 2; ++n) _Pragma("unroll") for (int k = 0; k < 2; ++k) dst[n][k] = *(const LAS bf16x8*)(lds + PG8_SB(b, h) + boff + n * 2048 + k * 1024); } while (0)
; #define PG8_WAIT_V(n) asm volatile("s_waitcnt vmcnt(" #n ")" ::: "memory")
; #define PG8_WAIT_L(n) asm volatile("s_waitcnt lgkmcnt(" #n ")" ::: "memory")
; #define PG8_BAR __builtin_amdgcn_s_barrier()
; #define PG8_SCHED __builtin_amdgcn_sched_barrier(0)
; template <class Epi, class Sched, bool ALIGN_EPI = true, bool SP2 = true, class Side = NoSide>
; __device__ __forceinline__ void gemm_phase(LAS unsigned char* lds, const Gemm g, const Sched& S, const Epi& E, const Side side = Side()) {
;     ...
;             PG8_LDB(B0, 0, 0); PG8_LDB(B1, 0, 1); PG8_SCHED; PG8_LDA(At, 0, 0); PG8_STAGE(PG8_SA(1, 1), a1 + hstepA, voffA);
;             if (!after_epi) PG8_WAIT_V(8);
;             PG8_WAIT_L(0); PG8_BAR; PG8_MMA(0, 0, At, B0); PG8_MMA(0, 1, At, B1); PG8_BAR; PG8_SCHED;
;             PG8_LDA(At, 0, 1); PG8_STAGE(PG8_SB(0, 0), b2, voffB); PG8_STAGE(PG8_SB(0, 1), b2 + hstepB, voffB); PG8_STAGE(PG8_SA(0, 0), a2, voffA);
;             if (!after_epi) PG8_WAIT_V(8);
;             PG8_WAIT_L(0); PG8_BAR; PG8_MMA(1, 0, At, B0); PG8_MMA(1, 1, At, B1); PG8_BAR; PG8_SCHED;
;             PG8_LDB(B0, 1, 0); PG8_LDB(B1, 1, 1); PG8_SCHED; PG8_LDA(At, 1, 0); PG8_STAGE(PG8_SA(0, 1), a2 + hstepA, voffA);
;             PG8_WAIT_V(8); PG8_WAIT_L(0); PG8_BAR; PG8_MMA(0, 0, At, B0); PG8_MMA(0, 1, At, B1); PG8_BAR; PG8_SCHED;
;             PG8_LDA(At, 1, 1); PG8_STAGE(PG8_SB(1, 0), b3, voffB); PG8_STAGE(PG8_SB(1, 1), b3 + hstepB, voffB); PG8_STAGE(PG8_SA(1, 0), a3, voffA);
;             PG8_WAIT_V(8); PG8_WAIT_L(0); PG8_BAR; PG8_MMA(1, 0, At, B0); PG8_MMA(1, 1, At, B1); PG8_BAR; PG8_SCHED;
	s_add_i32 s42, s44, s51
	v_lshl_add_u64 v[226:227], v[226:227], 0, s[18:19]
	s_mov_b32 m0, s42
	s_nop 0
	global_load_lds_dwordx4 v[226:227], off
	s_add_i32 m0, s42, 0x2000
	s_add_u32 s40, s40, 0x80080
	v_lshl_add_u64 v[224:225], v[224:225], 0, s[18:19]
	s_addc_u32 s41, s41, 0
	s_add_i32 s42, s45, s51
	global_load_lds_dwordx4 v[224:225], off
	v_lshl_add_u64 v[224:225], s[40:41], 0, v[196:197]
	s_mov_b32 m0, s42
	v_lshl_add_u64 v[220:221], v[220:221], 0, s[18:19]
	global_load_lds_dwordx4 v[224:225], off
	v_lshl_add_u64 v[224:225], s[40:41], 0, v[202:203]
	s_add_i32 m0, s42, 0x2000
	s_nop 0
	global_load_lds_dwordx4 v[224:225], off
	s_mov_b32 m0, s64
	s_nop 0
	global_load_lds_dwordx4 v[220:221], off
	v_lshl_add_u64 v[220:221], v[222:223], 0, s[18:19]
	s_mov_b32 m0, s65
	s_nop 0
	global_load_lds_dwordx4 v[220:221], off
	ds_read_b128 v[162:165], v231 offset:49152
	ds_read_b128 v[166:169], v231 offset:50176
	ds_read_b128 v[170:173], v231 offset:51200
	ds_read_b128 v[174:177], v231 offset:52224
	ds_read_b128 v[178:181], v231 offset:53248
	ds_read_b128 v[182:185], v231 offset:54272
	ds_read_b128 v[186:189], v231 offset:55296
	ds_read_b128 v[190:193], v231 offset:56320
	s_waitcnt vmcnt(8)
	s_waitcnt lgkmcnt(0)
	s_barrier
	s_setprio 1
	s_waitcnt lgkmcnt(0)
	v_mfma_i32_16x16x64_i8 v[62:65], v[130:133], v[162:165], v[62:65]
	v_mfma_i32_16x16x64_i8 v[58:61], v[138:141], v[162:165], v[58:61]
	v_mfma_i32_16x16x64_i8 v[46:49], v[130:133], v[170:173], v[46:49]
	v_mfma_i32_16x16x64_i8 v[42:45], v[138:141], v[170:173], v[42:45]
	v_mfma_i32_16x16x64_i8 v[30:33], v[130:133], v[178:181], v[30:33]
	v_mfma_i32_16x16x64_i8 v[26:29], v[138:141], v[178:181], v[26:29]
	v_mfma_i32_16x16x64_i8 v[14:17], v[130:133], v[186:189], v[14:17]
	v_mfma_i32_16x16x64_i8 v[10:13], v[138:141], v[186:189], v[10:13]
	v_mfma_i32_16x16x64_i8 v[62:65], v[134:137], v[166:169], v[62:65]
	v_mfma_i32_16x16x64_i8 v[58:61], v[142:145], v[166:169], v[58:61]
	v_mfma_i32_16x16x64_i8 v[46:49], v[134:137], v[174:177], v[46:49]
	v_mfma_i32_16x16x64_i8 v[42:45], v[142:145], v[174:177], v[42:45]
	v_mfma_i32_16x16x64_i8 v[30:33], v[134:137], v[182:185], v[30:33]
	v_mfma_i32_16x16x64_i8 v[26:29], v[142:145], v[182:185], v[26:29]
	v_mfma_i32_16x16x64_i8 v[14:17], v[134:137], v[190:193], v[14:17]
	v_mfma_i32_16x16x64_i8 v[10:13], v[142:145], v[190:193], v[10:13]
	s_setprio 0
	s_setprio 1
	v_mfma_i32_16x16x64_i8 v[54:57], v[146:149], v[162:165], v[54:57]
	v_mfma_i32_16x16x64_i8 v[50:53], v[154:157], v[162:165], v[50:53]
	v_mfma_i32_16x16x64_i8 v[38:41], v[146:149], v[170:173], v[38:41]
	v_mfma_i32_16x16x64_i8 v[34:37], v[154:157], v[170:173], v[34:37]
	v_mfma_i32_16x16x64_i8 v[22:25], v[146:149], v[178:181], v[22:25]
	v_mfma_i32_16x16x64_i8 v[18:21], v[154:157], v[178:181], v[18:21]
	v_mfma_i32_16x16x64_i8 v[6:9], v[146:149], v[186:189], v[6:9]
	v_mfma_i32_16x16x64_i8 v[2:5], v[154:157], v[186:189], v[2:5]
	v_mfma_i32_16x16x64_i8 v[54:57], v[150:153], v[166:169], v[54:57]
	v_mfma_i32_16x16x64_i8 v[50:53], v[158:161], v[166:169], v[50:53]
	v_mfma_i32_16x16x64_i8 v[38:41], v[150:153], v[174:177], v[38:41]
	v_mfma_i32_16x16x64_i8 v[34:37], v[158:161], v[174:177], v[34:37]
	v_mfma_i32_16x16x64_i8 v[22:25], v[150:153], v[182:185], v[22:25]
	v_mfma_i32_16x16x64_i8 v[18:21], v[158:161], v[182:185], v[18:21]
	v_mfma_i32_16x16x64_i8 v[6:9], v[150:153], v[190:193], v[6:9]
	v_mfma_i32_16x16x64_i8 v[2:5], v[158:161], v[190:193], v[2:5]
	s_setprio 0
	s_barrier
	s_add_i32 s80, s80, 2
	s_add_u32 s38, s38, 0x100
	s_addc_u32 s39, s39, 0
	s_cmp_gt_u32 s80, 29
	s_cbranch_scc1 .LBB0_165
.LBB0_161:
	s_cmp_eq_u32 s38, 0
	s_cselect_b64 s[40:41], -1, 0
	v_lshl_add_u64 v[220:221], v[216:217], 0, s[38:39]
	s_add_i32 m0, s52, 0xc000
	s_nop 0
	global_load_lds_dwordx4 v[220:221], off
	v_lshl_add_u64 v[220:221], v[218:219], 0, s[38:39]
	s_add_i32 m0, s52, 0xe000
	s_and_b64 s[40:41], s[36:37], s[40:41]
	global_load_lds_dwordx4 v[220:221], off
	ds_read_b128 v[146:149], v229
	ds_read_b128 v[150:153], v229 offset:1024
	ds_read_b128 v[154:157], v229 offset:2048
	ds_read_b128 v[158:161], v229 offset:3072
	ds_read_b128 v[130:133], v230
	ds_read_b128 v[134:137], v230 offset:1024
	ds_read_b128 v[138:141], v230 offset:2048
	ds_read_b128 v[142:145], v230 offset:3072
	ds_read_b128 v[186:189], v231
	ds_read_b128 v[190:193], v231 offset:1024
	ds_read_b128 v[178:181], v231 offset:2048
	ds_read_b128 v[182:185], v231 offset:3072
	ds_read_b128 v[170:173], v231 offset:4096
	ds_read_b128 v[174:177], v231 offset:5120
	ds_read_b128 v[162:165], v231 offset:6144
	ds_read_b128 v[166:169], v231 offset:7168
	s_and_b64 vcc, exec, s[40:41]
	s_cbranch_vccnz .LBB0_163
	s_waitcnt vmcnt(8)
;     __device__ __forceinline__ size_t a_off(const Unit& u, const Gemm& g) const { size_t o = (size_t)u.pm * BM * g.lda * 2; if (MODE == 1) o += (size_t)(u.pn >> 1) * 512 * 2; return o; }
;     __device__ __forceinline__ size_t b_off(const Unit& u, const Gemm& g) const { return (size_t)u.pn * BM * g.ldb * 2; }
; #define PG8_STAGE(bufoff, gbase, voff) do { _Pragma("unroll") for (int _i = 0; _i < 2; ++_i) \
;         __builtin_amdgcn_global_load_lds((const unsigned*)((const char*)(gbase) + (voff)[_i]), (LAS unsigned*)(lds + (bufoff) + ldsw + _i * 8192), 16, 0, 0); } while (0)
; #define PG8_LDA(dst, b, h) do { _Pragma("unroll") for (int m = 0; m < 4; ++m) _Pragma("unroll") for (int k = 0; k < 2; ++k) dst[m][k] = *(const LAS bf16x8*)(lds + PG8_SA(b, h) + aoff + m * 2048 + k * 1024); } while (0)
; #define PG8_WAIT_V(n) asm volatile("s_waitcnt vmcnt(" #n ")" ::: "memory")
; template <class Epi, class Sched, bool ALIGN_EPI = true, bool SP2 = true, class Side = NoSide>
; __device__ __forceinline__ void gemm_phase(LAS unsigned char* lds, const Gemm g, const Sched& S, const Epi& E, const Side side = Side()) {
;     ...
;         const bool has_next = S.next(ui + 1, nxt);
;         const char* nA = has_next ? (const char*)g.A + S.a_off(nxt, g) : cA; const char* nB = has_next ? (const char*)g.Bt + S.b_off(nxt, g) : cB;
; #pragma unroll 1
;         for (int t = 0; t < nt; t += 2) {
;             const bool last = (t == nt - 2);
;             const char* a1 = cA + (size_t)(t + 1) * kstep;
;             const char* a2 = last ? nA : cA + (size_t)(t + 2) * kstep; const char* b2 = last ? nB : cB + (size_t)(t + 2) * kstep;
;             const char* a3 = a2 + kstep; const char* b3 = b2 + kstep;
;             const bool after_epi = Epi::LOADS && t == 0 && ui > 0;
;             if constexpr (SP2) {
;             PG8_LDB(B0, 0, 0); PG8_LDB(B1, 0, 1); PG8_SCHED; PG8_LDA(At, 0, 0); PG8_STAGE(PG8_SA(1, 1), a1 + hstepA, voffA);
;             if (!after_epi) PG8_WAIT_V(8);
;             PG8_WAIT_L(0); PG8_BAR; PG8_MMA(0, 0, At, B0); PG8_MMA(0, 1, At, B1); PG8_BAR; PG8_SCHED;
;             PG8_LDA(At, 0, 1); PG8_STAGE(PG8_SB(0, 0), b2, voffB); PG8_STAGE(PG8_SB(0, 1), b2 + hstepB, voffB); PG8_STAGE(PG8_SA(0, 0), a2, voffA);
;             if (!after_epi) PG8_WAIT_V(8);
;             PG8_WAIT_L(0); PG8_BAR; PG8_MMA(1, 0, At, B0); PG8_MMA(1, 1, At, B1); PG8_BAR; PG8_SCHED;
.LBB0_163:
	s_xor_b64 s[44:45], s[40:41], -1
	s_add_u32 s40, s34, s38
	s_addc_u32 s41, s35, s39
	s_add_u32 s40, s40, 0x100
	s_addc_u32 s41, s41, 0
	s_add_u32 s81, s78, s38
	s_addc_u32 s82, s79, s39
	s_waitcnt lgkmcnt(0)
	s_cmpk_eq_i32 s38, 0xf00
	s_cselect_b32 s43, s11, s41
	s_cselect_b32 s42, s25, s40
	s_cselect_b32 s41, s23, s82
	s_cselect_b32 s40, s77, s81
	s_barrier
	s_setprio 1
	s_waitcnt lgkmcnt(0)
	v_mfma_i32_16x16x64_i8 v[126:129], v[146:149], v[186:189], v[126:129]
	v_mfma_i32_16x16x64_i8 v[122:125], v[154:157], v[186:189], v[122:125]
	v_mfma_i32_16x16x64_i8 v[110:113], v[146:149], v[178:181], v[110:113]
	v_mfma_i32_16x16x64_i8 v[106:109], v[154:157], v[178:181], v[106:109]
	v_mfma_i32_16x16x64_i8 v[94:97], v[146:149], v[170:173], v[94:97]
	v_mfma_i32_16x16x64_i8 v[90:93], v[154:157], v[170:173], v[90:93]
	v_mfma_i32_16x16x64_i8 v[78:81], v[146:149], v[162:165], v[78:81]
	v_mfma_i32_16x16x64_i8 v[74:77], v[154:157], v[162:165], v[74:77]
	v_mfma_i32_16x16x64_i8 v[126:129], v[150:153], v[190:193], v[126:129]
	v_mfma_i32_16x16x64_i8 v[122:125], v[158:161], v[190:193], v[122:125]
	v_mfma_i32_16x16x64_i8 v[110:113], v[150:153], v[182:185], v[110:113]
	v_mfma_i32_16x16x64_i8 v[106:109], v[158:161], v[182:185], v[106:109]
	v_mfma_i32_16x16x64_i8 v[94:97], v[150:153], v[174:177], v[94:97]
	v_mfma_i32_16x16x64_i8 v[90:93], v[158:161], v[174:177], v[90:93]
	v_mfma_i32_16x16x64_i8 v[78:81], v[150:153], v[166:169], v[78:81]
	v_mfma_i32_16x16x64_i8 v[74:77], v[158:161], v[166:169], v[74:77]
	s_setprio 0
	s_setprio 1
	v_mfma_i32_16x16x64_i8 v[118:121], v[130:133], v[186:189], v[118:121]
	v_mfma_i32_16x16x64_i8 v[114:117], v[138:141], v[186:189], v[114:117]
	v_mfma_i32_16x16x64_i8 v[102:105], v[130:133], v[178:181], v[102:105]
	v_mfma_i32_16x16x64_i8 v[98:101], v[138:141], v[178:181], v[98:101]
	v_mfma_i32_16x16x64_i8 v[86:89], v[130:133], v[170:173], v[86:89]
	v_mfma_i32_16x16x64_i8 v[82:85], v[138:141], v[170:173], v[82:85]
	v_mfma_i32_16x16x64_i8 v[70:73], v[130:133], v[162:165], v[70:73]
	v_mfma_i32_16x16x64_i8 v[66:69], v[138:141], v[162:165], v[66:69]
	v_mfma_i32_16x16x64_i8 v[118:121], v[134:137], v[190:193], v[118:121]
	v_mfma_i32_16x16x64_i8 v[114:117], v[142:145], v[190:193], v[114:117]
	v_mfma_i32_16x16x64_i8 v[102:105], v[134:137], v[182:185], v[102:105]
	v_mfma_i32_16x16x64_i8 v[98:101], v[142:145], v[182:185], v[98:101]
	v_mfma_i32_16x16x64_i8 v[86:89], v[134:137], v[174:177], v[86:89]
	v_mfma_i32_16x16x64_i8 v[82:85], v[142:145], v[174:177], v[82:85]
	v_mfma_i32_16x16x64_i8 v[70:73], v[134:137], v[166:169], v[70:73]
	v_mfma_i32_16x16x64_i8 v[66:69], v[142:145], v[166:169], v[66:69]
	s_setprio 0
	s_barrier
	s_mov_b32 m0, s53
	v_lshl_add_u64 v[226:227], s[40:41], 0, v[196:197]
	s_add_u32 s82, s40, 0x80000
	global_load_lds_dwordx4 v[226:227], off
	v_lshl_add_u64 v[224:225], s[40:41], 0, v[202:203]
	s_mov_b32 m0, s54
	s_addc_u32 s83, s41, 0
	global_load_lds_dwordx4 v[224:225], off
	v_lshl_add_u64 v[220:221], s[82:83], 0, v[196:197]
	s_mov_b32 m0, s55
	v_lshl_add_u64 v[222:223], s[42:43], 0, v[200:201]
	global_load_lds_dwordx4 v[220:221], off
	v_lshl_add_u64 v[220:221], s[82:83], 0, v[202:203]
	s_mov_b32 m0, s56
	s_andn2_b64 vcc, exec, s[44:45]
	global_load_lds_dwordx4 v[220:221], off
	v_lshl_add_u64 v[220:221], s[42:43], 0, v[198:199]
	s_mov_b32 m0, s52
	s_nop 0
	global_load_lds_dwordx4 v[220:221], off
	s_mov_b32 m0, s57
	s_nop 0
	global_load_lds_dwordx4 v[222:223], off
	ds_read_b128 v[186:189], v231 offset:16384
	ds_read_b128 v[190:193], v231 offset:17408
	ds_read_b128 v[178:181], v231 offset:18432
	ds_read_b128 v[182:185], v231 offset:19456
	ds_read_b128 v[170:173], v231 offset:20480
	ds_read_b128 v[174:177], v231 offset:21504
	ds_read_b128 v[162:165], v231 offset:22528
	ds_read_b128 v[166:169], v231 offset:23552
	s_cbranch_vccnz .LBB0_160
	s_waitcnt vmcnt(8)
	s_branch .LBB0_160

; #define PG8_STAGE(bufoff, gbase, voff) do { _Pragma("unroll") for (int _i = 0; _i < 2; ++_i) \
;         __builtin_amdgcn_global_load_lds((const unsigned*)((const char*)(gbase) + (voff)[_i]), (LAS unsigned*)(lds + (bufoff) + ldsw + _i * 8192), 16, 0, 0); } while (0)
; #define PG8_LDA(dst, b, h) do { _Pragma("unroll") for (int m = 0; m < 4; ++m) _Pragma("unroll") for (int k = 0; k < 2; ++k) dst[m][k] = *(const LAS bf16x8*)(lds + PG8_SA(b, h) + aoff + m * 2048 + k * 1024); } while (0)
; #define PG8_LDB(dst, b, h) do { _Pragma("unroll") for (int n = 0; n < 2; ++n) _Pragma("unroll") for (int k = 0; k < 2; ++k) dst[n][k] = *(const LAS bf16x8*)(lds + PG8_SB(b, h) + boff + n * 2048 + k * 1024); } while (0)
; #define PG8_WAIT_V(n) asm volatile("s_waitcnt vmcnt(" #n ")" ::: "memory")
; #define PG8_WAIT_L(n) asm volatile("s_waitcnt lgkmcnt(" #n ")" ::: "memory")
; #define PG8_BAR __builtin_amdgcn_s_barrier()
; #define PG8_SCHED __builtin_amdgcn_sched_barrier(0)
; template <class Epi, class Sched, bool ALIGN_EPI = true, bool SP2 = true, class Side = NoSide>
; __device__ __forceinline__ void gemm_phase(LAS unsigned char* lds, const Gemm g, const Sched& S, const Epi& E, const Side side = Side()) {
;     ...
;             PG8_WAIT_L(0); PG8_BAR; PG8_MMA(0, 0, At, B0); PG8_MMA(0, 1, At, B1); PG8_BAR; PG8_SCHED;
;             PG8_LDA(At, 0, 1); PG8_STAGE(PG8_SB(0, 0), b2, voffB); PG8_STAGE(PG8_SB(0, 1), b2 + hstepB, voffB); PG8_STAGE(PG8_SA(0, 0), a2, voffA);
;             if (!after_epi) PG8_WAIT_V(8);
;             PG8_WAIT_L(0); PG8_BAR; PG8_MMA(1, 0, At, B0); PG8_MMA(1, 1, At, B1); PG8_BAR; PG8_SCHED;
;             PG8_LDB(B0, 1, 0); PG8_LDB(B1, 1, 1); PG8_SCHED; PG8_LDA(At, 1, 0); PG8_STAGE(PG8_SA(0, 1), a2 + hstepA, voffA);
;             PG8_WAIT_V(8); PG8_WAIT_L(0); PG8_BAR; PG8_MMA(0, 0, At, B0); PG8_MMA(0, 1, At, B1); PG8_BAR; PG8_SCHED;
.LBB0_306:
	s_waitcnt lgkmcnt(0)
	s_barrier
	s_setprio 1
	s_waitcnt lgkmcnt(0)
	v_mfma_f32_16x16x32_bf16 v[62:65], v[146:149], v[186:189], v[62:65]
	v_mfma_f32_16x16x32_bf16 v[58:61], v[154:157], v[186:189], v[58:61]
	v_mfma_f32_16x16x32_bf16 v[50:53], v[146:149], v[178:181], v[50:53]
	v_mfma_f32_16x16x32_bf16 v[42:45], v[154:157], v[178:181], v[42:45]
	v_mfma_f32_16x16x32_bf16 v[34:37], v[146:149], v[170:173], v[34:37]
	v_mfma_f32_16x16x32_bf16 v[26:29], v[154:157], v[170:173], v[26:29]
	v_mfma_f32_16x16x32_bf16 v[18:21], v[146:149], v[162:165], v[18:21]
	v_mfma_f32_16x16x32_bf16 v[10:13], v[154:157], v[162:165], v[10:13]
	v_mfma_f32_16x16x32_bf16 v[62:65], v[150:153], v[190:193], v[62:65]
	v_mfma_f32_16x16x32_bf16 v[58:61], v[158:161], v[190:193], v[58:61]
	v_mfma_f32_16x16x32_bf16 v[50:53], v[150:153], v[182:185], v[50:53]
	v_mfma_f32_16x16x32_bf16 v[42:45], v[158:161], v[182:185], v[42:45]
	v_mfma_f32_16x16x32_bf16 v[34:37], v[150:153], v[174:177], v[34:37]
	v_mfma_f32_16x16x32_bf16 v[26:29], v[158:161], v[174:177], v[26:29]
	v_mfma_f32_16x16x32_bf16 v[18:21], v[150:153], v[166:169], v[18:21]
	v_mfma_f32_16x16x32_bf16 v[10:13], v[158:161], v[166:169], v[10:13]
	s_setprio 0
	s_setprio 1
	v_mfma_f32_16x16x32_bf16 v[54:57], v[130:133], v[186:189], v[54:57]
	v_mfma_f32_16x16x32_bf16 v[46:49], v[138:141], v[186:189], v[46:49]
	v_mfma_f32_16x16x32_bf16 v[38:41], v[130:133], v[178:181], v[38:41]
	v_mfma_f32_16x16x32_bf16 v[30:33], v[138:141], v[178:181], v[30:33]
	v_mfma_f32_16x16x32_bf16 v[22:25], v[130:133], v[170:173], v[22:25]
	v_mfma_f32_16x16x32_bf16 v[14:17], v[138:141], v[170:173], v[14:17]
	v_mfma_f32_16x16x32_bf16 v[6:9], v[130:133], v[162:165], v[6:9]
	v_mfma_f32_16x16x32_bf16 v[2:5], v[138:141], v[162:165], v[2:5]
	v_mfma_f32_16x16x32_bf16 v[54:57], v[134:137], v[190:193], v[54:57]
	v_mfma_f32_16x16x32_bf16 v[46:49], v[142:145], v[190:193], v[46:49]
	v_mfma_f32_16x16x32_bf16 v[38:41], v[134:137], v[182:185], v[38:41]
	v_mfma_f32_16x16x32_bf16 v[30:33], v[142:145], v[182:185], v[30:33]
	v_mfma_f32_16x16x32_bf16 v[22:25], v[134:137], v[174:177], v[22:25]
	v_mfma_f32_16x16x32_bf16 v[14:17], v[142:145], v[174:177], v[14:17]
	v_mfma_f32_16x16x32_bf16 v[6:9], v[134:137], v[166:169], v[6:9]
	v_mfma_f32_16x16x32_bf16 v[2:5], v[142:145], v[166:169], v[2:5]
	s_setprio 0
	s_barrier
	s_add_i32 s30, 0, 0x18000
	s_add_i32 s31, 0, 0x1c000
	v_add_u32_e32 v142, s30, v233
	v_add_u32_e32 v158, s31, v233
	s_add_u32 s28, s28, 0x3d0000
	s_addc_u32 s29, s29, 0
	s_mov_b32 m0, s44
	v_lshl_add_u64 v[238:239], s[28:29], 0, v[196:197]
	global_load_lds_dwordx4 v[238:239], off
	v_lshl_add_u64 v[238:239], s[28:29], 0, v[200:201]
	s_mov_b32 m0, s45
	s_nop 0
	global_load_lds_dwordx4 v[238:239], off
	ds_read_b128 v[130:133], v142
	ds_read_b128 v[134:137], v142 offset:1024
	ds_read_b128 v[138:141], v142 offset:2048
	ds_read_b128 v[142:145], v142 offset:3072
	ds_read_b128 v[146:149], v158
	ds_read_b128 v[150:153], v158 offset:1024
	ds_read_b128 v[154:157], v158 offset:2048
	ds_read_b128 v[158:161], v158 offset:3072
	ds_read_b128 v[162:165], v237 offset:32768
	ds_read_b128 v[166:169], v237 offset:33792
	ds_read_b128 v[170:173], v237 offset:34816
	ds_read_b128 v[174:177], v237 offset:35840
	ds_read_b128 v[178:181], v237 offset:36864
	ds_read_b128 v[182:185], v237 offset:37888
	ds_read_b128 v[186:189], v237 offset:38912
	ds_read_b128 v[190:193], v237 offset:39936
	s_waitcnt vmcnt(8)
	s_waitcnt lgkmcnt(0)
	s_barrier
	s_setprio 1
	s_waitcnt lgkmcnt(0)
	v_mfma_f32_16x16x32_bf16 v[126:129], v[130:133], v[162:165], v[126:129]
	v_mfma_f32_16x16x32_bf16 v[122:125], v[138:141], v[162:165], v[122:125]
	v_mfma_f32_16x16x32_bf16 v[118:121], v[130:133], v[170:173], v[118:121]
	v_mfma_f32_16x16x32_bf16 v[114:117], v[138:141], v[170:173], v[114:117]
	v_mfma_f32_16x16x32_bf16 v[110:113], v[130:133], v[178:181], v[110:113]
	v_mfma_f32_16x16x32_bf16 v[102:105], v[138:141], v[178:181], v[102:105]
	v_mfma_f32_16x16x32_bf16 v[94:97], v[130:133], v[186:189], v[94:97]
	v_mfma_f32_16x16x32_bf16 v[86:89], v[138:141], v[186:189], v[86:89]
	v_mfma_f32_16x16x32_bf16 v[126:129], v[134:137], v[166:169], v[126:129]
	v_mfma_f32_16x16x32_bf16 v[122:125], v[142:145], v[166:169], v[122:125]
	v_mfma_f32_16x16x32_bf16 v[118:121], v[134:137], v[174:177], v[118:121]
	v_mfma_f32_16x16x32_bf16 v[114:117], v[142:145], v[174:177], v[114:117]
	v_mfma_f32_16x16x32_bf16 v[110:113], v[134:137], v[182:185], v[110:113]
	v_mfma_f32_16x16x32_bf16 v[102:105], v[142:145], v[182:185], v[102:105]
	v_mfma_f32_16x16x32_bf16 v[94:97], v[134:137], v[190:193], v[94:97]
	v_mfma_f32_16x16x32_bf16 v[86:89], v[142:145], v[190:193], v[86:89]
	s_setprio 0
	s_setprio 1
	v_mfma_f32_16x16x32_bf16 v[106:109], v[146:149], v[162:165], v[106:109]
	v_mfma_f32_16x16x32_bf16 v[98:101], v[154:157], v[162:165], v[98:101]
	v_mfma_f32_16x16x32_bf16 v[90:93], v[146:149], v[170:173], v[90:93]
	v_mfma_f32_16x16x32_bf16 v[82:85], v[154:157], v[170:173], v[82:85]
	v_mfma_f32_16x16x32_bf16 v[78:81], v[146:149], v[178:181], v[78:81]
	v_mfma_f32_16x16x32_bf16 v[74:77], v[154:157], v[178:181], v[74:77]
	v_mfma_f32_16x16x32_bf16 v[70:73], v[146:149], v[186:189], v[70:73]
	v_mfma_f32_16x16x32_bf16 v[66:69], v[154:157], v[186:189], v[66:69]
	v_mfma_f32_16x16x32_bf16 v[106:109], v[150:153], v[166:169], v[106:109]
	v_mfma_f32_16x16x32_bf16 v[98:101], v[158:161], v[166:169], v[98:101]
	v_mfma_f32_16x16x32_bf16 v[90:93], v[150:153], v[174:177], v[90:93]
	v_mfma_f32_16x16x32_bf16 v[82:85], v[158:161], v[174:177], v[82:85]
	v_mfma_f32_16x16x32_bf16 v[78:81], v[150:153], v[182:185], v[78:81]
	v_mfma_f32_16x16x32_bf16 v[74:77], v[158:161], v[182:185], v[74:77]
	v_mfma_f32_16x16x32_bf16 v[70:73], v[150:153], v[190:193], v[70:73]
	v_mfma_f32_16x16x32_bf16 v[66:69], v[158:161], v[190:193], v[66:69]
	s_setprio 0
	s_barrier
; #define PG8_STAGE(bufoff, gbase, voff) do { _Pragma("unroll") for (int _i = 0; _i < 2; ++_i) \
;         __builtin_amdgcn_global_load_lds((const unsigned*)((const char*)(gbase) + (voff)[_i]), (LAS unsigned*)(lds + (bufoff) + ldsw + _i * 8192), 16, 0, 0); } while (0)
; #define PG8_LDA(dst, b, h) do { _Pragma("unroll") for (int m = 0; m < 4; ++m) _Pragma("unroll") for (int k = 0; k < 2; ++k) dst[m][k] = *(const LAS bf16x8*)(lds + PG8_SA(b, h) + aoff + m * 2048 + k * 1024); } while (0)
; #define PG8_LDB(dst, b, h) do { _Pragma("unroll") for (int n = 0; n < 2; ++n) _Pragma("unroll") for (int k = 0; k < 2; ++k) dst[n][k] = *(const LAS bf16x8*)(lds + PG8_SB(b, h) + boff + n * 2048 + k * 1024); } while (0)
; #define PG8_WAIT_V(n) asm volatile("s_waitcnt vmcnt(" #n ")" ::: "memory")
; #define PG8_WAIT_L(n) asm volatile("s_waitcnt lgkmcnt(" #n ")" ::: "memory")
; #define PG8_BAR __builtin_amdgcn_s_barrier()
; #define PG8_SCHED __builtin_amdgcn_sched_barrier(0)
; template <class Epi, class Sched, bool ALIGN_EPI = true, bool SP2 = true, class Side = NoSide>
; __device__ __forceinline__ void gemm_phase(LAS unsigned char* lds, const Gemm g, const Sched& S, const Epi& E, const Side side = Side()) {
;     ...
;             PG8_LDB(B0, 0, 0); PG8_LDB(B1, 0, 1); PG8_SCHED; PG8_LDA(At, 0, 0); PG8_STAGE(PG8_SA(1, 1), a1 + hstepA, voffA);
;             if (!after_epi) PG8_WAIT_V(8);
;             PG8_WAIT_L(0); PG8_BAR; PG8_MMA(0, 0, At, B0); PG8_MMA(0, 1, At, B1); PG8_BAR; PG8_SCHED;
;             PG8_LDA(At, 0, 1); PG8_STAGE(PG8_SB(0, 0), b2, voffB); PG8_STAGE(PG8_SB(0, 1), b2 + hstepB, voffB); PG8_STAGE(PG8_SA(0, 0), a2, voffA);
;             if (!after_epi) PG8_WAIT_V(8);
;             PG8_WAIT_L(0); PG8_BAR; PG8_MMA(1, 0, At, B0); PG8_MMA(1, 1, At, B1); PG8_BAR; PG8_SCHED;
;             PG8_LDB(B0, 1, 0); PG8_LDB(B1, 1, 1); PG8_SCHED; PG8_LDA(At, 1, 0); PG8_STAGE(PG8_SA(0, 1), a2 + hstepA, voffA);
;             PG8_WAIT_V(8); PG8_WAIT_L(0); PG8_BAR; PG8_MMA(0, 0, At, B0); PG8_MMA(0, 1, At, B1); PG8_BAR; PG8_SCHED;
;             PG8_LDA(At, 1, 1); PG8_STAGE(PG8_SB(1, 0), b3, voffB); PG8_STAGE(PG8_SB(1, 1), b3 + hstepB, voffB); PG8_STAGE(PG8_SA(1, 0), a3, voffA);
;             PG8_WAIT_V(8); PG8_WAIT_L(0); PG8_BAR; PG8_MMA(1, 0, At, B0); PG8_MMA(1, 1, At, B1); PG8_BAR; PG8_SCHED;
	s_add_i32 s28, s30, s34
	v_lshl_add_u64 v[222:223], v[222:223], 0, s[10:11]
	s_mov_b32 m0, s28
	s_nop 0
	global_load_lds_dwordx4 v[222:223], off
	s_add_i32 m0, s28, 0x2000
	s_add_u32 s26, s26, 0x20080
	v_lshl_add_u64 v[220:221], v[220:221], 0, s[10:11]
	s_addc_u32 s27, s27, 0
	s_add_i32 s28, s31, s34
	global_load_lds_dwordx4 v[220:221], off
	v_lshl_add_u64 v[220:221], s[26:27], 0, v[198:199]
	s_mov_b32 m0, s28
	v_lshl_add_u64 v[216:217], v[216:217], 0, s[10:11]
	global_load_lds_dwordx4 v[220:221], off
	v_lshl_add_u64 v[220:221], s[26:27], 0, v[202:203]
	s_add_i32 m0, s28, 0x2000
	s_nop 0
	global_load_lds_dwordx4 v[220:221], off
	s_mov_b32 m0, s46
	s_nop 0
	global_load_lds_dwordx4 v[216:217], off
	v_lshl_add_u64 v[216:217], v[218:219], 0, s[10:11]
	s_mov_b32 m0, s47
	s_nop 0
	global_load_lds_dwordx4 v[216:217], off
	ds_read_b128 v[162:165], v237 offset:49152
	ds_read_b128 v[166:169], v237 offset:50176
	ds_read_b128 v[170:173], v237 offset:51200
	ds_read_b128 v[174:177], v237 offset:52224
	ds_read_b128 v[178:181], v237 offset:53248
	ds_read_b128 v[182:185], v237 offset:54272
	ds_read_b128 v[186:189], v237 offset:55296
	ds_read_b128 v[190:193], v237 offset:56320
	s_waitcnt vmcnt(8)
	s_waitcnt lgkmcnt(0)
	s_barrier
	s_setprio 1
	s_waitcnt lgkmcnt(0)
	v_mfma_f32_16x16x32_bf16 v[62:65], v[130:133], v[162:165], v[62:65]
	v_mfma_f32_16x16x32_bf16 v[58:61], v[138:141], v[162:165], v[58:61]
	v_mfma_f32_16x16x32_bf16 v[50:53], v[130:133], v[170:173], v[50:53]
	v_mfma_f32_16x16x32_bf16 v[42:45], v[138:141], v[170:173], v[42:45]
	v_mfma_f32_16x16x32_bf16 v[34:37], v[130:133], v[178:181], v[34:37]
	v_mfma_f32_16x16x32_bf16 v[26:29], v[138:141], v[178:181], v[26:29]
	v_mfma_f32_16x16x32_bf16 v[18:21], v[130:133], v[186:189], v[18:21]
	v_mfma_f32_16x16x32_bf16 v[10:13], v[138:141], v[186:189], v[10:13]
	v_mfma_f32_16x16x32_bf16 v[62:65], v[134:137], v[166:169], v[62:65]
	v_mfma_f32_16x16x32_bf16 v[58:61], v[142:145], v[166:169], v[58:61]
	v_mfma_f32_16x16x32_bf16 v[50:53], v[134:137], v[174:177], v[50:53]
	v_mfma_f32_16x16x32_bf16 v[42:45], v[142:145], v[174:177], v[42:45]
	v_mfma_f32_16x16x32_bf16 v[34:37], v[134:137], v[182:185], v[34:37]
	v_mfma_f32_16x16x32_bf16 v[26:29], v[142:145], v[182:185], v[26:29]
	v_mfma_f32_16x16x32_bf16 v[18:21], v[134:137], v[190:193], v[18:21]
	v_mfma_f32_16x16x32_bf16 v[10:13], v[142:145], v[190:193], v[10:13]
	s_setprio 0
	s_setprio 1
	v_mfma_f32_16x16x32_bf16 v[54:57], v[146:149], v[162:165], v[54:57]
	v_mfma_f32_16x16x32_bf16 v[46:49], v[154:157], v[162:165], v[46:49]
	v_mfma_f32_16x16x32_bf16 v[38:41], v[146:149], v[170:173], v[38:41]
	v_mfma_f32_16x16x32_bf16 v[30:33], v[154:157], v[170:173], v[30:33]
	v_mfma_f32_16x16x32_bf16 v[22:25], v[146:149], v[178:181], v[22:25]
	v_mfma_f32_16x16x32_bf16 v[14:17], v[154:157], v[178:181], v[14:17]
	v_mfma_f32_16x16x32_bf16 v[6:9], v[146:149], v[186:189], v[6:9]
	v_mfma_f32_16x16x32_bf16 v[2:5], v[154:157], v[186:189], v[2:5]
	v_mfma_f32_16x16x32_bf16 v[54:57], v[150:153], v[166:169], v[54:57]
	v_mfma_f32_16x16x32_bf16 v[46:49], v[158:161], v[166:169], v[46:49]
	v_mfma_f32_16x16x32_bf16 v[38:41], v[150:153], v[174:177], v[38:41]
	v_mfma_f32_16x16x32_bf16 v[30:33], v[158:161], v[174:177], v[30:33]
	v_mfma_f32_16x16x32_bf16 v[22:25], v[150:153], v[182:185], v[22:25]
	v_mfma_f32_16x16x32_bf16 v[14:17], v[158:161], v[182:185], v[14:17]
	v_mfma_f32_16x16x32_bf16 v[6:9], v[150:153], v[190:193], v[6:9]
	v_mfma_f32_16x16x32_bf16 v[2:5], v[158:161], v[190:193], v[2:5]
	s_setprio 0
	s_barrier
	s_add_i32 s56, s56, 2
	s_add_u32 s24, s24, 0x100
	s_addc_u32 s25, s25, 0
	s_cmp_gt_u32 s56, 5
	s_cbranch_scc1 .LBB0_311
.LBB0_307:
	s_cmp_eq_u32 s24, 0
	s_cselect_b64 s[26:27], -1, 0
	v_lshl_add_u64 v[216:217], v[212:213], 0, s[24:25]
	s_add_i32 m0, s38, 0xc000
	s_nop 0
	global_load_lds_dwordx4 v[216:217], off
	v_lshl_add_u64 v[216:217], v[214:215], 0, s[24:25]
	s_add_i32 m0, s38, 0xe000
	s_and_b64 s[26:27], s[8:9], s[26:27]
	global_load_lds_dwordx4 v[216:217], off
	ds_read_b128 v[146:149], v235
	ds_read_b128 v[150:153], v235 offset:1024
	ds_read_b128 v[154:157], v235 offset:2048
	ds_read_b128 v[158:161], v235 offset:3072
	ds_read_b128 v[130:133], v236
	ds_read_b128 v[134:137], v236 offset:1024
	ds_read_b128 v[138:141], v236 offset:2048
	ds_read_b128 v[142:145], v236 offset:3072
	ds_read_b128 v[186:189], v237
	ds_read_b128 v[190:193], v237 offset:1024
	ds_read_b128 v[178:181], v237 offset:2048
	ds_read_b128 v[182:185], v237 offset:3072
	ds_read_b128 v[170:173], v237 offset:4096
	ds_read_b128 v[174:177], v237 offset:5120
	ds_read_b128 v[162:165], v237 offset:6144
	ds_read_b128 v[166:169], v237 offset:7168
	s_and_b64 vcc, exec, s[26:27]
	s_cbranch_vccnz .LBB0_309
	s_waitcnt vmcnt(8)
;     __device__ __forceinline__ size_t a_off(const Unit& u, const Gemm& g) const { size_t o = (size_t)u.pm * BM * g.lda * 2; if (MODE == 1) o += (size_t)(u.pn >> 1) * 512 * 2; return o; }
;     __device__ __forceinline__ size_t b_off(const Unit& u, const Gemm& g) const { return (size_t)u.pn * BM * g.ldb * 2; }
; #define PG8_STAGE(bufoff, gbase, voff) do { _Pragma("unroll") for (int _i = 0; _i < 2; ++_i) \
;         __builtin_amdgcn_global_load_lds((const unsigned*)((const char*)(gbase) + (voff)[_i]), (LAS unsigned*)(lds + (bufoff) + ldsw + _i * 8192), 16, 0, 0); } while (0)
; #define PG8_LDA(dst, b, h) do { _Pragma("unroll") for (int m = 0; m < 4; ++m) _Pragma("unroll") for (int k = 0; k < 2; ++k) dst[m][k] = *(const LAS bf16x8*)(lds + PG8_SA(b, h) + aoff + m * 2048 + k * 1024); } while (0)
; #define PG8_WAIT_V(n) asm volatile("s_waitcnt vmcnt(" #n ")" ::: "memory")
; template <class Epi, class Sched, bool ALIGN_EPI = true, bool SP2 = true, class Side = NoSide>
; __device__ __forceinline__ void gemm_phase(LAS unsigned char* lds, const Gemm g, const Sched& S, const Epi& E, const Side side = Side()) {
;     ...
;         const bool has_next = S.next(ui + 1, nxt);
;         const char* nA = has_next ? (const char*)g.A + S.a_off(nxt, g) : cA; const char* nB = has_next ? (const char*)g.Bt + S.b_off(nxt, g) : cB;
; #pragma unroll 1
;         for (int t = 0; t < nt; t += 2) {
;             const bool last = (t == nt - 2);
;             const char* a1 = cA + (size_t)(t + 1) * kstep;
;             const char* a2 = last ? nA : cA + (size_t)(t + 2) * kstep; const char* b2 = last ? nB : cB + (size_t)(t + 2) * kstep;
;             const char* a3 = a2 + kstep; const char* b3 = b2 + kstep;
;             const bool after_epi = Epi::LOADS && t == 0 && ui > 0;
;             if constexpr (SP2) {
;             PG8_LDB(B0, 0, 0); PG8_LDB(B1, 0, 1); PG8_SCHED; PG8_LDA(At, 0, 0); PG8_STAGE(PG8_SA(1, 1), a1 + hstepA, voffA);
;             if (!after_epi) PG8_WAIT_V(8);
;             PG8_WAIT_L(0); PG8_BAR; PG8_MMA(0, 0, At, B0); PG8_MMA(0, 1, At, B1); PG8_BAR; PG8_SCHED;
;             PG8_LDA(At, 0, 1); PG8_STAGE(PG8_SB(0, 0), b2, voffB); PG8_STAGE(PG8_SB(0, 1), b2 + hstepB, voffB); PG8_STAGE(PG8_SA(0, 0), a2, voffA);
;             if (!after_epi) PG8_WAIT_V(8);
;             PG8_WAIT_L(0); PG8_BAR; PG8_MMA(1, 0, At, B0); PG8_MMA(1, 1, At, B1); PG8_BAR; PG8_SCHED;
.LBB0_309:
	s_xor_b64 s[30:31], s[26:27], -1
	s_add_u32 s26, s22, s24
	s_addc_u32 s27, s23, s25
	s_add_u32 s26, s26, 0x100
	s_addc_u32 s27, s27, 0
	s_add_u32 s57, s54, s24
	s_addc_u32 s58, s55, s25
	s_waitcnt lgkmcnt(0)
	s_cmpk_eq_i32 s24, 0x300
	s_cselect_b32 s29, s19, s27
	s_cselect_b32 s28, s18, s26
	s_cselect_b32 s27, s17, s58
	s_cselect_b32 s26, s53, s57
	s_barrier
	s_setprio 1
	s_waitcnt lgkmcnt(0)
	v_mfma_f32_16x16x32_bf16 v[126:129], v[146:149], v[186:189], v[126:129]
	v_mfma_f32_16x16x32_bf16 v[122:125], v[154:157], v[186:189], v[122:125]
	v_mfma_f32_16x16x32_bf16 v[118:121], v[146:149], v[178:181], v[118:121]
	v_mfma_f32_16x16x32_bf16 v[114:117], v[154:157], v[178:181], v[114:117]
	v_mfma_f32_16x16x32_bf16 v[110:113], v[146:149], v[170:173], v[110:113]
	v_mfma_f32_16x16x32_bf16 v[102:105], v[154:157], v[170:173], v[102:105]
	v_mfma_f32_16x16x32_bf16 v[94:97], v[146:149], v[162:165], v[94:97]
	v_mfma_f32_16x16x32_bf16 v[86:89], v[154:157], v[162:165], v[86:89]
	v_mfma_f32_16x16x32_bf16 v[126:129], v[150:153], v[190:193], v[126:129]
	v_mfma_f32_16x16x32_bf16 v[122:125], v[158:161], v[190:193], v[122:125]
	v_mfma_f32_16x16x32_bf16 v[118:121], v[150:153], v[182:185], v[118:121]
	v_mfma_f32_16x16x32_bf16 v[114:117], v[158:161], v[182:185], v[114:117]
	v_mfma_f32_16x16x32_bf16 v[110:113], v[150:153], v[174:177], v[110:113]
	v_mfma_f32_16x16x32_bf16 v[102:105], v[158:161], v[174:177], v[102:105]
	v_mfma_f32_16x16x32_bf16 v[94:97], v[150:153], v[166:169], v[94:97]
	v_mfma_f32_16x16x32_bf16 v[86:89], v[158:161], v[166:169], v[86:89]
	s_setprio 0
	s_setprio 1
	v_mfma_f32_16x16x32_bf16 v[106:109], v[130:133], v[186:189], v[106:109]
	v_mfma_f32_16x16x32_bf16 v[98:101], v[138:141], v[186:189], v[98:101]
	v_mfma_f32_16x16x32_bf16 v[90:93], v[130:133], v[178:181], v[90:93]
	v_mfma_f32_16x16x32_bf16 v[82:85], v[138:141], v[178:181], v[82:85]
	v_mfma_f32_16x16x32_bf16 v[78:81], v[130:133], v[170:173], v[78:81]
	v_mfma_f32_16x16x32_bf16 v[74:77], v[138:141], v[170:173], v[74:77]
	v_mfma_f32_16x16x32_bf16 v[70:73], v[130:133], v[162:165], v[70:73]
	v_mfma_f32_16x16x32_bf16 v[66:69], v[138:141], v[162:165], v[66:69]
	v_mfma_f32_16x16x32_bf16 v[106:109], v[134:137], v[190:193], v[106:109]
	v_mfma_f32_16x16x32_bf16 v[98:101], v[142:145], v[190:193], v[98:101]
	v_mfma_f32_16x16x32_bf16 v[90:93], v[134:137], v[182:185], v[90:93]
	v_mfma_f32_16x16x32_bf16 v[82:85], v[142:145], v[182:185], v[82:85]
	v_mfma_f32_16x16x32_bf16 v[78:81], v[134:137], v[174:177], v[78:81]
	v_mfma_f32_16x16x32_bf16 v[74:77], v[142:145], v[174:177], v[74:77]
	v_mfma_f32_16x16x32_bf16 v[70:73], v[134:137], v[166:169], v[70:73]
	v_mfma_f32_16x16x32_bf16 v[66:69], v[142:145], v[166:169], v[66:69]
	s_setprio 0
	s_barrier
	s_mov_b32 m0, s39
	v_lshl_add_u64 v[222:223], s[26:27], 0, v[198:199]
	s_add_u32 s58, s26, 0x20000
	global_load_lds_dwordx4 v[222:223], off
	v_lshl_add_u64 v[220:221], s[26:27], 0, v[202:203]
	s_mov_b32 m0, s40
	s_addc_u32 s59, s27, 0
	global_load_lds_dwordx4 v[220:221], off
	v_lshl_add_u64 v[216:217], s[58:59], 0, v[198:199]
	s_mov_b32 m0, s41
	v_lshl_add_u64 v[218:219], s[28:29], 0, v[200:201]
	global_load_lds_dwordx4 v[216:217], off
	v_lshl_add_u64 v[216:217], s[58:59], 0, v[202:203]
	s_mov_b32 m0, s42
	s_andn2_b64 vcc, exec, s[30:31]
	global_load_lds_dwordx4 v[216:217], off
	v_lshl_add_u64 v[216:217], s[28:29], 0, v[196:197]
	s_mov_b32 m0, s38
	s_nop 0
	global_load_lds_dwordx4 v[216:217], off
	s_mov_b32 m0, s43
	s_nop 0
	global_load_lds_dwordx4 v[218:219], off
	ds_read_b128 v[186:189], v237 offset:16384
	ds_read_b128 v[190:193], v237 offset:17408
	ds_read_b128 v[178:181], v237 offset:18432
	ds_read_b128 v[182:185], v237 offset:19456
	ds_read_b128 v[170:173], v237 offset:20480
	ds_read_b128 v[174:177], v237 offset:21504
	ds_read_b128 v[162:165], v237 offset:22528
	ds_read_b128 v[166:169], v237 offset:23552
	s_cbranch_vccnz .LBB0_306
	s_waitcnt vmcnt(8)
	s_branch .LBB0_306

; #define PG8_STAGE(bufoff, gbase, voff) do { _Pragma("unroll") for (int _i = 0; _i < 2; ++_i) \
;         __builtin_amdgcn_global_load_lds((const unsigned*)((const char*)(gbase) + (voff)[_i]), (LAS unsigned*)(lds + (bufoff) + ldsw + _i * 8192), 16, 0, 0); } while (0)
; #define PG8_LDA(dst, b, h) do { _Pragma("unroll") for (int m = 0; m < 4; ++m) _Pragma("unroll") for (int k = 0; k < 2; ++k) dst[m][k] = *(const LAS bf16x8*)(lds + PG8_SA(b, h) + aoff + m * 2048 + k * 1024); } while (0)
; #define PG8_LDB(dst, b, h) do { _Pragma("unroll") for (int n = 0; n < 2; ++n) _Pragma("unroll") for (int k = 0; k < 2; ++k) dst[n][k] = *(const LAS bf16x8*)(lds + PG8_SB(b, h) + boff + n * 2048 + k * 1024); } while (0)
; #define PG8_WAIT_V(n) asm volatile("s_waitcnt vmcnt(" #n ")" ::: "memory")
; #define PG8_WAIT_L(n) asm volatile("s_waitcnt lgkmcnt(" #n ")" ::: "memory")
; #define PG8_BAR __builtin_amdgcn_s_barrier()
; #define PG8_SCHED __builtin_amdgcn_sched_barrier(0)
; template <class Epi, class Sched, bool ALIGN_EPI = true, bool SP2 = true, class Side = NoSide>
; __device__ __forceinline__ void gemm_phase(LAS unsigned char* lds, const Gemm g, const Sched& S, const Epi& E, const Side side = Side()) {
;     ...
;             PG8_WAIT_L(0); PG8_BAR; PG8_MMA(0, 0, At, B0); PG8_MMA(0, 1, At, B1); PG8_BAR; PG8_SCHED;
;             PG8_LDA(At, 0, 1); PG8_STAGE(PG8_SB(0, 0), b2, voffB); PG8_STAGE(PG8_SB(0, 1), b2 + hstepB, voffB); PG8_STAGE(PG8_SA(0, 0), a2, voffA);
;             if (!after_epi) PG8_WAIT_V(8);
;             PG8_WAIT_L(0); PG8_BAR; PG8_MMA(1, 0, At, B0); PG8_MMA(1, 1, At, B1); PG8_BAR; PG8_SCHED;
;             PG8_LDB(B0, 1, 0); PG8_LDB(B1, 1, 1); PG8_SCHED; PG8_LDA(At, 1, 0); PG8_STAGE(PG8_SA(0, 1), a2 + hstepA, voffA);
;             PG8_WAIT_V(8); PG8_WAIT_L(0); PG8_BAR; PG8_MMA(0, 0, At, B0); PG8_MMA(0, 1, At, B1); PG8_BAR; PG8_SCHED;
.LBB0_996:
	s_waitcnt lgkmcnt(0)
	s_barrier
	s_setprio 1
	s_waitcnt lgkmcnt(0)
	v_mfma_i32_16x16x64_i8 v[62:65], v[146:149], v[186:189], v[62:65]
	v_mfma_i32_16x16x64_i8 v[58:61], v[154:157], v[186:189], v[58:61]
	v_mfma_i32_16x16x64_i8 v[46:49], v[146:149], v[178:181], v[46:49]
	v_mfma_i32_16x16x64_i8 v[42:45], v[154:157], v[178:181], v[42:45]
	v_mfma_i32_16x16x64_i8 v[30:33], v[146:149], v[170:173], v[30:33]
	v_mfma_i32_16x16x64_i8 v[26:29], v[154:157], v[170:173], v[26:29]
	v_mfma_i32_16x16x64_i8 v[14:17], v[146:149], v[162:165], v[14:17]
	v_mfma_i32_16x16x64_i8 v[10:13], v[154:157], v[162:165], v[10:13]
	v_mfma_i32_16x16x64_i8 v[62:65], v[150:153], v[190:193], v[62:65]
	v_mfma_i32_16x16x64_i8 v[58:61], v[158:161], v[190:193], v[58:61]
	v_mfma_i32_16x16x64_i8 v[46:49], v[150:153], v[182:185], v[46:49]
	v_mfma_i32_16x16x64_i8 v[42:45], v[158:161], v[182:185], v[42:45]
	v_mfma_i32_16x16x64_i8 v[30:33], v[150:153], v[174:177], v[30:33]
	v_mfma_i32_16x16x64_i8 v[26:29], v[158:161], v[174:177], v[26:29]
	v_mfma_i32_16x16x64_i8 v[14:17], v[150:153], v[166:169], v[14:17]
	v_mfma_i32_16x16x64_i8 v[10:13], v[158:161], v[166:169], v[10:13]
	s_setprio 0
	s_setprio 1
	v_mfma_i32_16x16x64_i8 v[54:57], v[70:73], v[186:189], v[54:57]
	v_mfma_i32_16x16x64_i8 v[50:53], v[78:81], v[186:189], v[50:53]
	v_mfma_i32_16x16x64_i8 v[38:41], v[70:73], v[178:181], v[38:41]
	v_mfma_i32_16x16x64_i8 v[34:37], v[78:81], v[178:181], v[34:37]
	v_mfma_i32_16x16x64_i8 v[22:25], v[70:73], v[170:173], v[22:25]
	v_mfma_i32_16x16x64_i8 v[18:21], v[78:81], v[170:173], v[18:21]
	v_mfma_i32_16x16x64_i8 v[6:9], v[70:73], v[162:165], v[6:9]
	v_mfma_i32_16x16x64_i8 v[2:5], v[78:81], v[162:165], v[2:5]
	v_mfma_i32_16x16x64_i8 v[54:57], v[74:77], v[190:193], v[54:57]
	v_mfma_i32_16x16x64_i8 v[50:53], v[142:145], v[190:193], v[50:53]
	v_mfma_i32_16x16x64_i8 v[38:41], v[74:77], v[182:185], v[38:41]
	v_mfma_i32_16x16x64_i8 v[34:37], v[142:145], v[182:185], v[34:37]
	v_mfma_i32_16x16x64_i8 v[22:25], v[74:77], v[174:177], v[22:25]
	v_mfma_i32_16x16x64_i8 v[18:21], v[142:145], v[174:177], v[18:21]
	v_mfma_i32_16x16x64_i8 v[6:9], v[74:77], v[166:169], v[6:9]
	v_mfma_i32_16x16x64_i8 v[2:5], v[142:145], v[166:169], v[2:5]
	s_setprio 0
	s_barrier
	s_add_i32 s44, 0, 0x18000
	s_add_i32 s45, 0, 0x1c000
	v_add_u32_e32 v142, s44, v230
	v_add_u32_e32 v158, s45, v230
	s_add_u32 s42, s42, 0x40000
	s_addc_u32 s43, s43, 0
	s_mov_b32 m0, s60
	v_lshl_add_u64 v[236:237], s[42:43], 0, v[196:197]
	global_load_lds_dwordx4 v[236:237], off
	v_lshl_add_u64 v[236:237], s[42:43], 0, v[200:201]
	s_mov_b32 m0, s61
	s_nop 0
	global_load_lds_dwordx4 v[236:237], off
	ds_read_b128 v[70:73], v142
	ds_read_b128 v[74:77], v142 offset:1024
	ds_read_b128 v[78:81], v142 offset:2048
	ds_read_b128 v[142:145], v142 offset:3072
	ds_read_b128 v[146:149], v158
	ds_read_b128 v[150:153], v158 offset:1024
	ds_read_b128 v[154:157], v158 offset:2048
	ds_read_b128 v[158:161], v158 offset:3072
	ds_read_b128 v[162:165], v234 offset:32768
	ds_read_b128 v[166:169], v234 offset:33792
	ds_read_b128 v[170:173], v234 offset:34816
	ds_read_b128 v[174:177], v234 offset:35840
	ds_read_b128 v[178:181], v234 offset:36864
	ds_read_b128 v[182:185], v234 offset:37888
	ds_read_b128 v[186:189], v234 offset:38912
	ds_read_b128 v[190:193], v234 offset:39936
	s_waitcnt vmcnt(8)
	s_waitcnt lgkmcnt(0)
	s_barrier
	s_setprio 1
	s_waitcnt lgkmcnt(0)
	v_mfma_i32_16x16x64_i8 v[66:69], v[70:73], v[162:165], v[66:69]
	v_mfma_i32_16x16x64_i8 v[138:141], v[78:81], v[162:165], v[138:141]
	v_mfma_i32_16x16x64_i8 v[126:129], v[70:73], v[170:173], v[126:129]
	v_mfma_i32_16x16x64_i8 v[122:125], v[78:81], v[170:173], v[122:125]
	v_mfma_i32_16x16x64_i8 v[110:113], v[70:73], v[178:181], v[110:113]
	v_mfma_i32_16x16x64_i8 v[106:109], v[78:81], v[178:181], v[106:109]
	v_mfma_i32_16x16x64_i8 v[94:97], v[70:73], v[186:189], v[94:97]
	v_mfma_i32_16x16x64_i8 v[90:93], v[78:81], v[186:189], v[90:93]
	v_mfma_i32_16x16x64_i8 v[66:69], v[74:77], v[166:169], v[66:69]
	v_mfma_i32_16x16x64_i8 v[138:141], v[142:145], v[166:169], v[138:141]
	v_mfma_i32_16x16x64_i8 v[126:129], v[74:77], v[174:177], v[126:129]
	v_mfma_i32_16x16x64_i8 v[122:125], v[142:145], v[174:177], v[122:125]
	v_mfma_i32_16x16x64_i8 v[110:113], v[74:77], v[182:185], v[110:113]
	v_mfma_i32_16x16x64_i8 v[106:109], v[142:145], v[182:185], v[106:109]
	v_mfma_i32_16x16x64_i8 v[94:97], v[74:77], v[190:193], v[94:97]
	v_mfma_i32_16x16x64_i8 v[90:93], v[142:145], v[190:193], v[90:93]
	s_setprio 0
	s_setprio 1
	v_mfma_i32_16x16x64_i8 v[134:137], v[146:149], v[162:165], v[134:137]
	v_mfma_i32_16x16x64_i8 v[130:133], v[154:157], v[162:165], v[130:133]
	v_mfma_i32_16x16x64_i8 v[118:121], v[146:149], v[170:173], v[118:121]
	v_mfma_i32_16x16x64_i8 v[114:117], v[154:157], v[170:173], v[114:117]
	v_mfma_i32_16x16x64_i8 v[102:105], v[146:149], v[178:181], v[102:105]
	v_mfma_i32_16x16x64_i8 v[98:101], v[154:157], v[178:181], v[98:101]
	v_mfma_i32_16x16x64_i8 v[86:89], v[146:149], v[186:189], v[86:89]
	v_mfma_i32_16x16x64_i8 v[82:85], v[154:157], v[186:189], v[82:85]
	v_mfma_i32_16x16x64_i8 v[134:137], v[150:153], v[166:169], v[134:137]
	v_mfma_i32_16x16x64_i8 v[130:133], v[158:161], v[166:169], v[130:133]
	v_mfma_i32_16x16x64_i8 v[118:121], v[150:153], v[174:177], v[118:121]
	v_mfma_i32_16x16x64_i8 v[114:117], v[158:161], v[174:177], v[114:117]
	v_mfma_i32_16x16x64_i8 v[102:105], v[150:153], v[182:185], v[102:105]
	v_mfma_i32_16x16x64_i8 v[98:101], v[158:161], v[182:185], v[98:101]
	v_mfma_i32_16x16x64_i8 v[86:89], v[150:153], v[190:193], v[86:89]
	v_mfma_i32_16x16x64_i8 v[82:85], v[158:161], v[190:193], v[82:85]
	s_setprio 0
	s_barrier
; #define PG8_STAGE(bufoff, gbase, voff) do { _Pragma("unroll") for (int _i = 0; _i < 2; ++_i) \
;         __builtin_amdgcn_global_load_lds((const unsigned*)((const char*)(gbase) + (voff)[_i]), (LAS unsigned*)(lds + (bufoff) + ldsw + _i * 8192), 16, 0, 0); } while (0)
; #define PG8_LDA(dst, b, h) do { _Pragma("unroll") for (int m = 0; m < 4; ++m) _Pragma("unroll") for (int k = 0; k < 2; ++k) dst[m][k] = *(const LAS bf16x8*)(lds + PG8_SA(b, h) + aoff + m * 2048 + k * 1024); } while (0)
; #define PG8_LDB(dst, b, h) do { _Pragma("unroll") for (int n = 0; n < 2; ++n) _Pragma("unroll") for (int k = 0; k < 2; ++k) dst[n][k] = *(const LAS bf16x8*)(lds + PG8_SB(b, h) + boff + n * 2048 + k * 1024); } while (0)
; #define PG8_WAIT_V(n) asm volatile("s_waitcnt vmcnt(" #n ")" ::: "memory")
; #define PG8_WAIT_L(n) asm volatile("s_waitcnt lgkmcnt(" #n ")" ::: "memory")
; #define PG8_BAR __builtin_amdgcn_s_barrier()
; #define PG8_SCHED __builtin_amdgcn_sched_barrier(0)
; template <class Epi, class Sched, bool ALIGN_EPI = true, bool SP2 = true, class Side = NoSide>
; __device__ __forceinline__ void gemm_phase(LAS unsigned char* lds, const Gemm g, const Sched& S, const Epi& E, const Side side = Side()) {
;     ...
;             PG8_LDB(B0, 0, 0); PG8_LDB(B1, 0, 1); PG8_SCHED; PG8_LDA(At, 0, 0); PG8_STAGE(PG8_SA(1, 1), a1 + hstepA, voffA);
;             if (!after_epi) PG8_WAIT_V(8);
;             PG8_WAIT_L(0); PG8_BAR; PG8_MMA(0, 0, At, B0); PG8_MMA(0, 1, At, B1); PG8_BAR; PG8_SCHED;
;             PG8_LDA(At, 0, 1); PG8_STAGE(PG8_SB(0, 0), b2, voffB); PG8_STAGE(PG8_SB(0, 1), b2 + hstepB, voffB); PG8_STAGE(PG8_SA(0, 0), a2, voffA);
;             if (!after_epi) PG8_WAIT_V(8);
;             PG8_WAIT_L(0); PG8_BAR; PG8_MMA(1, 0, At, B0); PG8_MMA(1, 1, At, B1); PG8_BAR; PG8_SCHED;
;             PG8_LDB(B0, 1, 0); PG8_LDB(B1, 1, 1); PG8_SCHED; PG8_LDA(At, 1, 0); PG8_STAGE(PG8_SA(0, 1), a2 + hstepA, voffA);
;             PG8_WAIT_V(8); PG8_WAIT_L(0); PG8_BAR; PG8_MMA(0, 0, At, B0); PG8_MMA(0, 1, At, B1); PG8_BAR; PG8_SCHED;
;             PG8_LDA(At, 1, 1); PG8_STAGE(PG8_SB(1, 0), b3, voffB); PG8_STAGE(PG8_SB(1, 1), b3 + hstepB, voffB); PG8_STAGE(PG8_SA(1, 0), a3, voffA);
;             PG8_WAIT_V(8); PG8_WAIT_L(0); PG8_BAR; PG8_MMA(1, 0, At, B0); PG8_MMA(1, 1, At, B1); PG8_BAR; PG8_SCHED;
	s_add_i32 s42, s44, s54
	v_lshl_add_u64 v[222:223], v[222:223], 0, s[16:17]
	s_mov_b32 m0, s42
	s_nop 0
	global_load_lds_dwordx4 v[222:223], off
	s_add_i32 m0, s42, 0x2000
	s_add_u32 s40, s40, 0x40080
	v_lshl_add_u64 v[220:221], v[220:221], 0, s[16:17]
	s_addc_u32 s41, s41, 0
	s_add_i32 s42, s45, s54
	global_load_lds_dwordx4 v[220:221], off
	v_lshl_add_u64 v[220:221], s[40:41], 0, v[198:199]
	s_mov_b32 m0, s42
	v_lshl_add_u64 v[216:217], v[216:217], 0, s[16:17]
	global_load_lds_dwordx4 v[220:221], off
	v_lshl_add_u64 v[220:221], s[40:41], 0, v[202:203]
	s_add_i32 m0, s42, 0x2000
	s_nop 0
	global_load_lds_dwordx4 v[220:221], off
	s_mov_b32 m0, s62
	s_nop 0
	global_load_lds_dwordx4 v[216:217], off
	v_lshl_add_u64 v[216:217], v[218:219], 0, s[16:17]
	s_mov_b32 m0, s63
	s_nop 0
	global_load_lds_dwordx4 v[216:217], off
	ds_read_b128 v[162:165], v234 offset:49152
	ds_read_b128 v[166:169], v234 offset:50176
	ds_read_b128 v[170:173], v234 offset:51200
	ds_read_b128 v[174:177], v234 offset:52224
	ds_read_b128 v[178:181], v234 offset:53248
	ds_read_b128 v[182:185], v234 offset:54272
	ds_read_b128 v[186:189], v234 offset:55296
	ds_read_b128 v[190:193], v234 offset:56320
	s_waitcnt vmcnt(8)
	s_waitcnt lgkmcnt(0)
	s_barrier
	s_setprio 1
	s_waitcnt lgkmcnt(0)
	v_mfma_i32_16x16x64_i8 v[62:65], v[70:73], v[162:165], v[62:65]
	v_mfma_i32_16x16x64_i8 v[58:61], v[78:81], v[162:165], v[58:61]
	v_mfma_i32_16x16x64_i8 v[46:49], v[70:73], v[170:173], v[46:49]
	v_mfma_i32_16x16x64_i8 v[42:45], v[78:81], v[170:173], v[42:45]
	v_mfma_i32_16x16x64_i8 v[30:33], v[70:73], v[178:181], v[30:33]
	v_mfma_i32_16x16x64_i8 v[26:29], v[78:81], v[178:181], v[26:29]
	v_mfma_i32_16x16x64_i8 v[14:17], v[70:73], v[186:189], v[14:17]
	v_mfma_i32_16x16x64_i8 v[10:13], v[78:81], v[186:189], v[10:13]
	v_mfma_i32_16x16x64_i8 v[62:65], v[74:77], v[166:169], v[62:65]
	v_mfma_i32_16x16x64_i8 v[58:61], v[142:145], v[166:169], v[58:61]
	v_mfma_i32_16x16x64_i8 v[46:49], v[74:77], v[174:177], v[46:49]
	v_mfma_i32_16x16x64_i8 v[42:45], v[142:145], v[174:177], v[42:45]
	v_mfma_i32_16x16x64_i8 v[30:33], v[74:77], v[182:185], v[30:33]
	v_mfma_i32_16x16x64_i8 v[26:29], v[142:145], v[182:185], v[26:29]
	v_mfma_i32_16x16x64_i8 v[14:17], v[74:77], v[190:193], v[14:17]
	v_mfma_i32_16x16x64_i8 v[10:13], v[142:145], v[190:193], v[10:13]
	s_setprio 0
	s_setprio 1
	v_mfma_i32_16x16x64_i8 v[54:57], v[146:149], v[162:165], v[54:57]
	v_mfma_i32_16x16x64_i8 v[50:53], v[154:157], v[162:165], v[50:53]
	v_mfma_i32_16x16x64_i8 v[38:41], v[146:149], v[170:173], v[38:41]
	v_mfma_i32_16x16x64_i8 v[34:37], v[154:157], v[170:173], v[34:37]
	v_mfma_i32_16x16x64_i8 v[22:25], v[146:149], v[178:181], v[22:25]
	v_mfma_i32_16x16x64_i8 v[18:21], v[154:157], v[178:181], v[18:21]
	v_mfma_i32_16x16x64_i8 v[6:9], v[146:149], v[186:189], v[6:9]
	v_mfma_i32_16x16x64_i8 v[2:5], v[154:157], v[186:189], v[2:5]
	v_mfma_i32_16x16x64_i8 v[54:57], v[150:153], v[166:169], v[54:57]
	v_mfma_i32_16x16x64_i8 v[50:53], v[158:161], v[166:169], v[50:53]
	v_mfma_i32_16x16x64_i8 v[38:41], v[150:153], v[174:177], v[38:41]
	v_mfma_i32_16x16x64_i8 v[34:37], v[158:161], v[174:177], v[34:37]
	v_mfma_i32_16x16x64_i8 v[22:25], v[150:153], v[182:185], v[22:25]
	v_mfma_i32_16x16x64_i8 v[18:21], v[158:161], v[182:185], v[18:21]
	v_mfma_i32_16x16x64_i8 v[6:9], v[150:153], v[190:193], v[6:9]
	v_mfma_i32_16x16x64_i8 v[2:5], v[158:161], v[190:193], v[2:5]
	s_setprio 0
	s_barrier
	s_add_i32 s71, s71, 2
	s_add_u32 s38, s38, 0x100
	s_addc_u32 s39, s39, 0
	s_cmp_gt_u32 s71, 13
	s_cbranch_scc1 .LBB0_1001
.LBB0_997:
	s_cmp_eq_u32 s38, 0
	s_cselect_b64 s[40:41], -1, 0
	v_lshl_add_u64 v[216:217], v[212:213], 0, s[38:39]
	s_add_i32 m0, s31, 0xc000
	s_nop 0
	global_load_lds_dwordx4 v[216:217], off
	v_lshl_add_u64 v[216:217], v[214:215], 0, s[38:39]
	s_add_i32 m0, s31, 0xe000
	s_and_b64 s[40:41], s[36:37], s[40:41]
	global_load_lds_dwordx4 v[216:217], off
	ds_read_b128 v[146:149], v232
	ds_read_b128 v[150:153], v232 offset:1024
	ds_read_b128 v[154:157], v232 offset:2048
	ds_read_b128 v[158:161], v232 offset:3072
	ds_read_b128 v[70:73], v233
	ds_read_b128 v[74:77], v233 offset:1024
	ds_read_b128 v[78:81], v233 offset:2048
	ds_read_b128 v[142:145], v233 offset:3072
	ds_read_b128 v[186:189], v234
	ds_read_b128 v[190:193], v234 offset:1024
	ds_read_b128 v[178:181], v234 offset:2048
	ds_read_b128 v[182:185], v234 offset:3072
	ds_read_b128 v[170:173], v234 offset:4096
	ds_read_b128 v[174:177], v234 offset:5120
	ds_read_b128 v[162:165], v234 offset:6144
	ds_read_b128 v[166:169], v234 offset:7168
	s_and_b64 vcc, exec, s[40:41]
	s_cbranch_vccnz .LBB0_999
	s_waitcnt vmcnt(8)
; #define PG8_STAGE(bufoff, gbase, voff) do { _Pragma("unroll") for (int _i = 0; _i < 2; ++_i) \
;         __builtin_amdgcn_global_load_lds((const unsigned*)((const char*)(gbase) + (voff)[_i]), (LAS unsigned*)(lds + (bufoff) + ldsw + _i * 8192), 16, 0, 0); } while (0)
; #define PG8_LDA(dst, b, h) do { _Pragma("unroll") for (int m = 0; m < 4; ++m) _Pragma("unroll") for (int k = 0; k < 2; ++k) dst[m][k] = *(const LAS bf16x8*)(lds + PG8_SA(b, h) + aoff + m * 2048 + k * 1024); } while (0)
; #define PG8_LDB(dst, b, h) do { _Pragma("unroll") for (int n = 0; n < 2; ++n) _Pragma("unroll") for (int k = 0; k < 2; ++k) dst[n][k] = *(const LAS bf16x8*)(lds + PG8_SB(b, h) + boff + n * 2048 + k * 1024); } while (0)
; #define PG8_WAIT_V(n) asm volatile("s_waitcnt vmcnt(" #n ")" ::: "memory")
; #define PG8_WAIT_L(n) asm volatile("s_waitcnt lgkmcnt(" #n ")" ::: "memory")
; #define PG8_BAR __builtin_amdgcn_s_barrier()
; #define PG8_SCHED __builtin_amdgcn_sched_barrier(0)
; template <class Epi, class Sched, bool ALIGN_EPI = true, bool SP2 = true, class Side = NoSide>
; __device__ __forceinline__ void gemm_phase(LAS unsigned char* lds, const Gemm g, const Sched& S, const Epi& E, const Side side = Side()) {
;     ...
;             const bool last = (t == nt - 2);
;             const char* a1 = cA + (size_t)(t + 1) * kstep;
;             const char* a2 = last ? nA : cA + (size_t)(t + 2) * kstep; const char* b2 = last ? nB : cB + (size_t)(t + 2) * kstep;
;             const char* a3 = a2 + kstep; const char* b3 = b2 + kstep;
;             const bool after_epi = Epi::LOADS && t == 0 && ui > 0;
;             if constexpr (SP2) {
;             PG8_LDB(B0, 0, 0); PG8_LDB(B1, 0, 1); PG8_SCHED; PG8_LDA(At, 0, 0); PG8_STAGE(PG8_SA(1, 1), a1 + hstepA, voffA);
;             if (!after_epi) PG8_WAIT_V(8);
;             PG8_WAIT_L(0); PG8_BAR; PG8_MMA(0, 0, At, B0); PG8_MMA(0, 1, At, B1); PG8_BAR; PG8_SCHED;
;             PG8_LDA(At, 0, 1); PG8_STAGE(PG8_SB(0, 0), b2, voffB); PG8_STAGE(PG8_SB(0, 1), b2 + hstepB, voffB); PG8_STAGE(PG8_SA(0, 0), a2, voffA);
;             if (!after_epi) PG8_WAIT_V(8);
.LBB0_999:
	s_xor_b64 s[44:45], s[40:41], -1
	s_add_u32 s40, s34, s38
	s_addc_u32 s41, s35, s39
	s_add_u32 s40, s40, 0x100
	s_addc_u32 s41, s41, 0
	s_add_u32 s72, s69, s38
	s_addc_u32 s73, s70, s39
	s_waitcnt lgkmcnt(0)
	s_cmpk_eq_i32 s38, 0x700
	s_cselect_b32 s43, s25, s41
	s_cselect_b32 s42, s67, s40
	s_cselect_b32 s41, s23, s73
	s_cselect_b32 s40, s68, s72
	s_barrier
	s_setprio 1
	s_waitcnt lgkmcnt(0)
	v_mfma_i32_16x16x64_i8 v[66:69], v[146:149], v[186:189], v[66:69]
	v_mfma_i32_16x16x64_i8 v[138:141], v[154:157], v[186:189], v[138:141]
	v_mfma_i32_16x16x64_i8 v[126:129], v[146:149], v[178:181], v[126:129]
	v_mfma_i32_16x16x64_i8 v[122:125], v[154:157], v[178:181], v[122:125]
	v_mfma_i32_16x16x64_i8 v[110:113], v[146:149], v[170:173], v[110:113]
	v_mfma_i32_16x16x64_i8 v[106:109], v[154:157], v[170:173], v[106:109]
	v_mfma_i32_16x16x64_i8 v[94:97], v[146:149], v[162:165], v[94:97]
	v_mfma_i32_16x16x64_i8 v[90:93], v[154:157], v[162:165], v[90:93]
	v_mfma_i32_16x16x64_i8 v[66:69], v[150:153], v[190:193], v[66:69]
	v_mfma_i32_16x16x64_i8 v[138:141], v[158:161], v[190:193], v[138:141]
	v_mfma_i32_16x16x64_i8 v[126:129], v[150:153], v[182:185], v[126:129]
	v_mfma_i32_16x16x64_i8 v[122:125], v[158:161], v[182:185], v[122:125]
	v_mfma_i32_16x16x64_i8 v[110:113], v[150:153], v[174:177], v[110:113]
	v_mfma_i32_16x16x64_i8 v[106:109], v[158:161], v[174:177], v[106:109]
	v_mfma_i32_16x16x64_i8 v[94:97], v[150:153], v[166:169], v[94:97]
	v_mfma_i32_16x16x64_i8 v[90:93], v[158:161], v[166:169], v[90:93]
	s_setprio 0
	s_setprio 1
	v_mfma_i32_16x16x64_i8 v[134:137], v[70:73], v[186:189], v[134:137]
	v_mfma_i32_16x16x64_i8 v[130:133], v[78:81], v[186:189], v[130:133]
	v_mfma_i32_16x16x64_i8 v[118:121], v[70:73], v[178:181], v[118:121]
	v_mfma_i32_16x16x64_i8 v[114:117], v[78:81], v[178:181], v[114:117]
	v_mfma_i32_16x16x64_i8 v[102:105], v[70:73], v[170:173], v[102:105]
	v_mfma_i32_16x16x64_i8 v[98:101], v[78:81], v[170:173], v[98:101]
	v_mfma_i32_16x16x64_i8 v[86:89], v[70:73], v[162:165], v[86:89]
	v_mfma_i32_16x16x64_i8 v[82:85], v[78:81], v[162:165], v[82:85]
	v_mfma_i32_16x16x64_i8 v[134:137], v[74:77], v[190:193], v[134:137]
	v_mfma_i32_16x16x64_i8 v[130:133], v[142:145], v[190:193], v[130:133]
	v_mfma_i32_16x16x64_i8 v[118:121], v[74:77], v[182:185], v[118:121]
	v_mfma_i32_16x16x64_i8 v[114:117], v[142:145], v[182:185], v[114:117]
	v_mfma_i32_16x16x64_i8 v[102:105], v[74:77], v[174:177], v[102:105]
	v_mfma_i32_16x16x64_i8 v[98:101], v[142:145], v[174:177], v[98:101]
	v_mfma_i32_16x16x64_i8 v[86:89], v[74:77], v[166:169], v[86:89]
	v_mfma_i32_16x16x64_i8 v[82:85], v[142:145], v[166:169], v[82:85]
	s_setprio 0
	s_barrier
	s_mov_b32 m0, s55
	v_lshl_add_u64 v[222:223], s[40:41], 0, v[198:199]
	s_add_u32 s72, s40, 0x40000
	global_load_lds_dwordx4 v[222:223], off
	v_lshl_add_u64 v[220:221], s[40:41], 0, v[202:203]
	s_mov_b32 m0, s56
	s_addc_u32 s73, s41, 0
	global_load_lds_dwordx4 v[220:221], off
	v_lshl_add_u64 v[216:217], s[72:73], 0, v[198:199]
	s_mov_b32 m0, s57
	v_lshl_add_u64 v[218:219], s[42:43], 0, v[200:201]
	global_load_lds_dwordx4 v[216:217], off
	v_lshl_add_u64 v[216:217], s[72:73], 0, v[202:203]
	s_mov_b32 m0, s58
	s_andn2_b64 vcc, exec, s[44:45]
	global_load_lds_dwordx4 v[216:217], off
	v_lshl_add_u64 v[216:217], s[42:43], 0, v[196:197]
	s_mov_b32 m0, s31
	s_nop 0
	global_load_lds_dwordx4 v[216:217], off
	s_mov_b32 m0, s59
	s_nop 0
	global_load_lds_dwordx4 v[218:219], off
	ds_read_b128 v[186:189], v234 offset:16384
	ds_read_b128 v[190:193], v234 offset:17408
	ds_read_b128 v[178:181], v234 offset:18432
	ds_read_b128 v[182:185], v234 offset:19456
	ds_read_b128 v[170:173], v234 offset:20480
	ds_read_b128 v[174:177], v234 offset:21504
	ds_read_b128 v[162:165], v234 offset:22528
	ds_read_b128 v[166:169], v234 offset:23552
	s_cbranch_vccnz .LBB0_996
	s_waitcnt vmcnt(8)
	s_branch .LBB0_996

; #define PG8_STAGE(bufoff, gbase, voff) do { _Pragma("unroll") for (int _i = 0; _i < 2; ++_i) \
;         __builtin_amdgcn_global_load_lds((const unsigned*)((const char*)(gbase) + (voff)[_i]), (LAS unsigned*)(lds + (bufoff) + ldsw + _i * 8192), 16, 0, 0); } while (0)
; #define PG8_LDA(dst, b, h) do { _Pragma("unroll") for (int m = 0; m < 4; ++m) _Pragma("unroll") for (int k = 0; k < 2; ++k) dst[m][k] = *(const LAS bf16x8*)(lds + PG8_SA(b, h) + aoff + m * 2048 + k * 1024); } while (0)
; #define PG8_LDB(dst, b, h) do { _Pragma("unroll") for (int n = 0; n < 2; ++n) _Pragma("unroll") for (int k = 0; k < 2; ++k) dst[n][k] = *(const LAS bf16x8*)(lds + PG8_SB(b, h) + boff + n * 2048 + k * 1024); } while (0)
; #define PG8_WAIT_V(n) asm volatile("s_waitcnt vmcnt(" #n ")" ::: "memory")
; #define PG8_WAIT_L(n) asm volatile("s_waitcnt lgkmcnt(" #n ")" ::: "memory")
; #define PG8_BAR __builtin_amdgcn_s_barrier()
; #define PG8_SCHED __builtin_amdgcn_sched_barrier(0)
; template <class Epi, class Sched, bool ALIGN_EPI = true, bool SP2 = true, class Side = NoSide>
; __device__ __forceinline__ void gemm_phase(LAS unsigned char* lds, const Gemm g, const Sched& S, const Epi& E, const Side side = Side()) {
;     ...
;             PG8_LDA(At, 0, 1); PG8_STAGE(PG8_SB(0, 0), b2, voffB); PG8_STAGE(PG8_SB(0, 1), b2 + hstepB, voffB); PG8_STAGE(PG8_SA(0, 0), a2, voffA);
;             if (!after_epi) PG8_WAIT_V(8);
;             PG8_WAIT_L(0); PG8_BAR; PG8_MMA(1, 0, At, B0); PG8_MMA(1, 1, At, B1); PG8_BAR; PG8_SCHED;
;             PG8_LDB(B0, 1, 0); PG8_LDB(B1, 1, 1); PG8_SCHED; PG8_LDA(At, 1, 0); PG8_STAGE(PG8_SA(0, 1), a2 + hstepA, voffA);
;             PG8_WAIT_V(8); PG8_WAIT_L(0); PG8_BAR; PG8_MMA(0, 0, At, B0); PG8_MMA(0, 1, At, B1); PG8_BAR; PG8_SCHED;
.LBB0_1023:
	s_waitcnt lgkmcnt(0)
	s_barrier
	s_setprio 1
	s_waitcnt lgkmcnt(0)
	v_mfma_i32_16x16x64_i8 v[78:81], v[146:149], v[186:189], v[78:81]
	v_mfma_i32_16x16x64_i8 v[74:77], v[154:157], v[186:189], v[74:77]
	v_mfma_i32_16x16x64_i8 v[46:49], v[146:149], v[178:181], v[46:49]
	v_mfma_i32_16x16x64_i8 v[42:45], v[154:157], v[178:181], v[42:45]
	v_mfma_i32_16x16x64_i8 v[30:33], v[146:149], v[170:173], v[30:33]
	v_mfma_i32_16x16x64_i8 v[26:29], v[154:157], v[170:173], v[26:29]
	v_mfma_i32_16x16x64_i8 v[14:17], v[146:149], v[162:165], v[14:17]
	v_mfma_i32_16x16x64_i8 v[10:13], v[154:157], v[162:165], v[10:13]
	v_mfma_i32_16x16x64_i8 v[78:81], v[150:153], v[190:193], v[78:81]
	v_mfma_i32_16x16x64_i8 v[74:77], v[158:161], v[190:193], v[74:77]
	v_mfma_i32_16x16x64_i8 v[46:49], v[150:153], v[182:185], v[46:49]
	v_mfma_i32_16x16x64_i8 v[42:45], v[158:161], v[182:185], v[42:45]
	v_mfma_i32_16x16x64_i8 v[30:33], v[150:153], v[174:177], v[30:33]
	v_mfma_i32_16x16x64_i8 v[26:29], v[158:161], v[174:177], v[26:29]
	v_mfma_i32_16x16x64_i8 v[14:17], v[150:153], v[166:169], v[14:17]
	v_mfma_i32_16x16x64_i8 v[10:13], v[158:161], v[166:169], v[10:13]
	s_setprio 0
	s_setprio 1
	v_mfma_i32_16x16x64_i8 v[70:73], v[62:65], v[186:189], v[70:73]
	v_mfma_i32_16x16x64_i8 v[58:61], v[138:141], v[186:189], v[58:61]
	v_mfma_i32_16x16x64_i8 v[38:41], v[62:65], v[178:181], v[38:41]
	v_mfma_i32_16x16x64_i8 v[34:37], v[138:141], v[178:181], v[34:37]
	v_mfma_i32_16x16x64_i8 v[22:25], v[62:65], v[170:173], v[22:25]
	v_mfma_i32_16x16x64_i8 v[18:21], v[138:141], v[170:173], v[18:21]
	v_mfma_i32_16x16x64_i8 v[6:9], v[62:65], v[162:165], v[6:9]
	v_mfma_i32_16x16x64_i8 v[2:5], v[138:141], v[162:165], v[2:5]
	v_mfma_i32_16x16x64_i8 v[70:73], v[66:69], v[190:193], v[70:73]
	v_mfma_i32_16x16x64_i8 v[58:61], v[142:145], v[190:193], v[58:61]
	v_mfma_i32_16x16x64_i8 v[38:41], v[66:69], v[182:185], v[38:41]
	v_mfma_i32_16x16x64_i8 v[34:37], v[142:145], v[182:185], v[34:37]
	v_mfma_i32_16x16x64_i8 v[22:25], v[66:69], v[174:177], v[22:25]
	v_mfma_i32_16x16x64_i8 v[18:21], v[142:145], v[174:177], v[18:21]
	v_mfma_i32_16x16x64_i8 v[6:9], v[66:69], v[166:169], v[6:9]
	v_mfma_i32_16x16x64_i8 v[2:5], v[142:145], v[166:169], v[2:5]
	s_setprio 0
	s_barrier
	s_add_i32 s48, 0, 0x18000
	s_add_i32 s49, 0, 0x1c000
	v_add_u32_e32 v142, s48, v195
	v_add_u32_e32 v158, s49, v195
	s_add_u32 s46, s46, 0x40000
	s_addc_u32 s47, s47, 0
	s_mov_b32 m0, s61
	v_lshl_add_u64 v[230:231], s[46:47], 0, v[196:197]
	global_load_lds_dwordx4 v[230:231], off
	v_lshl_add_u64 v[230:231], s[46:47], 0, v[200:201]
	s_mov_b32 m0, s62
	s_nop 0
	global_load_lds_dwordx4 v[230:231], off
	ds_read_b128 v[62:65], v142
	ds_read_b128 v[66:69], v142 offset:1024
	ds_read_b128 v[138:141], v142 offset:2048
	ds_read_b128 v[142:145], v142 offset:3072
	ds_read_b128 v[146:149], v158
	ds_read_b128 v[150:153], v158 offset:1024
	ds_read_b128 v[154:157], v158 offset:2048
	ds_read_b128 v[158:161], v158 offset:3072
	ds_read_b128 v[162:165], v227 offset:32768
	ds_read_b128 v[166:169], v227 offset:33792
	ds_read_b128 v[170:173], v227 offset:34816
	ds_read_b128 v[174:177], v227 offset:35840
	ds_read_b128 v[178:181], v227 offset:36864
	ds_read_b128 v[182:185], v227 offset:37888
	ds_read_b128 v[186:189], v227 offset:38912
	ds_read_b128 v[190:193], v227 offset:39936
	s_waitcnt vmcnt(8)
	s_waitcnt lgkmcnt(0)
	s_barrier
	s_setprio 1
	s_waitcnt lgkmcnt(0)
	v_mfma_i32_16x16x64_i8 v[54:57], v[62:65], v[162:165], v[54:57]
	v_mfma_i32_16x16x64_i8 v[50:53], v[138:141], v[162:165], v[50:53]
	v_mfma_i32_16x16x64_i8 v[126:129], v[62:65], v[170:173], v[126:129]
	v_mfma_i32_16x16x64_i8 v[122:125], v[138:141], v[170:173], v[122:125]
	v_mfma_i32_16x16x64_i8 v[110:113], v[62:65], v[178:181], v[110:113]
	v_mfma_i32_16x16x64_i8 v[106:109], v[138:141], v[178:181], v[106:109]
	v_mfma_i32_16x16x64_i8 v[94:97], v[62:65], v[186:189], v[94:97]
	v_mfma_i32_16x16x64_i8 v[90:93], v[138:141], v[186:189], v[90:93]
	v_mfma_i32_16x16x64_i8 v[54:57], v[66:69], v[166:169], v[54:57]
	v_mfma_i32_16x16x64_i8 v[50:53], v[142:145], v[166:169], v[50:53]
	v_mfma_i32_16x16x64_i8 v[126:129], v[66:69], v[174:177], v[126:129]
	v_mfma_i32_16x16x64_i8 v[122:125], v[142:145], v[174:177], v[122:125]
	v_mfma_i32_16x16x64_i8 v[110:113], v[66:69], v[182:185], v[110:113]
	v_mfma_i32_16x16x64_i8 v[106:109], v[142:145], v[182:185], v[106:109]
	v_mfma_i32_16x16x64_i8 v[94:97], v[66:69], v[190:193], v[94:97]
	v_mfma_i32_16x16x64_i8 v[90:93], v[142:145], v[190:193], v[90:93]
	s_setprio 0
	s_setprio 1
	v_mfma_i32_16x16x64_i8 v[134:137], v[146:149], v[162:165], v[134:137]
	v_mfma_i32_16x16x64_i8 v[130:133], v[154:157], v[162:165], v[130:133]
	v_mfma_i32_16x16x64_i8 v[118:121], v[146:149], v[170:173], v[118:121]
	v_mfma_i32_16x16x64_i8 v[114:117], v[154:157], v[170:173], v[114:117]
	v_mfma_i32_16x16x64_i8 v[102:105], v[146:149], v[178:181], v[102:105]
	v_mfma_i32_16x16x64_i8 v[98:101], v[154:157], v[178:181], v[98:101]
	v_mfma_i32_16x16x64_i8 v[86:89], v[146:149], v[186:189], v[86:89]
	v_mfma_i32_16x16x64_i8 v[82:85], v[154:157], v[186:189], v[82:85]
	v_mfma_i32_16x16x64_i8 v[134:137], v[150:153], v[166:169], v[134:137]
	v_mfma_i32_16x16x64_i8 v[130:133], v[158:161], v[166:169], v[130:133]
	v_mfma_i32_16x16x64_i8 v[118:121], v[150:153], v[174:177], v[118:121]
	v_mfma_i32_16x16x64_i8 v[114:117], v[158:161], v[174:177], v[114:117]
	v_mfma_i32_16x16x64_i8 v[102:105], v[150:153], v[182:185], v[102:105]
	v_mfma_i32_16x16x64_i8 v[98:101], v[158:161], v[182:185], v[98:101]
	v_mfma_i32_16x16x64_i8 v[86:89], v[150:153], v[190:193], v[86:89]
	v_mfma_i32_16x16x64_i8 v[82:85], v[158:161], v[190:193], v[82:85]
	s_setprio 0
	s_barrier
; #define PG8_STAGE(bufoff, gbase, voff) do { _Pragma("unroll") for (int _i = 0; _i < 2; ++_i) \
;         __builtin_amdgcn_global_load_lds((const unsigned*)((const char*)(gbase) + (voff)[_i]), (LAS unsigned*)(lds + (bufoff) + ldsw + _i * 8192), 16, 0, 0); } while (0)
; #define PG8_LDA(dst, b, h) do { _Pragma("unroll") for (int m = 0; m < 4; ++m) _Pragma("unroll") for (int k = 0; k < 2; ++k) dst[m][k] = *(const LAS bf16x8*)(lds + PG8_SA(b, h) + aoff + m * 2048 + k * 1024); } while (0)
; #define PG8_WAIT_V(n) asm volatile("s_waitcnt vmcnt(" #n ")" ::: "memory")
; template <class Epi, class Sched, bool ALIGN_EPI = true, bool SP2 = true, class Side = NoSide>
; __device__ __forceinline__ void gemm_phase(LAS unsigned char* lds, const Gemm g, const Sched& S, const Epi& E, const Side side = Side()) {
;     ...
;         for (int t = 0; t < nt; t += 2) {
;             const bool last = (t == nt - 2);
;             const char* a1 = cA + (size_t)(t + 1) * kstep;
;             const char* a2 = last ? nA : cA + (size_t)(t + 2) * kstep; const char* b2 = last ? nB : cB + (size_t)(t + 2) * kstep;
;             const char* a3 = a2 + kstep; const char* b3 = b2 + kstep;
;             const bool after_epi = Epi::LOADS && t == 0 && ui > 0;
;             if constexpr (SP2) {
;             PG8_LDB(B0, 0, 0); PG8_LDB(B1, 0, 1); PG8_SCHED; PG8_LDA(At, 0, 0); PG8_STAGE(PG8_SA(1, 1), a1 + hstepA, voffA);
;             if (!after_epi) PG8_WAIT_V(8);
;             PG8_WAIT_L(0); PG8_BAR; PG8_MMA(0, 0, At, B0); PG8_MMA(0, 1, At, B1); PG8_BAR; PG8_SCHED;
;             PG8_LDA(At, 0, 1); PG8_STAGE(PG8_SB(0, 0), b2, voffB); PG8_STAGE(PG8_SB(0, 1), b2 + hstepB, voffB); PG8_STAGE(PG8_SA(0, 0), a2, voffA);
;             if (!after_epi) PG8_WAIT_V(8);
;             PG8_WAIT_L(0); PG8_BAR; PG8_MMA(1, 0, At, B0); PG8_MMA(1, 1, At, B1); PG8_BAR; PG8_SCHED;
;             PG8_LDB(B0, 1, 0); PG8_LDB(B1, 1, 1); PG8_SCHED; PG8_LDA(At, 1, 0); PG8_STAGE(PG8_SA(0, 1), a2 + hstepA, voffA);
;             PG8_WAIT_V(8); PG8_WAIT_L(0); PG8_BAR; PG8_MMA(0, 0, At, B0); PG8_MMA(0, 1, At, B1); PG8_BAR; PG8_SCHED;
;             PG8_LDA(At, 1, 1); PG8_STAGE(PG8_SB(1, 0), b3, voffB); PG8_STAGE(PG8_SB(1, 1), b3 + hstepB, voffB); PG8_STAGE(PG8_SA(1, 0), a3, voffA);
;             PG8_WAIT_V(8); PG8_WAIT_L(0); PG8_BAR; PG8_MMA(1, 0, At, B0); PG8_MMA(1, 1, At, B1); PG8_BAR; PG8_SCHED;
	s_add_i32 s46, s48, s51
	v_lshl_add_u64 v[222:223], v[222:223], 0, s[20:21]
	s_mov_b32 m0, s46
	s_nop 0
	global_load_lds_dwordx4 v[222:223], off
	s_add_i32 m0, s46, 0x2000
	s_add_u32 s44, s44, 0x40080
	v_lshl_add_u64 v[220:221], v[220:221], 0, s[20:21]
	s_addc_u32 s45, s45, 0
	s_add_i32 s46, s49, s51
	global_load_lds_dwordx4 v[220:221], off
	v_lshl_add_u64 v[220:221], s[44:45], 0, v[198:199]
	s_mov_b32 m0, s46
	v_lshl_add_u64 v[216:217], v[216:217], 0, s[20:21]
	global_load_lds_dwordx4 v[220:221], off
	v_lshl_add_u64 v[220:221], s[44:45], 0, v[202:203]
	s_add_i32 m0, s46, 0x2000
	s_nop 0
	global_load_lds_dwordx4 v[220:221], off
	s_mov_b32 m0, s63
	s_nop 0
	global_load_lds_dwordx4 v[216:217], off
	v_lshl_add_u64 v[216:217], v[218:219], 0, s[20:21]
	s_mov_b32 m0, s64
	s_nop 0
	global_load_lds_dwordx4 v[216:217], off
	ds_read_b128 v[162:165], v227 offset:49152
	ds_read_b128 v[166:169], v227 offset:50176
	ds_read_b128 v[170:173], v227 offset:51200
	ds_read_b128 v[174:177], v227 offset:52224
	ds_read_b128 v[178:181], v227 offset:53248
	ds_read_b128 v[182:185], v227 offset:54272
	ds_read_b128 v[186:189], v227 offset:55296
	ds_read_b128 v[190:193], v227 offset:56320
	s_waitcnt vmcnt(8)
	s_waitcnt lgkmcnt(0)
	s_barrier
	s_setprio 1
	s_waitcnt lgkmcnt(0)
	v_mfma_i32_16x16x64_i8 v[78:81], v[62:65], v[162:165], v[78:81]
	v_mfma_i32_16x16x64_i8 v[74:77], v[138:141], v[162:165], v[74:77]
	v_mfma_i32_16x16x64_i8 v[46:49], v[62:65], v[170:173], v[46:49]
	v_mfma_i32_16x16x64_i8 v[42:45], v[138:141], v[170:173], v[42:45]
	v_mfma_i32_16x16x64_i8 v[30:33], v[62:65], v[178:181], v[30:33]
	v_mfma_i32_16x16x64_i8 v[26:29], v[138:141], v[178:181], v[26:29]
	v_mfma_i32_16x16x64_i8 v[14:17], v[62:65], v[186:189], v[14:17]
	v_mfma_i32_16x16x64_i8 v[10:13], v[138:141], v[186:189], v[10:13]
	v_mfma_i32_16x16x64_i8 v[78:81], v[66:69], v[166:169], v[78:81]
	v_mfma_i32_16x16x64_i8 v[74:77], v[142:145], v[166:169], v[74:77]
	v_mfma_i32_16x16x64_i8 v[46:49], v[66:69], v[174:177], v[46:49]
	v_mfma_i32_16x16x64_i8 v[42:45], v[142:145], v[174:177], v[42:45]
	v_mfma_i32_16x16x64_i8 v[30:33], v[66:69], v[182:185], v[30:33]
	v_mfma_i32_16x16x64_i8 v[26:29], v[142:145], v[182:185], v[26:29]
	v_mfma_i32_16x16x64_i8 v[14:17], v[66:69], v[190:193], v[14:17]
	v_mfma_i32_16x16x64_i8 v[10:13], v[142:145], v[190:193], v[10:13]
	s_setprio 0
	s_setprio 1
	v_mfma_i32_16x16x64_i8 v[62:65], v[146:149], v[162:165], v[70:73]
	v_mfma_i32_16x16x64_i8 v[58:61], v[154:157], v[162:165], v[58:61]
	v_mfma_i32_16x16x64_i8 v[38:41], v[146:149], v[170:173], v[38:41]
	v_mfma_i32_16x16x64_i8 v[34:37], v[154:157], v[170:173], v[34:37]
	v_mfma_i32_16x16x64_i8 v[22:25], v[146:149], v[178:181], v[22:25]
	v_mfma_i32_16x16x64_i8 v[18:21], v[154:157], v[178:181], v[18:21]
	v_mfma_i32_16x16x64_i8 v[6:9], v[146:149], v[186:189], v[6:9]
	v_mfma_i32_16x16x64_i8 v[2:5], v[154:157], v[186:189], v[2:5]
	v_mfma_i32_16x16x64_i8 v[70:73], v[150:153], v[166:169], v[62:65]
	v_mfma_i32_16x16x64_i8 v[58:61], v[158:161], v[166:169], v[58:61]
	v_mfma_i32_16x16x64_i8 v[38:41], v[150:153], v[174:177], v[38:41]
	v_mfma_i32_16x16x64_i8 v[34:37], v[158:161], v[174:177], v[34:37]
	v_mfma_i32_16x16x64_i8 v[22:25], v[150:153], v[182:185], v[22:25]
	v_mfma_i32_16x16x64_i8 v[18:21], v[158:161], v[182:185], v[18:21]
	v_mfma_i32_16x16x64_i8 v[6:9], v[150:153], v[190:193], v[6:9]
	v_mfma_i32_16x16x64_i8 v[2:5], v[158:161], v[190:193], v[2:5]
	s_setprio 0
	s_barrier
	s_add_i32 s70, s70, 2
	s_add_u32 s42, s42, 0x100
	s_addc_u32 s43, s43, 0
	s_cmp_gt_u32 s70, 13
	s_cbranch_scc1 .LBB0_1028
.LBB0_1024:
	s_cmp_eq_u32 s42, 0
	s_cselect_b64 s[44:45], -1, 0
	v_lshl_add_u64 v[216:217], v[212:213], 0, s[42:43]
	s_add_i32 m0, s37, 0xc000
	s_nop 0
	global_load_lds_dwordx4 v[216:217], off
	v_lshl_add_u64 v[216:217], v[214:215], 0, s[42:43]
	s_add_i32 m0, s37, 0xe000
	s_and_b64 s[44:45], s[40:41], s[44:45]
	global_load_lds_dwordx4 v[216:217], off
	ds_read_b128 v[146:149], v225
	ds_read_b128 v[150:153], v225 offset:1024
	ds_read_b128 v[154:157], v225 offset:2048
	ds_read_b128 v[158:161], v225 offset:3072
	ds_read_b128 v[62:65], v226
	ds_read_b128 v[66:69], v226 offset:1024
	ds_read_b128 v[138:141], v226 offset:2048
	ds_read_b128 v[142:145], v226 offset:3072
	ds_read_b128 v[186:189], v227
	ds_read_b128 v[190:193], v227 offset:1024
	ds_read_b128 v[178:181], v227 offset:2048
	ds_read_b128 v[182:185], v227 offset:3072
	ds_read_b128 v[170:173], v227 offset:4096
	ds_read_b128 v[174:177], v227 offset:5120
	ds_read_b128 v[162:165], v227 offset:6144
	ds_read_b128 v[166:169], v227 offset:7168
	s_and_b64 vcc, exec, s[44:45]
	s_cbranch_vccnz .LBB0_1026
	s_waitcnt vmcnt(8)
; #define PG8_STAGE(bufoff, gbase, voff) do { _Pragma("unroll") for (int _i = 0; _i < 2; ++_i) \
;         __builtin_amdgcn_global_load_lds((const unsigned*)((const char*)(gbase) + (voff)[_i]), (LAS unsigned*)(lds + (bufoff) + ldsw + _i * 8192), 16, 0, 0); } while (0)
; #define PG8_LDA(dst, b, h) do { _Pragma("unroll") for (int m = 0; m < 4; ++m) _Pragma("unroll") for (int k = 0; k < 2; ++k) dst[m][k] = *(const LAS bf16x8*)(lds + PG8_SA(b, h) + aoff + m * 2048 + k * 1024); } while (0)
; #define PG8_LDB(dst, b, h) do { _Pragma("unroll") for (int n = 0; n < 2; ++n) _Pragma("unroll") for (int k = 0; k < 2; ++k) dst[n][k] = *(const LAS bf16x8*)(lds + PG8_SB(b, h) + boff + n * 2048 + k * 1024); } while (0)
; #define PG8_WAIT_V(n) asm volatile("s_waitcnt vmcnt(" #n ")" ::: "memory")
; #define PG8_WAIT_L(n) asm volatile("s_waitcnt lgkmcnt(" #n ")" ::: "memory")
; #define PG8_BAR __builtin_amdgcn_s_barrier()
; #define PG8_SCHED __builtin_amdgcn_sched_barrier(0)
; template <class Epi, class Sched, bool ALIGN_EPI = true, bool SP2 = true, class Side = NoSide>
; __device__ __forceinline__ void gemm_phase(LAS unsigned char* lds, const Gemm g, const Sched& S, const Epi& E, const Side side = Side()) {
;     ...
;             const bool last = (t == nt - 2);
;             const char* a1 = cA + (size_t)(t + 1) * kstep;
;             const char* a2 = last ? nA : cA + (size_t)(t + 2) * kstep; const char* b2 = last ? nB : cB + (size_t)(t + 2) * kstep;
;             const char* a3 = a2 + kstep; const char* b3 = b2 + kstep;
;             const bool after_epi = Epi::LOADS && t == 0 && ui > 0;
;             if constexpr (SP2) {
;             PG8_LDB(B0, 0, 0); PG8_LDB(B1, 0, 1); PG8_SCHED; PG8_LDA(At, 0, 0); PG8_STAGE(PG8_SA(1, 1), a1 + hstepA, voffA);
;             if (!after_epi) PG8_WAIT_V(8);
;             PG8_WAIT_L(0); PG8_BAR; PG8_MMA(0, 0, At, B0); PG8_MMA(0, 1, At, B1); PG8_BAR; PG8_SCHED;
;             PG8_LDA(At, 0, 1); PG8_STAGE(PG8_SB(0, 0), b2, voffB); PG8_STAGE(PG8_SB(0, 1), b2 + hstepB, voffB); PG8_STAGE(PG8_SA(0, 0), a2, voffA);
;             if (!after_epi) PG8_WAIT_V(8);
.LBB0_1026:
	s_xor_b64 s[48:49], s[44:45], -1
	s_add_u32 s44, s38, s42
	s_addc_u32 s45, s39, s43
	s_add_u32 s44, s44, 0x100
	s_addc_u32 s45, s45, 0
	s_add_u32 s71, s68, s42
	s_addc_u32 s72, s69, s43
	s_waitcnt lgkmcnt(0)
	s_cmpk_eq_i32 s42, 0x700
	s_cselect_b32 s47, s27, s45
	s_cselect_b32 s46, s35, s44
	s_cselect_b32 s45, s25, s72
	s_cselect_b32 s44, s67, s71
	s_barrier
	s_setprio 1
	s_waitcnt lgkmcnt(0)
	v_mfma_i32_16x16x64_i8 v[54:57], v[146:149], v[186:189], v[54:57]
	v_mfma_i32_16x16x64_i8 v[50:53], v[154:157], v[186:189], v[50:53]
	v_mfma_i32_16x16x64_i8 v[126:129], v[146:149], v[178:181], v[126:129]
	v_mfma_i32_16x16x64_i8 v[122:125], v[154:157], v[178:181], v[122:125]
	v_mfma_i32_16x16x64_i8 v[110:113], v[146:149], v[170:173], v[110:113]
	v_mfma_i32_16x16x64_i8 v[106:109], v[154:157], v[170:173], v[106:109]
	v_mfma_i32_16x16x64_i8 v[94:97], v[146:149], v[162:165], v[94:97]
	v_mfma_i32_16x16x64_i8 v[90:93], v[154:157], v[162:165], v[90:93]
	v_mfma_i32_16x16x64_i8 v[54:57], v[150:153], v[190:193], v[54:57]
	v_mfma_i32_16x16x64_i8 v[50:53], v[158:161], v[190:193], v[50:53]
	v_mfma_i32_16x16x64_i8 v[126:129], v[150:153], v[182:185], v[126:129]
	v_mfma_i32_16x16x64_i8 v[122:125], v[158:161], v[182:185], v[122:125]
	v_mfma_i32_16x16x64_i8 v[110:113], v[150:153], v[174:177], v[110:113]
	v_mfma_i32_16x16x64_i8 v[106:109], v[158:161], v[174:177], v[106:109]
	v_mfma_i32_16x16x64_i8 v[94:97], v[150:153], v[166:169], v[94:97]
	v_mfma_i32_16x16x64_i8 v[90:93], v[158:161], v[166:169], v[90:93]
	s_setprio 0
	s_setprio 1
	v_mfma_i32_16x16x64_i8 v[134:137], v[62:65], v[186:189], v[134:137]
	v_mfma_i32_16x16x64_i8 v[130:133], v[138:141], v[186:189], v[130:133]
	v_mfma_i32_16x16x64_i8 v[118:121], v[62:65], v[178:181], v[118:121]
	v_mfma_i32_16x16x64_i8 v[114:117], v[138:141], v[178:181], v[114:117]
	v_mfma_i32_16x16x64_i8 v[102:105], v[62:65], v[170:173], v[102:105]
	v_mfma_i32_16x16x64_i8 v[98:101], v[138:141], v[170:173], v[98:101]
	v_mfma_i32_16x16x64_i8 v[86:89], v[62:65], v[162:165], v[86:89]
	v_mfma_i32_16x16x64_i8 v[82:85], v[138:141], v[162:165], v[82:85]
	v_mfma_i32_16x16x64_i8 v[134:137], v[66:69], v[190:193], v[134:137]
	v_mfma_i32_16x16x64_i8 v[130:133], v[142:145], v[190:193], v[130:133]
	v_mfma_i32_16x16x64_i8 v[118:121], v[66:69], v[182:185], v[118:121]
	v_mfma_i32_16x16x64_i8 v[114:117], v[142:145], v[182:185], v[114:117]
	v_mfma_i32_16x16x64_i8 v[102:105], v[66:69], v[174:177], v[102:105]
	v_mfma_i32_16x16x64_i8 v[98:101], v[142:145], v[174:177], v[98:101]
	v_mfma_i32_16x16x64_i8 v[86:89], v[66:69], v[166:169], v[86:89]
	v_mfma_i32_16x16x64_i8 v[82:85], v[142:145], v[166:169], v[82:85]
	s_setprio 0
	s_barrier
	s_mov_b32 m0, s56
	v_lshl_add_u64 v[222:223], s[44:45], 0, v[198:199]
	s_add_u32 s72, s44, 0x40000
	global_load_lds_dwordx4 v[222:223], off
	v_lshl_add_u64 v[220:221], s[44:45], 0, v[202:203]
	s_mov_b32 m0, s57
	s_addc_u32 s73, s45, 0
	global_load_lds_dwordx4 v[220:221], off
	v_lshl_add_u64 v[216:217], s[72:73], 0, v[198:199]
	s_mov_b32 m0, s58
	v_lshl_add_u64 v[218:219], s[46:47], 0, v[200:201]
	global_load_lds_dwordx4 v[216:217], off
	v_lshl_add_u64 v[216:217], s[72:73], 0, v[202:203]
	s_mov_b32 m0, s59
	s_andn2_b64 vcc, exec, s[48:49]
	global_load_lds_dwordx4 v[216:217], off
	v_lshl_add_u64 v[216:217], s[46:47], 0, v[196:197]
	s_mov_b32 m0, s37
	s_nop 0
	global_load_lds_dwordx4 v[216:217], off
	s_mov_b32 m0, s60
	s_nop 0
	global_load_lds_dwordx4 v[218:219], off
	ds_read_b128 v[186:189], v227 offset:16384
	ds_read_b128 v[190:193], v227 offset:17408
	ds_read_b128 v[178:181], v227 offset:18432
	ds_read_b128 v[182:185], v227 offset:19456
	ds_read_b128 v[170:173], v227 offset:20480
	ds_read_b128 v[174:177], v227 offset:21504
	ds_read_b128 v[162:165], v227 offset:22528
	ds_read_b128 v[166:169], v227 offset:23552
	s_cbranch_vccnz .LBB0_1023
	s_waitcnt vmcnt(8)
	s_branch .LBB0_1023

; #define PG8_STAGE(bufoff, gbase, voff) do { _Pragma("unroll") for (int _i = 0; _i < 2; ++_i) \
;         __builtin_amdgcn_global_load_lds((const unsigned*)((const char*)(gbase) + (voff)[_i]), (LAS unsigned*)(lds + (bufoff) + ldsw + _i * 8192), 16, 0, 0); } while (0)
; #define PG8_LDA(dst, b, h) do { _Pragma("unroll") for (int m = 0; m < 4; ++m) _Pragma("unroll") for (int k = 0; k < 2; ++k) dst[m][k] = *(const LAS bf16x8*)(lds + PG8_SA(b, h) + aoff + m * 2048 + k * 1024); } while (0)
; #define PG8_LDB(dst, b, h) do { _Pragma("unroll") for (int n = 0; n < 2; ++n) _Pragma("unroll") for (int k = 0; k < 2; ++k) dst[n][k] = *(const LAS bf16x8*)(lds + PG8_SB(b, h) + boff + n * 2048 + k * 1024); } while (0)
; #define PG8_WAIT_V(n) asm volatile("s_waitcnt vmcnt(" #n ")" ::: "memory")
; #define PG8_WAIT_L(n) asm volatile("s_waitcnt lgkmcnt(" #n ")" ::: "memory")
; #define PG8_BAR __builtin_amdgcn_s_barrier()
; #define PG8_SCHED __builtin_amdgcn_sched_barrier(0)
; template <class Epi, class Sched, bool ALIGN_EPI = true, bool SP2 = true, class Side = NoSide>
; __device__ __forceinline__ void gemm_phase(LAS unsigned char* lds, const Gemm g, const Sched& S, const Epi& E, const Side side = Side()) {
;     ...
;             PG8_LDA(At, 0, 1); PG8_STAGE(PG8_SB(0, 0), b2, voffB); PG8_STAGE(PG8_SB(0, 1), b2 + hstepB, voffB); PG8_STAGE(PG8_SA(0, 0), a2, voffA);
;             if (!after_epi) PG8_WAIT_V(8);
;             PG8_WAIT_L(0); PG8_BAR; PG8_MMA(1, 0, At, B0); PG8_MMA(1, 1, At, B1); PG8_BAR; PG8_SCHED;
;             PG8_LDB(B0, 1, 0); PG8_LDB(B1, 1, 1); PG8_SCHED; PG8_LDA(At, 1, 0); PG8_STAGE(PG8_SA(0, 1), a2 + hstepA, voffA);
;             PG8_WAIT_V(8); PG8_WAIT_L(0); PG8_BAR; PG8_MMA(0, 0, At, B0); PG8_MMA(0, 1, At, B1); PG8_BAR; PG8_SCHED;
.LBB0_1181:
	s_waitcnt lgkmcnt(0)
	s_barrier
	s_setprio 1
	s_waitcnt lgkmcnt(0)
	v_mfma_i32_16x16x64_i8 v[62:65], v[146:149], v[186:189], v[62:65]
	v_mfma_i32_16x16x64_i8 v[58:61], v[154:157], v[186:189], v[58:61]
	v_mfma_i32_16x16x64_i8 v[46:49], v[146:149], v[178:181], v[46:49]
	v_mfma_i32_16x16x64_i8 v[42:45], v[154:157], v[178:181], v[42:45]
	v_mfma_i32_16x16x64_i8 v[30:33], v[146:149], v[170:173], v[30:33]
	v_mfma_i32_16x16x64_i8 v[26:29], v[154:157], v[170:173], v[26:29]
	v_mfma_i32_16x16x64_i8 v[14:17], v[146:149], v[162:165], v[14:17]
	v_mfma_i32_16x16x64_i8 v[10:13], v[154:157], v[162:165], v[10:13]
	v_mfma_i32_16x16x64_i8 v[62:65], v[150:153], v[190:193], v[62:65]
	v_mfma_i32_16x16x64_i8 v[58:61], v[158:161], v[190:193], v[58:61]
	v_mfma_i32_16x16x64_i8 v[46:49], v[150:153], v[182:185], v[46:49]
	v_mfma_i32_16x16x64_i8 v[42:45], v[158:161], v[182:185], v[42:45]
	v_mfma_i32_16x16x64_i8 v[30:33], v[150:153], v[174:177], v[30:33]
	v_mfma_i32_16x16x64_i8 v[26:29], v[158:161], v[174:177], v[26:29]
	v_mfma_i32_16x16x64_i8 v[14:17], v[150:153], v[166:169], v[14:17]
	v_mfma_i32_16x16x64_i8 v[10:13], v[158:161], v[166:169], v[10:13]
	s_setprio 0
	s_setprio 1
	v_mfma_i32_16x16x64_i8 v[54:57], v[106:109], v[186:189], v[54:57]
	v_mfma_i32_16x16x64_i8 v[50:53], v[122:125], v[186:189], v[50:53]
	v_mfma_i32_16x16x64_i8 v[38:41], v[106:109], v[178:181], v[38:41]
	v_mfma_i32_16x16x64_i8 v[34:37], v[122:125], v[178:181], v[34:37]
	v_mfma_i32_16x16x64_i8 v[22:25], v[106:109], v[170:173], v[22:25]
	v_mfma_i32_16x16x64_i8 v[18:21], v[122:125], v[170:173], v[18:21]
	v_mfma_i32_16x16x64_i8 v[6:9], v[106:109], v[162:165], v[6:9]
	v_mfma_i32_16x16x64_i8 v[2:5], v[122:125], v[162:165], v[2:5]
	v_mfma_i32_16x16x64_i8 v[54:57], v[110:113], v[190:193], v[54:57]
	v_mfma_i32_16x16x64_i8 v[50:53], v[126:129], v[190:193], v[50:53]
	v_mfma_i32_16x16x64_i8 v[38:41], v[110:113], v[182:185], v[38:41]
	v_mfma_i32_16x16x64_i8 v[34:37], v[126:129], v[182:185], v[34:37]
	v_mfma_i32_16x16x64_i8 v[22:25], v[110:113], v[174:177], v[22:25]
	v_mfma_i32_16x16x64_i8 v[18:21], v[126:129], v[174:177], v[18:21]
	v_mfma_i32_16x16x64_i8 v[6:9], v[110:113], v[166:169], v[6:9]
	v_mfma_i32_16x16x64_i8 v[2:5], v[126:129], v[166:169], v[2:5]
	s_setprio 0
	s_barrier
	s_add_i32 s40, 0, 0x18000
	s_add_i32 s41, 0, 0x1c000
	v_add_u32_e32 v126, s40, v195
	v_add_u32_e32 v158, s41, v195
	s_add_u32 s38, s38, 0x80000
	s_addc_u32 s39, s39, 0
	s_mov_b32 m0, s52
	v_lshl_add_u64 v[228:229], s[38:39], 0, v[196:197]
	global_load_lds_dwordx4 v[228:229], off
	v_lshl_add_u64 v[228:229], s[38:39], 0, v[200:201]
	s_mov_b32 m0, s53
	s_nop 0
	global_load_lds_dwordx4 v[228:229], off
	ds_read_b128 v[106:109], v126
	ds_read_b128 v[110:113], v126 offset:1024
	ds_read_b128 v[122:125], v126 offset:2048
	ds_read_b128 v[126:129], v126 offset:3072
	ds_read_b128 v[146:149], v158
	ds_read_b128 v[150:153], v158 offset:1024
	ds_read_b128 v[154:157], v158 offset:2048
	ds_read_b128 v[158:161], v158 offset:3072
	ds_read_b128 v[162:165], v227 offset:32768
	ds_read_b128 v[166:169], v227 offset:33792
	ds_read_b128 v[170:173], v227 offset:34816
	ds_read_b128 v[174:177], v227 offset:35840
	ds_read_b128 v[178:181], v227 offset:36864
	ds_read_b128 v[182:185], v227 offset:37888
	ds_read_b128 v[186:189], v227 offset:38912
	ds_read_b128 v[190:193], v227 offset:39936
	s_waitcnt vmcnt(8)
	s_waitcnt lgkmcnt(0)
	s_barrier
	s_setprio 1
	s_waitcnt lgkmcnt(0)
	v_mfma_i32_16x16x64_i8 v[142:145], v[106:109], v[162:165], v[142:145]
	v_mfma_i32_16x16x64_i8 v[138:141], v[122:125], v[162:165], v[138:141]
	v_mfma_i32_16x16x64_i8 v[118:121], v[106:109], v[170:173], v[118:121]
	v_mfma_i32_16x16x64_i8 v[114:117], v[122:125], v[170:173], v[114:117]
	v_mfma_i32_16x16x64_i8 v[94:97], v[106:109], v[178:181], v[94:97]
	v_mfma_i32_16x16x64_i8 v[90:93], v[122:125], v[178:181], v[90:93]
	v_mfma_i32_16x16x64_i8 v[78:81], v[106:109], v[186:189], v[78:81]
	v_mfma_i32_16x16x64_i8 v[74:77], v[122:125], v[186:189], v[74:77]
	v_mfma_i32_16x16x64_i8 v[142:145], v[110:113], v[166:169], v[142:145]
	v_mfma_i32_16x16x64_i8 v[138:141], v[126:129], v[166:169], v[138:141]
	v_mfma_i32_16x16x64_i8 v[118:121], v[110:113], v[174:177], v[118:121]
	v_mfma_i32_16x16x64_i8 v[114:117], v[126:129], v[174:177], v[114:117]
	v_mfma_i32_16x16x64_i8 v[94:97], v[110:113], v[182:185], v[94:97]
	v_mfma_i32_16x16x64_i8 v[90:93], v[126:129], v[182:185], v[90:93]
	v_mfma_i32_16x16x64_i8 v[78:81], v[110:113], v[190:193], v[78:81]
	v_mfma_i32_16x16x64_i8 v[74:77], v[126:129], v[190:193], v[74:77]
	s_setprio 0
	s_setprio 1
	v_mfma_i32_16x16x64_i8 v[134:137], v[146:149], v[162:165], v[134:137]
	v_mfma_i32_16x16x64_i8 v[130:133], v[154:157], v[162:165], v[130:133]
	v_mfma_i32_16x16x64_i8 v[102:105], v[146:149], v[170:173], v[102:105]
	v_mfma_i32_16x16x64_i8 v[98:101], v[154:157], v[170:173], v[98:101]
	v_mfma_i32_16x16x64_i8 v[86:89], v[146:149], v[178:181], v[86:89]
	v_mfma_i32_16x16x64_i8 v[82:85], v[154:157], v[178:181], v[82:85]
	v_mfma_i32_16x16x64_i8 v[70:73], v[146:149], v[186:189], v[70:73]
	v_mfma_i32_16x16x64_i8 v[66:69], v[154:157], v[186:189], v[66:69]
	v_mfma_i32_16x16x64_i8 v[134:137], v[150:153], v[166:169], v[134:137]
	v_mfma_i32_16x16x64_i8 v[130:133], v[158:161], v[166:169], v[130:133]
	v_mfma_i32_16x16x64_i8 v[102:105], v[150:153], v[174:177], v[102:105]
	v_mfma_i32_16x16x64_i8 v[98:101], v[158:161], v[174:177], v[98:101]
	v_mfma_i32_16x16x64_i8 v[86:89], v[150:153], v[182:185], v[86:89]
	v_mfma_i32_16x16x64_i8 v[82:85], v[158:161], v[182:185], v[82:85]
	v_mfma_i32_16x16x64_i8 v[70:73], v[150:153], v[190:193], v[70:73]
	v_mfma_i32_16x16x64_i8 v[66:69], v[158:161], v[190:193], v[66:69]
	s_setprio 0
	s_barrier
; #define PG8_STAGE(bufoff, gbase, voff) do { _Pragma("unroll") for (int _i = 0; _i < 2; ++_i) \
;         __builtin_amdgcn_global_load_lds((const unsigned*)((const char*)(gbase) + (voff)[_i]), (LAS unsigned*)(lds + (bufoff) + ldsw + _i * 8192), 16, 0, 0); } while (0)
; #define PG8_LDA(dst, b, h) do { _Pragma("unroll") for (int m = 0; m < 4; ++m) _Pragma("unroll") for (int k = 0; k < 2; ++k) dst[m][k] = *(const LAS bf16x8*)(lds + PG8_SA(b, h) + aoff + m * 2048 + k * 1024); } while (0)
; #define PG8_WAIT_V(n) asm volatile("s_waitcnt vmcnt(" #n ")" ::: "memory")
; template <class Epi, class Sched, bool ALIGN_EPI = true, bool SP2 = true, class Side = NoSide>
; __device__ __forceinline__ void gemm_phase(LAS unsigned char* lds, const Gemm g, const Sched& S, const Epi& E, const Side side = Side()) {
;     ...
;         for (int t = 0; t < nt; t += 2) {
;             const bool last = (t == nt - 2);
;             const char* a1 = cA + (size_t)(t + 1) * kstep;
;             const char* a2 = last ? nA : cA + (size_t)(t + 2) * kstep; const char* b2 = last ? nB : cB + (size_t)(t + 2) * kstep;
;             const char* a3 = a2 + kstep; const char* b3 = b2 + kstep;
;             const bool after_epi = Epi::LOADS && t == 0 && ui > 0;
;             if constexpr (SP2) {
;             PG8_LDB(B0, 0, 0); PG8_LDB(B1, 0, 1); PG8_SCHED; PG8_LDA(At, 0, 0); PG8_STAGE(PG8_SA(1, 1), a1 + hstepA, voffA);
;             if (!after_epi) PG8_WAIT_V(8);
;             PG8_WAIT_L(0); PG8_BAR; PG8_MMA(0, 0, At, B0); PG8_MMA(0, 1, At, B1); PG8_BAR; PG8_SCHED;
;             PG8_LDA(At, 0, 1); PG8_STAGE(PG8_SB(0, 0), b2, voffB); PG8_STAGE(PG8_SB(0, 1), b2 + hstepB, voffB); PG8_STAGE(PG8_SA(0, 0), a2, voffA);
;             if (!after_epi) PG8_WAIT_V(8);
;             PG8_WAIT_L(0); PG8_BAR; PG8_MMA(1, 0, At, B0); PG8_MMA(1, 1, At, B1); PG8_BAR; PG8_SCHED;
;             PG8_LDB(B0, 1, 0); PG8_LDB(B1, 1, 1); PG8_SCHED; PG8_LDA(At, 1, 0); PG8_STAGE(PG8_SA(0, 1), a2 + hstepA, voffA);
;             PG8_WAIT_V(8); PG8_WAIT_L(0); PG8_BAR; PG8_MMA(0, 0, At, B0); PG8_MMA(0, 1, At, B1); PG8_BAR; PG8_SCHED;
;             PG8_LDA(At, 1, 1); PG8_STAGE(PG8_SB(1, 0), b3, voffB); PG8_STAGE(PG8_SB(1, 1), b3 + hstepB, voffB); PG8_STAGE(PG8_SA(1, 0), a3, voffA);
;             PG8_WAIT_V(8); PG8_WAIT_L(0); PG8_BAR; PG8_MMA(1, 0, At, B0); PG8_MMA(1, 1, At, B1); PG8_BAR; PG8_SCHED;
	s_add_i32 s38, s40, s45
	v_lshl_add_u64 v[222:223], v[222:223], 0, s[12:13]
	s_mov_b32 m0, s38
	s_nop 0
	global_load_lds_dwordx4 v[222:223], off
	s_add_i32 m0, s38, 0x2000
	s_add_u32 s36, s36, 0x80080
	v_lshl_add_u64 v[220:221], v[220:221], 0, s[12:13]
	s_addc_u32 s37, s37, 0
	s_add_i32 s38, s41, s45
	global_load_lds_dwordx4 v[220:221], off
	v_lshl_add_u64 v[220:221], s[36:37], 0, v[198:199]
	s_mov_b32 m0, s38
	v_lshl_add_u64 v[216:217], v[216:217], 0, s[12:13]
	global_load_lds_dwordx4 v[220:221], off
	v_lshl_add_u64 v[220:221], s[36:37], 0, v[202:203]
	s_add_i32 m0, s38, 0x2000
	s_nop 0
	global_load_lds_dwordx4 v[220:221], off
	s_mov_b32 m0, s55
	s_nop 0
	global_load_lds_dwordx4 v[216:217], off
	v_lshl_add_u64 v[216:217], v[218:219], 0, s[12:13]
	s_mov_b32 m0, s56
	s_nop 0
	global_load_lds_dwordx4 v[216:217], off
	ds_read_b128 v[162:165], v227 offset:49152
	ds_read_b128 v[166:169], v227 offset:50176
	ds_read_b128 v[170:173], v227 offset:51200
	ds_read_b128 v[174:177], v227 offset:52224
	ds_read_b128 v[178:181], v227 offset:53248
	ds_read_b128 v[182:185], v227 offset:54272
	ds_read_b128 v[186:189], v227 offset:55296
	ds_read_b128 v[190:193], v227 offset:56320
	s_waitcnt vmcnt(8)
	s_waitcnt lgkmcnt(0)
	s_barrier
	s_setprio 1
	s_waitcnt lgkmcnt(0)
	v_mfma_i32_16x16x64_i8 v[62:65], v[106:109], v[162:165], v[62:65]
	v_mfma_i32_16x16x64_i8 v[58:61], v[122:125], v[162:165], v[58:61]
	v_mfma_i32_16x16x64_i8 v[46:49], v[106:109], v[170:173], v[46:49]
	v_mfma_i32_16x16x64_i8 v[42:45], v[122:125], v[170:173], v[42:45]
	v_mfma_i32_16x16x64_i8 v[30:33], v[106:109], v[178:181], v[30:33]
	v_mfma_i32_16x16x64_i8 v[26:29], v[122:125], v[178:181], v[26:29]
	v_mfma_i32_16x16x64_i8 v[14:17], v[106:109], v[186:189], v[14:17]
	v_mfma_i32_16x16x64_i8 v[10:13], v[122:125], v[186:189], v[10:13]
	v_mfma_i32_16x16x64_i8 v[62:65], v[110:113], v[166:169], v[62:65]
	v_mfma_i32_16x16x64_i8 v[58:61], v[126:129], v[166:169], v[58:61]
	v_mfma_i32_16x16x64_i8 v[46:49], v[110:113], v[174:177], v[46:49]
	v_mfma_i32_16x16x64_i8 v[42:45], v[126:129], v[174:177], v[42:45]
	v_mfma_i32_16x16x64_i8 v[30:33], v[110:113], v[182:185], v[30:33]
	v_mfma_i32_16x16x64_i8 v[26:29], v[126:129], v[182:185], v[26:29]
	v_mfma_i32_16x16x64_i8 v[14:17], v[110:113], v[190:193], v[14:17]
	v_mfma_i32_16x16x64_i8 v[10:13], v[126:129], v[190:193], v[10:13]
	s_setprio 0
	s_setprio 1
	v_mfma_i32_16x16x64_i8 v[54:57], v[146:149], v[162:165], v[54:57]
	v_mfma_i32_16x16x64_i8 v[50:53], v[154:157], v[162:165], v[50:53]
	v_mfma_i32_16x16x64_i8 v[38:41], v[146:149], v[170:173], v[38:41]
	v_mfma_i32_16x16x64_i8 v[34:37], v[154:157], v[170:173], v[34:37]
	v_mfma_i32_16x16x64_i8 v[22:25], v[146:149], v[178:181], v[22:25]
	v_mfma_i32_16x16x64_i8 v[18:21], v[154:157], v[178:181], v[18:21]
	v_mfma_i32_16x16x64_i8 v[6:9], v[146:149], v[186:189], v[6:9]
	v_mfma_i32_16x16x64_i8 v[2:5], v[154:157], v[186:189], v[2:5]
	v_mfma_i32_16x16x64_i8 v[54:57], v[150:153], v[166:169], v[54:57]
	v_mfma_i32_16x16x64_i8 v[50:53], v[158:161], v[166:169], v[50:53]
	v_mfma_i32_16x16x64_i8 v[38:41], v[150:153], v[174:177], v[38:41]
	v_mfma_i32_16x16x64_i8 v[34:37], v[158:161], v[174:177], v[34:37]
	v_mfma_i32_16x16x64_i8 v[22:25], v[150:153], v[182:185], v[22:25]
	v_mfma_i32_16x16x64_i8 v[18:21], v[158:161], v[182:185], v[18:21]
	v_mfma_i32_16x16x64_i8 v[6:9], v[150:153], v[190:193], v[6:9]
	v_mfma_i32_16x16x64_i8 v[2:5], v[158:161], v[190:193], v[2:5]
	s_setprio 0
	s_barrier
	s_add_i32 s63, s63, 2
	s_add_u32 s34, s34, 0x100
	s_addc_u32 s35, s35, 0
	s_cmp_gt_u32 s63, 29
	s_cbranch_scc1 .LBB0_1186
.LBB0_1182:
	s_cmp_eq_u32 s34, 0
	s_cselect_b64 s[36:37], -1, 0
	v_lshl_add_u64 v[216:217], v[212:213], 0, s[34:35]
	s_add_i32 m0, s27, 0xc000
	s_nop 0
	global_load_lds_dwordx4 v[216:217], off
	v_lshl_add_u64 v[216:217], v[214:215], 0, s[34:35]
	s_add_i32 m0, s27, 0xe000
	s_and_b64 s[36:37], s[30:31], s[36:37]
	global_load_lds_dwordx4 v[216:217], off
	ds_read_b128 v[146:149], v225
	ds_read_b128 v[150:153], v225 offset:1024
	ds_read_b128 v[154:157], v225 offset:2048
	ds_read_b128 v[158:161], v225 offset:3072
	ds_read_b128 v[106:109], v226
	ds_read_b128 v[110:113], v226 offset:1024
	ds_read_b128 v[122:125], v226 offset:2048
	ds_read_b128 v[126:129], v226 offset:3072
	ds_read_b128 v[186:189], v227
	ds_read_b128 v[190:193], v227 offset:1024
	ds_read_b128 v[178:181], v227 offset:2048
	ds_read_b128 v[182:185], v227 offset:3072
	ds_read_b128 v[170:173], v227 offset:4096
	ds_read_b128 v[174:177], v227 offset:5120
	ds_read_b128 v[162:165], v227 offset:6144
	ds_read_b128 v[166:169], v227 offset:7168
	s_and_b64 vcc, exec, s[36:37]
	s_cbranch_vccnz .LBB0_1184
	s_waitcnt vmcnt(8)
; #define PG8_STAGE(bufoff, gbase, voff) do { _Pragma("unroll") for (int _i = 0; _i < 2; ++_i) \
;         __builtin_amdgcn_global_load_lds((const unsigned*)((const char*)(gbase) + (voff)[_i]), (LAS unsigned*)(lds + (bufoff) + ldsw + _i * 8192), 16, 0, 0); } while (0)
; #define PG8_LDA(dst, b, h) do { _Pragma("unroll") for (int m = 0; m < 4; ++m) _Pragma("unroll") for (int k = 0; k < 2; ++k) dst[m][k] = *(const LAS bf16x8*)(lds + PG8_SA(b, h) + aoff + m * 2048 + k * 1024); } while (0)
; #define PG8_LDB(dst, b, h) do { _Pragma("unroll") for (int n = 0; n < 2; ++n) _Pragma("unroll") for (int k = 0; k < 2; ++k) dst[n][k] = *(const LAS bf16x8*)(lds + PG8_SB(b, h) + boff + n * 2048 + k * 1024); } while (0)
; #define PG8_WAIT_V(n) asm volatile("s_waitcnt vmcnt(" #n ")" ::: "memory")
; #define PG8_WAIT_L(n) asm volatile("s_waitcnt lgkmcnt(" #n ")" ::: "memory")
; #define PG8_BAR __builtin_amdgcn_s_barrier()
; #define PG8_SCHED __builtin_amdgcn_sched_barrier(0)
; template <class Epi, class Sched, bool ALIGN_EPI = true, bool SP2 = true, class Side = NoSide>
; __device__ __forceinline__ void gemm_phase(LAS unsigned char* lds, const Gemm g, const Sched& S, const Epi& E, const Side side = Side()) {
;     ...
;             const bool last = (t == nt - 2);
;             const char* a1 = cA + (size_t)(t + 1) * kstep;
;             const char* a2 = last ? nA : cA + (size_t)(t + 2) * kstep; const char* b2 = last ? nB : cB + (size_t)(t + 2) * kstep;
;             const char* a3 = a2 + kstep; const char* b3 = b2 + kstep;
;             const bool after_epi = Epi::LOADS && t == 0 && ui > 0;
;             if constexpr (SP2) {
;             PG8_LDB(B0, 0, 0); PG8_LDB(B1, 0, 1); PG8_SCHED; PG8_LDA(At, 0, 0); PG8_STAGE(PG8_SA(1, 1), a1 + hstepA, voffA);
;             if (!after_epi) PG8_WAIT_V(8);
;             PG8_WAIT_L(0); PG8_BAR; PG8_MMA(0, 0, At, B0); PG8_MMA(0, 1, At, B1); PG8_BAR; PG8_SCHED;
;             PG8_LDA(At, 0, 1); PG8_STAGE(PG8_SB(0, 0), b2, voffB); PG8_STAGE(PG8_SB(0, 1), b2 + hstepB, voffB); PG8_STAGE(PG8_SA(0, 0), a2, voffA);
;             if (!after_epi) PG8_WAIT_V(8);
.LBB0_1184:
	s_xor_b64 s[40:41], s[36:37], -1
	s_add_u32 s36, s28, s34
	s_addc_u32 s37, s29, s35
	s_add_u32 s36, s36, 0x100
	s_addc_u32 s37, s37, 0
	s_add_u32 s64, s61, s34
	s_addc_u32 s65, s62, s35
	s_waitcnt lgkmcnt(0)
	s_cmpk_eq_i32 s34, 0xf00
	s_cselect_b32 s39, s21, s37
	s_cselect_b32 s38, s59, s36
	s_cselect_b32 s37, s17, s65
	s_cselect_b32 s36, s60, s64
	s_barrier
	s_setprio 1
	s_waitcnt lgkmcnt(0)
	v_mfma_i32_16x16x64_i8 v[142:145], v[146:149], v[186:189], v[142:145]
	v_mfma_i32_16x16x64_i8 v[138:141], v[154:157], v[186:189], v[138:141]
	v_mfma_i32_16x16x64_i8 v[118:121], v[146:149], v[178:181], v[118:121]
	v_mfma_i32_16x16x64_i8 v[114:117], v[154:157], v[178:181], v[114:117]
	v_mfma_i32_16x16x64_i8 v[94:97], v[146:149], v[170:173], v[94:97]
	v_mfma_i32_16x16x64_i8 v[90:93], v[154:157], v[170:173], v[90:93]
	v_mfma_i32_16x16x64_i8 v[78:81], v[146:149], v[162:165], v[78:81]
	v_mfma_i32_16x16x64_i8 v[74:77], v[154:157], v[162:165], v[74:77]
	v_mfma_i32_16x16x64_i8 v[142:145], v[150:153], v[190:193], v[142:145]
	v_mfma_i32_16x16x64_i8 v[138:141], v[158:161], v[190:193], v[138:141]
	v_mfma_i32_16x16x64_i8 v[118:121], v[150:153], v[182:185], v[118:121]
	v_mfma_i32_16x16x64_i8 v[114:117], v[158:161], v[182:185], v[114:117]
	v_mfma_i32_16x16x64_i8 v[94:97], v[150:153], v[174:177], v[94:97]
	v_mfma_i32_16x16x64_i8 v[90:93], v[158:161], v[174:177], v[90:93]
	v_mfma_i32_16x16x64_i8 v[78:81], v[150:153], v[166:169], v[78:81]
	v_mfma_i32_16x16x64_i8 v[74:77], v[158:161], v[166:169], v[74:77]
	s_setprio 0
	s_setprio 1
	v_mfma_i32_16x16x64_i8 v[134:137], v[106:109], v[186:189], v[134:137]
	v_mfma_i32_16x16x64_i8 v[130:133], v[122:125], v[186:189], v[130:133]
	v_mfma_i32_16x16x64_i8 v[102:105], v[106:109], v[178:181], v[102:105]
	v_mfma_i32_16x16x64_i8 v[98:101], v[122:125], v[178:181], v[98:101]
	v_mfma_i32_16x16x64_i8 v[86:89], v[106:109], v[170:173], v[86:89]
	v_mfma_i32_16x16x64_i8 v[82:85], v[122:125], v[170:173], v[82:85]
	v_mfma_i32_16x16x64_i8 v[70:73], v[106:109], v[162:165], v[70:73]
	v_mfma_i32_16x16x64_i8 v[66:69], v[122:125], v[162:165], v[66:69]
	v_mfma_i32_16x16x64_i8 v[134:137], v[110:113], v[190:193], v[134:137]
	v_mfma_i32_16x16x64_i8 v[130:133], v[126:129], v[190:193], v[130:133]
	v_mfma_i32_16x16x64_i8 v[102:105], v[110:113], v[182:185], v[102:105]
	v_mfma_i32_16x16x64_i8 v[98:101], v[126:129], v[182:185], v[98:101]
	v_mfma_i32_16x16x64_i8 v[86:89], v[110:113], v[174:177], v[86:89]
	v_mfma_i32_16x16x64_i8 v[82:85], v[126:129], v[174:177], v[82:85]
	v_mfma_i32_16x16x64_i8 v[70:73], v[110:113], v[166:169], v[70:73]
	v_mfma_i32_16x16x64_i8 v[66:69], v[126:129], v[166:169], v[66:69]
	s_setprio 0
	s_barrier
	s_mov_b32 m0, s47
	v_lshl_add_u64 v[222:223], s[36:37], 0, v[198:199]
	s_add_u32 s64, s36, 0x80000
	global_load_lds_dwordx4 v[222:223], off
	v_lshl_add_u64 v[220:221], s[36:37], 0, v[202:203]
	s_mov_b32 m0, s48
	s_addc_u32 s65, s37, 0
	global_load_lds_dwordx4 v[220:221], off
	v_lshl_add_u64 v[216:217], s[64:65], 0, v[198:199]
	s_mov_b32 m0, s49
	v_lshl_add_u64 v[218:219], s[38:39], 0, v[200:201]
	global_load_lds_dwordx4 v[216:217], off
	v_lshl_add_u64 v[216:217], s[64:65], 0, v[202:203]
	s_mov_b32 m0, s50
	s_andn2_b64 vcc, exec, s[40:41]
	global_load_lds_dwordx4 v[216:217], off
	v_lshl_add_u64 v[216:217], s[38:39], 0, v[196:197]
	s_mov_b32 m0, s27
	s_nop 0
	global_load_lds_dwordx4 v[216:217], off
	s_mov_b32 m0, s51
	s_nop 0
	global_load_lds_dwordx4 v[218:219], off
	ds_read_b128 v[186:189], v227 offset:16384
	ds_read_b128 v[190:193], v227 offset:17408
	ds_read_b128 v[178:181], v227 offset:18432
	ds_read_b128 v[182:185], v227 offset:19456
	ds_read_b128 v[170:173], v227 offset:20480
	ds_read_b128 v[174:177], v227 offset:21504
	ds_read_b128 v[162:165], v227 offset:22528
	ds_read_b128 v[166:169], v227 offset:23552
	s_cbranch_vccnz .LBB0_1181
	s_waitcnt vmcnt(8)
	s_branch .LBB0_1181

; #define PG8_STAGE(bufoff, gbase, voff) do { _Pragma("unroll") for (int _i = 0; _i < 2; ++_i) \
;         __builtin_amdgcn_global_load_lds((const unsigned*)((const char*)(gbase) + (voff)[_i]), (LAS unsigned*)(lds + (bufoff) + ldsw + _i * 8192), 16, 0, 0); } while (0)
; #define PG8_LDA(dst, b, h) do { _Pragma("unroll") for (int m = 0; m < 4; ++m) _Pragma("unroll") for (int k = 0; k < 2; ++k) dst[m][k] = *(const LAS bf16x8*)(lds + PG8_SA(b, h) + aoff + m * 2048 + k * 1024); } while (0)
; #define PG8_LDB(dst, b, h) do { _Pragma("unroll") for (int n = 0; n < 2; ++n) _Pragma("unroll") for (int k = 0; k < 2; ++k) dst[n][k] = *(const LAS bf16x8*)(lds + PG8_SB(b, h) + boff + n * 2048 + k * 1024); } while (0)
; #define PG8_WAIT_V(n) asm volatile("s_waitcnt vmcnt(" #n ")" ::: "memory")
; #define PG8_WAIT_L(n) asm volatile("s_waitcnt lgkmcnt(" #n ")" ::: "memory")
; #define PG8_BAR __builtin_amdgcn_s_barrier()
; #define PG8_SCHED __builtin_amdgcn_sched_barrier(0)
; template <class Epi, class Sched, bool ALIGN_EPI = true, bool SP2 = true, class Side = NoSide>
; __device__ __forceinline__ void gemm_phase(LAS unsigned char* lds, const Gemm g, const Sched& S, const Epi& E, const Side side = Side()) {
;     ...
;             PG8_LDA(At, 0, 1); PG8_STAGE(PG8_SB(0, 0), b2, voffB); PG8_STAGE(PG8_SB(0, 1), b2 + hstepB, voffB); PG8_STAGE(PG8_SA(0, 0), a2, voffA);
;             if (!after_epi) PG8_WAIT_V(8);
;             PG8_WAIT_L(0); PG8_BAR; PG8_MMA(1, 0, At, B0); PG8_MMA(1, 1, At, B1); PG8_BAR; PG8_SCHED;
;             PG8_LDB(B0, 1, 0); PG8_LDB(B1, 1, 1); PG8_SCHED; PG8_LDA(At, 1, 0); PG8_STAGE(PG8_SA(0, 1), a2 + hstepA, voffA);
;             PG8_WAIT_V(8); PG8_WAIT_L(0); PG8_BAR; PG8_MMA(0, 0, At, B0); PG8_MMA(0, 1, At, B1); PG8_BAR; PG8_SCHED;
.LBB0_1325:
	s_waitcnt lgkmcnt(0)
	s_barrier
	s_setprio 1
	s_waitcnt lgkmcnt(0)
	v_mfma_i32_16x16x64_i8 v[62:65], v[146:149], v[186:189], v[62:65]
	v_mfma_i32_16x16x64_i8 v[58:61], v[154:157], v[186:189], v[58:61]
	v_mfma_i32_16x16x64_i8 v[46:49], v[146:149], v[178:181], v[46:49]
	v_mfma_i32_16x16x64_i8 v[42:45], v[154:157], v[178:181], v[42:45]
	v_mfma_i32_16x16x64_i8 v[30:33], v[146:149], v[170:173], v[30:33]
	v_mfma_i32_16x16x64_i8 v[26:29], v[154:157], v[170:173], v[26:29]
	v_mfma_i32_16x16x64_i8 v[14:17], v[146:149], v[162:165], v[14:17]
	v_mfma_i32_16x16x64_i8 v[10:13], v[154:157], v[162:165], v[10:13]
	v_mfma_i32_16x16x64_i8 v[62:65], v[150:153], v[190:193], v[62:65]
	v_mfma_i32_16x16x64_i8 v[58:61], v[158:161], v[190:193], v[58:61]
	v_mfma_i32_16x16x64_i8 v[46:49], v[150:153], v[182:185], v[46:49]
	v_mfma_i32_16x16x64_i8 v[42:45], v[158:161], v[182:185], v[42:45]
	v_mfma_i32_16x16x64_i8 v[30:33], v[150:153], v[174:177], v[30:33]
	v_mfma_i32_16x16x64_i8 v[26:29], v[158:161], v[174:177], v[26:29]
	v_mfma_i32_16x16x64_i8 v[14:17], v[150:153], v[166:169], v[14:17]
	v_mfma_i32_16x16x64_i8 v[10:13], v[158:161], v[166:169], v[10:13]
	s_setprio 0
	s_setprio 1
	v_mfma_i32_16x16x64_i8 v[54:57], v[114:117], v[186:189], v[54:57]
	v_mfma_i32_16x16x64_i8 v[50:53], v[130:133], v[186:189], v[50:53]
	v_mfma_i32_16x16x64_i8 v[38:41], v[114:117], v[178:181], v[38:41]
	v_mfma_i32_16x16x64_i8 v[34:37], v[130:133], v[178:181], v[34:37]
	v_mfma_i32_16x16x64_i8 v[22:25], v[114:117], v[170:173], v[22:25]
	v_mfma_i32_16x16x64_i8 v[18:21], v[130:133], v[170:173], v[18:21]
	v_mfma_i32_16x16x64_i8 v[6:9], v[114:117], v[162:165], v[6:9]
	v_mfma_i32_16x16x64_i8 v[2:5], v[130:133], v[162:165], v[2:5]
	v_mfma_i32_16x16x64_i8 v[54:57], v[122:125], v[190:193], v[54:57]
	v_mfma_i32_16x16x64_i8 v[50:53], v[134:137], v[190:193], v[50:53]
	v_mfma_i32_16x16x64_i8 v[38:41], v[122:125], v[182:185], v[38:41]
	v_mfma_i32_16x16x64_i8 v[34:37], v[134:137], v[182:185], v[34:37]
	v_mfma_i32_16x16x64_i8 v[22:25], v[122:125], v[174:177], v[22:25]
	v_mfma_i32_16x16x64_i8 v[18:21], v[134:137], v[174:177], v[18:21]
	v_mfma_i32_16x16x64_i8 v[6:9], v[122:125], v[166:169], v[6:9]
	v_mfma_i32_16x16x64_i8 v[2:5], v[134:137], v[166:169], v[2:5]
	s_setprio 0
	s_barrier
	s_add_i32 s40, 0, 0x18000
	s_add_i32 s41, 0, 0x1c000
	v_add_u32_e32 v134, s40, v195
	v_add_u32_e32 v158, s41, v195
	s_add_u32 s38, s38, 0x80000
	s_addc_u32 s39, s39, 0
	s_mov_b32 m0, s52
	v_lshl_add_u64 v[228:229], s[38:39], 0, v[196:197]
	global_load_lds_dwordx4 v[228:229], off
	v_lshl_add_u64 v[228:229], s[38:39], 0, v[200:201]
	s_mov_b32 m0, s53
	s_nop 0
	global_load_lds_dwordx4 v[228:229], off
	ds_read_b128 v[114:117], v134
	ds_read_b128 v[122:125], v134 offset:1024
	ds_read_b128 v[130:133], v134 offset:2048
	ds_read_b128 v[134:137], v134 offset:3072
	ds_read_b128 v[146:149], v158
	ds_read_b128 v[150:153], v158 offset:1024
	ds_read_b128 v[154:157], v158 offset:2048
	ds_read_b128 v[158:161], v158 offset:3072
	ds_read_b128 v[162:165], v227 offset:32768
	ds_read_b128 v[166:169], v227 offset:33792
	ds_read_b128 v[170:173], v227 offset:34816
	ds_read_b128 v[174:177], v227 offset:35840
	ds_read_b128 v[178:181], v227 offset:36864
	ds_read_b128 v[182:185], v227 offset:37888
	ds_read_b128 v[186:189], v227 offset:38912
	ds_read_b128 v[190:193], v227 offset:39936
	s_waitcnt vmcnt(8)
	s_waitcnt lgkmcnt(0)
	s_barrier
	s_setprio 1
	s_waitcnt lgkmcnt(0)
	v_mfma_i32_16x16x64_i8 v[142:145], v[114:117], v[162:165], v[142:145]
	v_mfma_i32_16x16x64_i8 v[138:141], v[130:133], v[162:165], v[138:141]
	v_mfma_i32_16x16x64_i8 v[110:113], v[114:117], v[170:173], v[110:113]
	v_mfma_i32_16x16x64_i8 v[106:109], v[130:133], v[170:173], v[106:109]
	v_mfma_i32_16x16x64_i8 v[94:97], v[114:117], v[178:181], v[94:97]
	v_mfma_i32_16x16x64_i8 v[90:93], v[130:133], v[178:181], v[90:93]
	v_mfma_i32_16x16x64_i8 v[78:81], v[114:117], v[186:189], v[78:81]
	v_mfma_i32_16x16x64_i8 v[74:77], v[130:133], v[186:189], v[74:77]
	v_mfma_i32_16x16x64_i8 v[142:145], v[122:125], v[166:169], v[142:145]
	v_mfma_i32_16x16x64_i8 v[138:141], v[134:137], v[166:169], v[138:141]
	v_mfma_i32_16x16x64_i8 v[110:113], v[122:125], v[174:177], v[110:113]
	v_mfma_i32_16x16x64_i8 v[106:109], v[134:137], v[174:177], v[106:109]
	v_mfma_i32_16x16x64_i8 v[94:97], v[122:125], v[182:185], v[94:97]
	v_mfma_i32_16x16x64_i8 v[90:93], v[134:137], v[182:185], v[90:93]
	v_mfma_i32_16x16x64_i8 v[78:81], v[122:125], v[190:193], v[78:81]
	v_mfma_i32_16x16x64_i8 v[74:77], v[134:137], v[190:193], v[74:77]
	s_setprio 0
	s_setprio 1
	v_mfma_i32_16x16x64_i8 v[126:129], v[146:149], v[162:165], v[126:129]
	v_mfma_i32_16x16x64_i8 v[118:121], v[154:157], v[162:165], v[118:121]
	v_mfma_i32_16x16x64_i8 v[102:105], v[146:149], v[170:173], v[102:105]
	v_mfma_i32_16x16x64_i8 v[98:101], v[154:157], v[170:173], v[98:101]
	v_mfma_i32_16x16x64_i8 v[86:89], v[146:149], v[178:181], v[86:89]
	v_mfma_i32_16x16x64_i8 v[82:85], v[154:157], v[178:181], v[82:85]
	v_mfma_i32_16x16x64_i8 v[70:73], v[146:149], v[186:189], v[70:73]
	v_mfma_i32_16x16x64_i8 v[66:69], v[154:157], v[186:189], v[66:69]
	v_mfma_i32_16x16x64_i8 v[126:129], v[150:153], v[166:169], v[126:129]
	v_mfma_i32_16x16x64_i8 v[118:121], v[158:161], v[166:169], v[118:121]
	v_mfma_i32_16x16x64_i8 v[102:105], v[150:153], v[174:177], v[102:105]
	v_mfma_i32_16x16x64_i8 v[98:101], v[158:161], v[174:177], v[98:101]
	v_mfma_i32_16x16x64_i8 v[86:89], v[150:153], v[182:185], v[86:89]
	v_mfma_i32_16x16x64_i8 v[82:85], v[158:161], v[182:185], v[82:85]
	v_mfma_i32_16x16x64_i8 v[70:73], v[150:153], v[190:193], v[70:73]
	v_mfma_i32_16x16x64_i8 v[66:69], v[158:161], v[190:193], v[66:69]
	s_setprio 0
	s_barrier
; #define PG8_STAGE(bufoff, gbase, voff) do { _Pragma("unroll") for (int _i = 0; _i < 2; ++_i) \
;         __builtin_amdgcn_global_load_lds((const unsigned*)((const char*)(gbase) + (voff)[_i]), (LAS unsigned*)(lds + (bufoff) + ldsw + _i * 8192), 16, 0, 0); } while (0)
; #define PG8_LDA(dst, b, h) do { _Pragma("unroll") for (int m = 0; m < 4; ++m) _Pragma("unroll") for (int k = 0; k < 2; ++k) dst[m][k] = *(const LAS bf16x8*)(lds + PG8_SA(b, h) + aoff + m * 2048 + k * 1024); } while (0)
; #define PG8_WAIT_V(n) asm volatile("s_waitcnt vmcnt(" #n ")" ::: "memory")
; template <class Epi, class Sched, bool ALIGN_EPI = true, bool SP2 = true, class Side = NoSide>
; __device__ __forceinline__ void gemm_phase(LAS unsigned char* lds, const Gemm g, const Sched& S, const Epi& E, const Side side = Side()) {
;     ...
;         for (int t = 0; t < nt; t += 2) {
;             const bool last = (t == nt - 2);
;             const char* a1 = cA + (size_t)(t + 1) * kstep;
;             const char* a2 = last ? nA : cA + (size_t)(t + 2) * kstep; const char* b2 = last ? nB : cB + (size_t)(t + 2) * kstep;
;             const char* a3 = a2 + kstep; const char* b3 = b2 + kstep;
;             const bool after_epi = Epi::LOADS && t == 0 && ui > 0;
;             if constexpr (SP2) {
;             PG8_LDB(B0, 0, 0); PG8_LDB(B1, 0, 1); PG8_SCHED; PG8_LDA(At, 0, 0); PG8_STAGE(PG8_SA(1, 1), a1 + hstepA, voffA);
;             if (!after_epi) PG8_WAIT_V(8);
;             PG8_WAIT_L(0); PG8_BAR; PG8_MMA(0, 0, At, B0); PG8_MMA(0, 1, At, B1); PG8_BAR; PG8_SCHED;
;             PG8_LDA(At, 0, 1); PG8_STAGE(PG8_SB(0, 0), b2, voffB); PG8_STAGE(PG8_SB(0, 1), b2 + hstepB, voffB); PG8_STAGE(PG8_SA(0, 0), a2, voffA);
;             if (!after_epi) PG8_WAIT_V(8);
;             PG8_WAIT_L(0); PG8_BAR; PG8_MMA(1, 0, At, B0); PG8_MMA(1, 1, At, B1); PG8_BAR; PG8_SCHED;
;             PG8_LDB(B0, 1, 0); PG8_LDB(B1, 1, 1); PG8_SCHED; PG8_LDA(At, 1, 0); PG8_STAGE(PG8_SA(0, 1), a2 + hstepA, voffA);
;             PG8_WAIT_V(8); PG8_WAIT_L(0); PG8_BAR; PG8_MMA(0, 0, At, B0); PG8_MMA(0, 1, At, B1); PG8_BAR; PG8_SCHED;
;             PG8_LDA(At, 1, 1); PG8_STAGE(PG8_SB(1, 0), b3, voffB); PG8_STAGE(PG8_SB(1, 1), b3 + hstepB, voffB); PG8_STAGE(PG8_SA(1, 0), a3, voffA);
;             PG8_WAIT_V(8); PG8_WAIT_L(0); PG8_BAR; PG8_MMA(1, 0, At, B0); PG8_MMA(1, 1, At, B1); PG8_BAR; PG8_SCHED;
	s_add_i32 s38, s40, s45
	v_lshl_add_u64 v[222:223], v[222:223], 0, s[12:13]
	s_mov_b32 m0, s38
	s_nop 0
	global_load_lds_dwordx4 v[222:223], off
	s_add_i32 m0, s38, 0x2000
	s_add_u32 s36, s36, 0x80080
	v_lshl_add_u64 v[220:221], v[220:221], 0, s[12:13]
	s_addc_u32 s37, s37, 0
	s_add_i32 s38, s41, s45
	global_load_lds_dwordx4 v[220:221], off
	v_lshl_add_u64 v[220:221], s[36:37], 0, v[198:199]
	s_mov_b32 m0, s38
	v_lshl_add_u64 v[216:217], v[216:217], 0, s[12:13]
	global_load_lds_dwordx4 v[220:221], off
	v_lshl_add_u64 v[220:221], s[36:37], 0, v[202:203]
	s_add_i32 m0, s38, 0x2000
	s_nop 0
	global_load_lds_dwordx4 v[220:221], off
	s_mov_b32 m0, s55
	s_nop 0
	global_load_lds_dwordx4 v[216:217], off
	v_lshl_add_u64 v[216:217], v[218:219], 0, s[12:13]
	s_mov_b32 m0, s56
	s_nop 0
	global_load_lds_dwordx4 v[216:217], off
	ds_read_b128 v[162:165], v227 offset:49152
	ds_read_b128 v[166:169], v227 offset:50176
	ds_read_b128 v[170:173], v227 offset:51200
	ds_read_b128 v[174:177], v227 offset:52224
	ds_read_b128 v[178:181], v227 offset:53248
	ds_read_b128 v[182:185], v227 offset:54272
	ds_read_b128 v[186:189], v227 offset:55296
	ds_read_b128 v[190:193], v227 offset:56320
	s_waitcnt vmcnt(8)
	s_waitcnt lgkmcnt(0)
	s_barrier
	s_setprio 1
	s_waitcnt lgkmcnt(0)
	v_mfma_i32_16x16x64_i8 v[62:65], v[114:117], v[162:165], v[62:65]
	v_mfma_i32_16x16x64_i8 v[58:61], v[130:133], v[162:165], v[58:61]
	v_mfma_i32_16x16x64_i8 v[46:49], v[114:117], v[170:173], v[46:49]
	v_mfma_i32_16x16x64_i8 v[42:45], v[130:133], v[170:173], v[42:45]
	v_mfma_i32_16x16x64_i8 v[30:33], v[114:117], v[178:181], v[30:33]
	v_mfma_i32_16x16x64_i8 v[26:29], v[130:133], v[178:181], v[26:29]
	v_mfma_i32_16x16x64_i8 v[14:17], v[114:117], v[186:189], v[14:17]
	v_mfma_i32_16x16x64_i8 v[10:13], v[130:133], v[186:189], v[10:13]
	v_mfma_i32_16x16x64_i8 v[62:65], v[122:125], v[166:169], v[62:65]
	v_mfma_i32_16x16x64_i8 v[58:61], v[134:137], v[166:169], v[58:61]
	v_mfma_i32_16x16x64_i8 v[46:49], v[122:125], v[174:177], v[46:49]
	v_mfma_i32_16x16x64_i8 v[42:45], v[134:137], v[174:177], v[42:45]
	v_mfma_i32_16x16x64_i8 v[30:33], v[122:125], v[182:185], v[30:33]
	v_mfma_i32_16x16x64_i8 v[26:29], v[134:137], v[182:185], v[26:29]
	v_mfma_i32_16x16x64_i8 v[14:17], v[122:125], v[190:193], v[14:17]
	v_mfma_i32_16x16x64_i8 v[10:13], v[134:137], v[190:193], v[10:13]
	s_setprio 0
	s_setprio 1
	v_mfma_i32_16x16x64_i8 v[54:57], v[146:149], v[162:165], v[54:57]
	v_mfma_i32_16x16x64_i8 v[50:53], v[154:157], v[162:165], v[50:53]
	v_mfma_i32_16x16x64_i8 v[38:41], v[146:149], v[170:173], v[38:41]
	v_mfma_i32_16x16x64_i8 v[34:37], v[154:157], v[170:173], v[34:37]
	v_mfma_i32_16x16x64_i8 v[22:25], v[146:149], v[178:181], v[22:25]
	v_mfma_i32_16x16x64_i8 v[18:21], v[154:157], v[178:181], v[18:21]
	v_mfma_i32_16x16x64_i8 v[6:9], v[146:149], v[186:189], v[6:9]
	v_mfma_i32_16x16x64_i8 v[2:5], v[154:157], v[186:189], v[2:5]
	v_mfma_i32_16x16x64_i8 v[54:57], v[150:153], v[166:169], v[54:57]
	v_mfma_i32_16x16x64_i8 v[50:53], v[158:161], v[166:169], v[50:53]
	v_mfma_i32_16x16x64_i8 v[38:41], v[150:153], v[174:177], v[38:41]
	v_mfma_i32_16x16x64_i8 v[34:37], v[158:161], v[174:177], v[34:37]
	v_mfma_i32_16x16x64_i8 v[22:25], v[150:153], v[182:185], v[22:25]
	v_mfma_i32_16x16x64_i8 v[18:21], v[158:161], v[182:185], v[18:21]
	v_mfma_i32_16x16x64_i8 v[6:9], v[150:153], v[190:193], v[6:9]
	v_mfma_i32_16x16x64_i8 v[2:5], v[158:161], v[190:193], v[2:5]
	s_setprio 0
	s_barrier
	s_add_i32 s64, s64, 2
	s_add_u32 s34, s34, 0x100
	s_addc_u32 s35, s35, 0
	s_cmp_gt_u32 s64, 29
	s_cbranch_scc1 .LBB0_1330
.LBB0_1326:
	s_cmp_eq_u32 s34, 0
	s_cselect_b64 s[36:37], -1, 0
	v_lshl_add_u64 v[216:217], v[212:213], 0, s[34:35]
	s_add_i32 m0, s27, 0xc000
	s_nop 0
	global_load_lds_dwordx4 v[216:217], off
	v_lshl_add_u64 v[216:217], v[214:215], 0, s[34:35]
	s_add_i32 m0, s27, 0xe000
	s_and_b64 s[36:37], s[30:31], s[36:37]
	global_load_lds_dwordx4 v[216:217], off
	ds_read_b128 v[146:149], v225
	ds_read_b128 v[150:153], v225 offset:1024
	ds_read_b128 v[154:157], v225 offset:2048
	ds_read_b128 v[158:161], v225 offset:3072
	ds_read_b128 v[114:117], v226
	ds_read_b128 v[122:125], v226 offset:1024
	ds_read_b128 v[130:133], v226 offset:2048
	ds_read_b128 v[134:137], v226 offset:3072
	ds_read_b128 v[186:189], v227
	ds_read_b128 v[190:193], v227 offset:1024
	ds_read_b128 v[178:181], v227 offset:2048
	ds_read_b128 v[182:185], v227 offset:3072
	ds_read_b128 v[170:173], v227 offset:4096
	ds_read_b128 v[174:177], v227 offset:5120
	ds_read_b128 v[162:165], v227 offset:6144
	ds_read_b128 v[166:169], v227 offset:7168
	s_and_b64 vcc, exec, s[36:37]
	s_cbranch_vccnz .LBB0_1328
	s_waitcnt vmcnt(8)
; #define PG8_STAGE(bufoff, gbase, voff) do { _Pragma("unroll") for (int _i = 0; _i < 2; ++_i) \
;         __builtin_amdgcn_global_load_lds((const unsigned*)((const char*)(gbase) + (voff)[_i]), (LAS unsigned*)(lds + (bufoff) + ldsw + _i * 8192), 16, 0, 0); } while (0)
; #define PG8_LDA(dst, b, h) do { _Pragma("unroll") for (int m = 0; m < 4; ++m) _Pragma("unroll") for (int k = 0; k < 2; ++k) dst[m][k] = *(const LAS bf16x8*)(lds + PG8_SA(b, h) + aoff + m * 2048 + k * 1024); } while (0)
; #define PG8_LDB(dst, b, h) do { _Pragma("unroll") for (int n = 0; n < 2; ++n) _Pragma("unroll") for (int k = 0; k < 2; ++k) dst[n][k] = *(const LAS bf16x8*)(lds + PG8_SB(b, h) + boff + n * 2048 + k * 1024); } while (0)
; #define PG8_WAIT_V(n) asm volatile("s_waitcnt vmcnt(" #n ")" ::: "memory")
; #define PG8_WAIT_L(n) asm volatile("s_waitcnt lgkmcnt(" #n ")" ::: "memory")
; #define PG8_BAR __builtin_amdgcn_s_barrier()
; #define PG8_SCHED __builtin_amdgcn_sched_barrier(0)
; template <class Epi, class Sched, bool ALIGN_EPI = true, bool SP2 = true, class Side = NoSide>
; __device__ __forceinline__ void gemm_phase(LAS unsigned char* lds, const Gemm g, const Sched& S, const Epi& E, const Side side = Side()) {
;     ...
;             const bool last = (t == nt - 2);
;             const char* a1 = cA + (size_t)(t + 1) * kstep;
;             const char* a2 = last ? nA : cA + (size_t)(t + 2) * kstep; const char* b2 = last ? nB : cB + (size_t)(t + 2) * kstep;
;             const char* a3 = a2 + kstep; const char* b3 = b2 + kstep;
;             const bool after_epi = Epi::LOADS && t == 0 && ui > 0;
;             if constexpr (SP2) {
;             PG8_LDB(B0, 0, 0); PG8_LDB(B1, 0, 1); PG8_SCHED; PG8_LDA(At, 0, 0); PG8_STAGE(PG8_SA(1, 1), a1 + hstepA, voffA);
;             if (!after_epi) PG8_WAIT_V(8);
;             PG8_WAIT_L(0); PG8_BAR; PG8_MMA(0, 0, At, B0); PG8_MMA(0, 1, At, B1); PG8_BAR; PG8_SCHED;
;             PG8_LDA(At, 0, 1); PG8_STAGE(PG8_SB(0, 0), b2, voffB); PG8_STAGE(PG8_SB(0, 1), b2 + hstepB, voffB); PG8_STAGE(PG8_SA(0, 0), a2, voffA);
;             if (!after_epi) PG8_WAIT_V(8);
.LBB0_1328:
	s_xor_b64 s[40:41], s[36:37], -1
	s_add_u32 s36, s28, s34
	s_addc_u32 s37, s29, s35
	s_add_u32 s36, s36, 0x100
	s_addc_u32 s37, s37, 0
	s_add_u32 s65, s62, s34
	s_addc_u32 s66, s63, s35
	s_waitcnt lgkmcnt(0)
	s_cmpk_eq_i32 s34, 0xf00
	s_cselect_b32 s39, s21, s37
	s_cselect_b32 s38, s60, s36
	s_cselect_b32 s37, s17, s66
	s_cselect_b32 s36, s61, s65
	s_barrier
	s_setprio 1
	s_waitcnt lgkmcnt(0)
	v_mfma_i32_16x16x64_i8 v[142:145], v[146:149], v[186:189], v[142:145]
	v_mfma_i32_16x16x64_i8 v[138:141], v[154:157], v[186:189], v[138:141]
	v_mfma_i32_16x16x64_i8 v[110:113], v[146:149], v[178:181], v[110:113]
	v_mfma_i32_16x16x64_i8 v[106:109], v[154:157], v[178:181], v[106:109]
	v_mfma_i32_16x16x64_i8 v[94:97], v[146:149], v[170:173], v[94:97]
	v_mfma_i32_16x16x64_i8 v[90:93], v[154:157], v[170:173], v[90:93]
	v_mfma_i32_16x16x64_i8 v[78:81], v[146:149], v[162:165], v[78:81]
	v_mfma_i32_16x16x64_i8 v[74:77], v[154:157], v[162:165], v[74:77]
	v_mfma_i32_16x16x64_i8 v[142:145], v[150:153], v[190:193], v[142:145]
	v_mfma_i32_16x16x64_i8 v[138:141], v[158:161], v[190:193], v[138:141]
	v_mfma_i32_16x16x64_i8 v[110:113], v[150:153], v[182:185], v[110:113]
	v_mfma_i32_16x16x64_i8 v[106:109], v[158:161], v[182:185], v[106:109]
	v_mfma_i32_16x16x64_i8 v[94:97], v[150:153], v[174:177], v[94:97]
	v_mfma_i32_16x16x64_i8 v[90:93], v[158:161], v[174:177], v[90:93]
	v_mfma_i32_16x16x64_i8 v[78:81], v[150:153], v[166:169], v[78:81]
	v_mfma_i32_16x16x64_i8 v[74:77], v[158:161], v[166:169], v[74:77]
	s_setprio 0
	s_setprio 1
	v_mfma_i32_16x16x64_i8 v[126:129], v[114:117], v[186:189], v[126:129]
	v_mfma_i32_16x16x64_i8 v[118:121], v[130:133], v[186:189], v[118:121]
	v_mfma_i32_16x16x64_i8 v[102:105], v[114:117], v[178:181], v[102:105]
	v_mfma_i32_16x16x64_i8 v[98:101], v[130:133], v[178:181], v[98:101]
	v_mfma_i32_16x16x64_i8 v[86:89], v[114:117], v[170:173], v[86:89]
	v_mfma_i32_16x16x64_i8 v[82:85], v[130:133], v[170:173], v[82:85]
	v_mfma_i32_16x16x64_i8 v[70:73], v[114:117], v[162:165], v[70:73]
	v_mfma_i32_16x16x64_i8 v[66:69], v[130:133], v[162:165], v[66:69]
	v_mfma_i32_16x16x64_i8 v[126:129], v[122:125], v[190:193], v[126:129]
	v_mfma_i32_16x16x64_i8 v[118:121], v[134:137], v[190:193], v[118:121]
	v_mfma_i32_16x16x64_i8 v[102:105], v[122:125], v[182:185], v[102:105]
	v_mfma_i32_16x16x64_i8 v[98:101], v[134:137], v[182:185], v[98:101]
	v_mfma_i32_16x16x64_i8 v[86:89], v[122:125], v[174:177], v[86:89]
	v_mfma_i32_16x16x64_i8 v[82:85], v[134:137], v[174:177], v[82:85]
	v_mfma_i32_16x16x64_i8 v[70:73], v[122:125], v[166:169], v[70:73]
	v_mfma_i32_16x16x64_i8 v[66:69], v[134:137], v[166:169], v[66:69]
	s_setprio 0
	s_barrier
	s_mov_b32 m0, s47
	v_lshl_add_u64 v[222:223], s[36:37], 0, v[198:199]
	s_add_u32 s66, s36, 0x80000
	global_load_lds_dwordx4 v[222:223], off
	v_lshl_add_u64 v[220:221], s[36:37], 0, v[202:203]
	s_mov_b32 m0, s48
	s_addc_u32 s67, s37, 0
	global_load_lds_dwordx4 v[220:221], off
	v_lshl_add_u64 v[216:217], s[66:67], 0, v[198:199]
	s_mov_b32 m0, s49
	v_lshl_add_u64 v[218:219], s[38:39], 0, v[200:201]
	global_load_lds_dwordx4 v[216:217], off
	v_lshl_add_u64 v[216:217], s[66:67], 0, v[202:203]
	s_mov_b32 m0, s50
	s_andn2_b64 vcc, exec, s[40:41]
	global_load_lds_dwordx4 v[216:217], off
	v_lshl_add_u64 v[216:217], s[38:39], 0, v[196:197]
	s_mov_b32 m0, s27
	s_nop 0
	global_load_lds_dwordx4 v[216:217], off
	s_mov_b32 m0, s51
	s_nop 0
	global_load_lds_dwordx4 v[218:219], off
	ds_read_b128 v[186:189], v227 offset:16384
	ds_read_b128 v[190:193], v227 offset:17408
	ds_read_b128 v[178:181], v227 offset:18432
	ds_read_b128 v[182:185], v227 offset:19456
	ds_read_b128 v[170:173], v227 offset:20480
	ds_read_b128 v[174:177], v227 offset:21504
	ds_read_b128 v[162:165], v227 offset:22528
	ds_read_b128 v[166:169], v227 offset:23552
	s_cbranch_vccnz .LBB0_1325
	s_waitcnt vmcnt(8)
	s_branch .LBB0_1325

; #define PG8_STAGE(bufoff, gbase, voff) do { _Pragma("unroll") for (int _i = 0; _i < 2; ++_i) \
;         __builtin_amdgcn_global_load_lds((const unsigned*)((const char*)(gbase) + (voff)[_i]), (LAS unsigned*)(lds + (bufoff) + ldsw + _i * 8192), 16, 0, 0); } while (0)
; #define PG8_LDA(dst, b, h) do { _Pragma("unroll") for (int m = 0; m < 4; ++m) _Pragma("unroll") for (int k = 0; k < 2; ++k) dst[m][k] = *(const LAS bf16x8*)(lds + PG8_SA(b, h) + aoff + m * 2048 + k * 1024); } while (0)
; #define PG8_LDB(dst, b, h) do { _Pragma("unroll") for (int n = 0; n < 2; ++n) _Pragma("unroll") for (int k = 0; k < 2; ++k) dst[n][k] = *(const LAS bf16x8*)(lds + PG8_SB(b, h) + boff + n * 2048 + k * 1024); } while (0)
; #define PG8_WAIT_V(n) asm volatile("s_waitcnt vmcnt(" #n ")" ::: "memory")
; #define PG8_WAIT_L(n) asm volatile("s_waitcnt lgkmcnt(" #n ")" ::: "memory")
; #define PG8_BAR __builtin_amdgcn_s_barrier()
; #define PG8_SCHED __builtin_amdgcn_sched_barrier(0)
; template <class Epi, class Sched, bool ALIGN_EPI = true, bool SP2 = true, class Side = NoSide>
; __device__ __forceinline__ void gemm_phase(LAS unsigned char* lds, const Gemm g, const Sched& S, const Epi& E, const Side side = Side()) {
;     ...
;             PG8_LDA(At, 0, 1); PG8_STAGE(PG8_SB(0, 0), b2, voffB); PG8_STAGE(PG8_SB(0, 1), b2 + hstepB, voffB); PG8_STAGE(PG8_SA(0, 0), a2, voffA);
;             if (!after_epi) PG8_WAIT_V(8);
;             PG8_WAIT_L(0); PG8_BAR; PG8_MMA(1, 0, At, B0); PG8_MMA(1, 1, At, B1); PG8_BAR; PG8_SCHED;
;             PG8_LDB(B0, 1, 0); PG8_LDB(B1, 1, 1); PG8_SCHED; PG8_LDA(At, 1, 0); PG8_STAGE(PG8_SA(0, 1), a2 + hstepA, voffA);
;             PG8_WAIT_V(8); PG8_WAIT_L(0); PG8_BAR; PG8_MMA(0, 0, At, B0); PG8_MMA(0, 1, At, B1); PG8_BAR; PG8_SCHED;
.LBB0_1730:
	s_waitcnt lgkmcnt(0)
	s_barrier
	s_setprio 1
	s_waitcnt lgkmcnt(0)
	v_mfma_i32_16x16x64_i8 v[68:71], v[144:147], v[184:187], v[68:71]
	v_mfma_i32_16x16x64_i8 v[64:67], v[152:155], v[184:187], v[64:67]
	v_mfma_i32_16x16x64_i8 v[44:47], v[144:147], v[176:179], v[44:47]
	v_mfma_i32_16x16x64_i8 v[40:43], v[152:155], v[176:179], v[40:43]
	v_mfma_i32_16x16x64_i8 v[28:31], v[144:147], v[168:171], v[28:31]
	v_mfma_i32_16x16x64_i8 v[24:27], v[152:155], v[168:171], v[24:27]
	v_mfma_i32_16x16x64_i8 v[12:15], v[144:147], v[160:163], v[12:15]
	v_mfma_i32_16x16x64_i8 v[8:11], v[152:155], v[160:163], v[8:11]
	v_mfma_i32_16x16x64_i8 v[68:71], v[148:151], v[188:191], v[68:71]
	v_mfma_i32_16x16x64_i8 v[64:67], v[156:159], v[188:191], v[64:67]
	v_mfma_i32_16x16x64_i8 v[44:47], v[148:151], v[180:183], v[44:47]
	v_mfma_i32_16x16x64_i8 v[40:43], v[156:159], v[180:183], v[40:43]
	v_mfma_i32_16x16x64_i8 v[28:31], v[148:151], v[172:175], v[28:31]
	v_mfma_i32_16x16x64_i8 v[24:27], v[156:159], v[172:175], v[24:27]
	v_mfma_i32_16x16x64_i8 v[12:15], v[148:151], v[164:167], v[12:15]
	v_mfma_i32_16x16x64_i8 v[8:11], v[156:159], v[164:167], v[8:11]
	s_setprio 0
	s_setprio 1
	v_mfma_i32_16x16x64_i8 v[52:55], v[72:75], v[184:187], v[52:55]
	v_mfma_i32_16x16x64_i8 v[48:51], v[136:139], v[184:187], v[48:51]
	v_mfma_i32_16x16x64_i8 v[36:39], v[72:75], v[176:179], v[36:39]
	v_mfma_i32_16x16x64_i8 v[32:35], v[136:139], v[176:179], v[32:35]
	v_mfma_i32_16x16x64_i8 v[20:23], v[72:75], v[168:171], v[20:23]
	v_mfma_i32_16x16x64_i8 v[16:19], v[136:139], v[168:171], v[16:19]
	v_mfma_i32_16x16x64_i8 v[4:7], v[72:75], v[160:163], v[4:7]
	v_mfma_i32_16x16x64_i8 v[0:3], v[136:139], v[160:163], v[0:3]
	v_mfma_i32_16x16x64_i8 v[52:55], v[76:79], v[188:191], v[52:55]
	v_mfma_i32_16x16x64_i8 v[48:51], v[140:143], v[188:191], v[48:51]
	v_mfma_i32_16x16x64_i8 v[36:39], v[76:79], v[180:183], v[36:39]
	v_mfma_i32_16x16x64_i8 v[32:35], v[140:143], v[180:183], v[32:35]
	v_mfma_i32_16x16x64_i8 v[20:23], v[76:79], v[172:175], v[20:23]
	v_mfma_i32_16x16x64_i8 v[16:19], v[140:143], v[172:175], v[16:19]
	v_mfma_i32_16x16x64_i8 v[4:7], v[76:79], v[164:167], v[4:7]
	v_mfma_i32_16x16x64_i8 v[0:3], v[140:143], v[164:167], v[0:3]
	s_setprio 0
	s_barrier
	s_add_i32 s42, 0, 0x18000
	s_add_i32 s43, 0, 0x1c000
	v_add_u32_e32 v140, s42, v222
	v_add_u32_e32 v156, s43, v222
	s_add_u32 s40, s40, 0x80000
	s_addc_u32 s41, s41, 0
	s_mov_b32 m0, s54
	v_lshl_add_u64 v[228:229], s[40:41], 0, v[192:193]
	global_load_lds_dwordx4 v[228:229], off
	v_lshl_add_u64 v[228:229], s[40:41], 0, v[198:199]
	s_mov_b32 m0, s55
	s_nop 0
	global_load_lds_dwordx4 v[228:229], off
	ds_read_b128 v[72:75], v140
	ds_read_b128 v[76:79], v140 offset:1024
	ds_read_b128 v[136:139], v140 offset:2048
	ds_read_b128 v[140:143], v140 offset:3072
	ds_read_b128 v[144:147], v156
	ds_read_b128 v[148:151], v156 offset:1024
	ds_read_b128 v[152:155], v156 offset:2048
	ds_read_b128 v[156:159], v156 offset:3072
	ds_read_b128 v[160:163], v226 offset:32768
	ds_read_b128 v[164:167], v226 offset:33792
	ds_read_b128 v[168:171], v226 offset:34816
	ds_read_b128 v[172:175], v226 offset:35840
	ds_read_b128 v[176:179], v226 offset:36864
	ds_read_b128 v[180:183], v226 offset:37888
	ds_read_b128 v[184:187], v226 offset:38912
	ds_read_b128 v[188:191], v226 offset:39936
	s_waitcnt vmcnt(8)
	s_waitcnt lgkmcnt(0)
	s_barrier
	s_setprio 1
	s_waitcnt lgkmcnt(0)
	v_mfma_i32_16x16x64_i8 v[60:63], v[72:75], v[160:163], v[60:63]
	v_mfma_i32_16x16x64_i8 v[56:59], v[136:139], v[160:163], v[56:59]
	v_mfma_i32_16x16x64_i8 v[124:127], v[72:75], v[168:171], v[124:127]
	v_mfma_i32_16x16x64_i8 v[120:123], v[136:139], v[168:171], v[120:123]
	v_mfma_i32_16x16x64_i8 v[108:111], v[72:75], v[176:179], v[108:111]
	v_mfma_i32_16x16x64_i8 v[104:107], v[136:139], v[176:179], v[104:107]
	v_mfma_i32_16x16x64_i8 v[92:95], v[72:75], v[184:187], v[92:95]
	v_mfma_i32_16x16x64_i8 v[88:91], v[136:139], v[184:187], v[88:91]
	v_mfma_i32_16x16x64_i8 v[60:63], v[76:79], v[164:167], v[60:63]
	v_mfma_i32_16x16x64_i8 v[56:59], v[140:143], v[164:167], v[56:59]
	v_mfma_i32_16x16x64_i8 v[124:127], v[76:79], v[172:175], v[124:127]
	v_mfma_i32_16x16x64_i8 v[120:123], v[140:143], v[172:175], v[120:123]
	v_mfma_i32_16x16x64_i8 v[108:111], v[76:79], v[180:183], v[108:111]
	v_mfma_i32_16x16x64_i8 v[104:107], v[140:143], v[180:183], v[104:107]
	v_mfma_i32_16x16x64_i8 v[92:95], v[76:79], v[188:191], v[92:95]
	v_mfma_i32_16x16x64_i8 v[88:91], v[140:143], v[188:191], v[88:91]
	s_setprio 0
	s_setprio 1
	v_mfma_i32_16x16x64_i8 v[132:135], v[144:147], v[160:163], v[132:135]
	v_mfma_i32_16x16x64_i8 v[128:131], v[152:155], v[160:163], v[128:131]
	v_mfma_i32_16x16x64_i8 v[116:119], v[144:147], v[168:171], v[116:119]
	v_mfma_i32_16x16x64_i8 v[112:115], v[152:155], v[168:171], v[112:115]
	v_mfma_i32_16x16x64_i8 v[100:103], v[144:147], v[176:179], v[100:103]
	v_mfma_i32_16x16x64_i8 v[96:99], v[152:155], v[176:179], v[96:99]
	v_mfma_i32_16x16x64_i8 v[84:87], v[144:147], v[184:187], v[84:87]
	v_mfma_i32_16x16x64_i8 v[80:83], v[152:155], v[184:187], v[80:83]
	v_mfma_i32_16x16x64_i8 v[132:135], v[148:151], v[164:167], v[132:135]
	v_mfma_i32_16x16x64_i8 v[128:131], v[156:159], v[164:167], v[128:131]
	v_mfma_i32_16x16x64_i8 v[116:119], v[148:151], v[172:175], v[116:119]
	v_mfma_i32_16x16x64_i8 v[112:115], v[156:159], v[172:175], v[112:115]
	v_mfma_i32_16x16x64_i8 v[100:103], v[148:151], v[180:183], v[100:103]
	v_mfma_i32_16x16x64_i8 v[96:99], v[156:159], v[180:183], v[96:99]
	v_mfma_i32_16x16x64_i8 v[84:87], v[148:151], v[188:191], v[84:87]
	v_mfma_i32_16x16x64_i8 v[80:83], v[156:159], v[188:191], v[80:83]
	s_setprio 0
	s_barrier
; #define PG8_STAGE(bufoff, gbase, voff) do { _Pragma("unroll") for (int _i = 0; _i < 2; ++_i) \
;         __builtin_amdgcn_global_load_lds((const unsigned*)((const char*)(gbase) + (voff)[_i]), (LAS unsigned*)(lds + (bufoff) + ldsw + _i * 8192), 16, 0, 0); } while (0)
; #define PG8_LDA(dst, b, h) do { _Pragma("unroll") for (int m = 0; m < 4; ++m) _Pragma("unroll") for (int k = 0; k < 2; ++k) dst[m][k] = *(const LAS bf16x8*)(lds + PG8_SA(b, h) + aoff + m * 2048 + k * 1024); } while (0)
; #define PG8_WAIT_V(n) asm volatile("s_waitcnt vmcnt(" #n ")" ::: "memory")
; template <class Epi, class Sched, bool ALIGN_EPI = true, bool SP2 = true, class Side = NoSide>
; __device__ __forceinline__ void gemm_phase(LAS unsigned char* lds, const Gemm g, const Sched& S, const Epi& E, const Side side = Side()) {
;     ...
;         for (int t = 0; t < nt; t += 2) {
;             const bool last = (t == nt - 2);
;             const char* a1 = cA + (size_t)(t + 1) * kstep;
;             const char* a2 = last ? nA : cA + (size_t)(t + 2) * kstep; const char* b2 = last ? nB : cB + (size_t)(t + 2) * kstep;
;             const char* a3 = a2 + kstep; const char* b3 = b2 + kstep;
;             const bool after_epi = Epi::LOADS && t == 0 && ui > 0;
;             if constexpr (SP2) {
;             PG8_LDB(B0, 0, 0); PG8_LDB(B1, 0, 1); PG8_SCHED; PG8_LDA(At, 0, 0); PG8_STAGE(PG8_SA(1, 1), a1 + hstepA, voffA);
;             if (!after_epi) PG8_WAIT_V(8);
;             PG8_WAIT_L(0); PG8_BAR; PG8_MMA(0, 0, At, B0); PG8_MMA(0, 1, At, B1); PG8_BAR; PG8_SCHED;
;             PG8_LDA(At, 0, 1); PG8_STAGE(PG8_SB(0, 0), b2, voffB); PG8_STAGE(PG8_SB(0, 1), b2 + hstepB, voffB); PG8_STAGE(PG8_SA(0, 0), a2, voffA);
;             if (!after_epi) PG8_WAIT_V(8);
;             PG8_WAIT_L(0); PG8_BAR; PG8_MMA(1, 0, At, B0); PG8_MMA(1, 1, At, B1); PG8_BAR; PG8_SCHED;
;             PG8_LDB(B0, 1, 0); PG8_LDB(B1, 1, 1); PG8_SCHED; PG8_LDA(At, 1, 0); PG8_STAGE(PG8_SA(0, 1), a2 + hstepA, voffA);
;             PG8_WAIT_V(8); PG8_WAIT_L(0); PG8_BAR; PG8_MMA(0, 0, At, B0); PG8_MMA(0, 1, At, B1); PG8_BAR; PG8_SCHED;
;             PG8_LDA(At, 1, 1); PG8_STAGE(PG8_SB(1, 0), b3, voffB); PG8_STAGE(PG8_SB(1, 1), b3 + hstepB, voffB); PG8_STAGE(PG8_SA(1, 0), a3, voffA);
;             PG8_WAIT_V(8); PG8_WAIT_L(0); PG8_BAR; PG8_MMA(1, 0, At, B0); PG8_MMA(1, 1, At, B1); PG8_BAR; PG8_SCHED;
	s_add_i32 s40, s42, s47
	v_lshl_add_u64 v[220:221], v[220:221], 0, s[12:13]
	s_mov_b32 m0, s40
	s_nop 0
	global_load_lds_dwordx4 v[220:221], off
	s_add_i32 m0, s40, 0x2000
	s_add_u32 s38, s38, 0x80080
	v_lshl_add_u64 v[218:219], v[218:219], 0, s[12:13]
	s_addc_u32 s39, s39, 0
	s_add_i32 s40, s43, s47
	global_load_lds_dwordx4 v[218:219], off
	v_lshl_add_u64 v[218:219], s[38:39], 0, v[196:197]
	s_mov_b32 m0, s40
	v_lshl_add_u64 v[214:215], v[214:215], 0, s[12:13]
	global_load_lds_dwordx4 v[218:219], off
	v_lshl_add_u64 v[218:219], s[38:39], 0, v[200:201]
	s_add_i32 m0, s40, 0x2000
	s_nop 0
	global_load_lds_dwordx4 v[218:219], off
	s_mov_b32 m0, s57
	s_nop 0
	global_load_lds_dwordx4 v[214:215], off
	v_lshl_add_u64 v[214:215], v[216:217], 0, s[12:13]
	s_mov_b32 m0, s58
	s_nop 0
	global_load_lds_dwordx4 v[214:215], off
	ds_read_b128 v[160:163], v226 offset:49152
	ds_read_b128 v[164:167], v226 offset:50176
	ds_read_b128 v[168:171], v226 offset:51200
	ds_read_b128 v[172:175], v226 offset:52224
	ds_read_b128 v[176:179], v226 offset:53248
	ds_read_b128 v[180:183], v226 offset:54272
	ds_read_b128 v[184:187], v226 offset:55296
	ds_read_b128 v[188:191], v226 offset:56320
	s_waitcnt vmcnt(8)
	s_waitcnt lgkmcnt(0)
	s_barrier
	s_setprio 1
	s_waitcnt lgkmcnt(0)
	v_mfma_i32_16x16x64_i8 v[68:71], v[72:75], v[160:163], v[68:71]
	v_mfma_i32_16x16x64_i8 v[64:67], v[136:139], v[160:163], v[64:67]
	v_mfma_i32_16x16x64_i8 v[44:47], v[72:75], v[168:171], v[44:47]
	v_mfma_i32_16x16x64_i8 v[40:43], v[136:139], v[168:171], v[40:43]
	v_mfma_i32_16x16x64_i8 v[28:31], v[72:75], v[176:179], v[28:31]
	v_mfma_i32_16x16x64_i8 v[24:27], v[136:139], v[176:179], v[24:27]
	v_mfma_i32_16x16x64_i8 v[12:15], v[72:75], v[184:187], v[12:15]
	v_mfma_i32_16x16x64_i8 v[8:11], v[136:139], v[184:187], v[8:11]
	v_mfma_i32_16x16x64_i8 v[68:71], v[76:79], v[164:167], v[68:71]
	v_mfma_i32_16x16x64_i8 v[64:67], v[140:143], v[164:167], v[64:67]
	v_mfma_i32_16x16x64_i8 v[44:47], v[76:79], v[172:175], v[44:47]
	v_mfma_i32_16x16x64_i8 v[40:43], v[140:143], v[172:175], v[40:43]
	v_mfma_i32_16x16x64_i8 v[28:31], v[76:79], v[180:183], v[28:31]
	v_mfma_i32_16x16x64_i8 v[24:27], v[140:143], v[180:183], v[24:27]
	v_mfma_i32_16x16x64_i8 v[12:15], v[76:79], v[188:191], v[12:15]
	v_mfma_i32_16x16x64_i8 v[8:11], v[140:143], v[188:191], v[8:11]
	s_setprio 0
	s_setprio 1
	v_mfma_i32_16x16x64_i8 v[52:55], v[144:147], v[160:163], v[52:55]
	v_mfma_i32_16x16x64_i8 v[48:51], v[152:155], v[160:163], v[48:51]
	v_mfma_i32_16x16x64_i8 v[36:39], v[144:147], v[168:171], v[36:39]
	v_mfma_i32_16x16x64_i8 v[32:35], v[152:155], v[168:171], v[32:35]
	v_mfma_i32_16x16x64_i8 v[20:23], v[144:147], v[176:179], v[20:23]
	v_mfma_i32_16x16x64_i8 v[16:19], v[152:155], v[176:179], v[16:19]
	v_mfma_i32_16x16x64_i8 v[4:7], v[144:147], v[184:187], v[4:7]
	v_mfma_i32_16x16x64_i8 v[0:3], v[152:155], v[184:187], v[0:3]
	v_mfma_i32_16x16x64_i8 v[52:55], v[148:151], v[164:167], v[52:55]
	v_mfma_i32_16x16x64_i8 v[48:51], v[156:159], v[164:167], v[48:51]
	v_mfma_i32_16x16x64_i8 v[36:39], v[148:151], v[172:175], v[36:39]
	v_mfma_i32_16x16x64_i8 v[32:35], v[156:159], v[172:175], v[32:35]
	v_mfma_i32_16x16x64_i8 v[20:23], v[148:151], v[180:183], v[20:23]
	v_mfma_i32_16x16x64_i8 v[16:19], v[156:159], v[180:183], v[16:19]
	v_mfma_i32_16x16x64_i8 v[4:7], v[148:151], v[188:191], v[4:7]
	v_mfma_i32_16x16x64_i8 v[0:3], v[156:159], v[188:191], v[0:3]
	s_setprio 0
	s_barrier
	s_add_i32 s65, s65, 2
	s_add_u32 s36, s36, 0x100
	s_addc_u32 s37, s37, 0
	s_cmp_gt_u32 s65, 29
	s_cbranch_scc1 .LBB0_1735
.LBB0_1731:
	s_cmp_eq_u32 s36, 0
	s_cselect_b64 s[38:39], -1, 0
	v_lshl_add_u64 v[214:215], v[210:211], 0, s[36:37]
	s_add_i32 m0, s29, 0xc000
	s_nop 0
	global_load_lds_dwordx4 v[214:215], off
	v_lshl_add_u64 v[214:215], v[212:213], 0, s[36:37]
	s_add_i32 m0, s29, 0xe000
	s_and_b64 s[38:39], s[34:35], s[38:39]
	global_load_lds_dwordx4 v[214:215], off
	ds_read_b128 v[144:147], v224
	ds_read_b128 v[148:151], v224 offset:1024
	ds_read_b128 v[152:155], v224 offset:2048
	ds_read_b128 v[156:159], v224 offset:3072
	ds_read_b128 v[72:75], v225
	ds_read_b128 v[76:79], v225 offset:1024
	ds_read_b128 v[136:139], v225 offset:2048
	ds_read_b128 v[140:143], v225 offset:3072
	ds_read_b128 v[184:187], v226
	ds_read_b128 v[188:191], v226 offset:1024
	ds_read_b128 v[176:179], v226 offset:2048
	ds_read_b128 v[180:183], v226 offset:3072
	ds_read_b128 v[168:171], v226 offset:4096
	ds_read_b128 v[172:175], v226 offset:5120
	ds_read_b128 v[160:163], v226 offset:6144
	ds_read_b128 v[164:167], v226 offset:7168
	s_and_b64 vcc, exec, s[38:39]
	s_cbranch_vccnz .LBB0_1733
	s_waitcnt vmcnt(8)
; #define PG8_STAGE(bufoff, gbase, voff) do { _Pragma("unroll") for (int _i = 0; _i < 2; ++_i) \
;         __builtin_amdgcn_global_load_lds((const unsigned*)((const char*)(gbase) + (voff)[_i]), (LAS unsigned*)(lds + (bufoff) + ldsw + _i * 8192), 16, 0, 0); } while (0)
; #define PG8_LDA(dst, b, h) do { _Pragma("unroll") for (int m = 0; m < 4; ++m) _Pragma("unroll") for (int k = 0; k < 2; ++k) dst[m][k] = *(const LAS bf16x8*)(lds + PG8_SA(b, h) + aoff + m * 2048 + k * 1024); } while (0)
; #define PG8_LDB(dst, b, h) do { _Pragma("unroll") for (int n = 0; n < 2; ++n) _Pragma("unroll") for (int k = 0; k < 2; ++k) dst[n][k] = *(const LAS bf16x8*)(lds + PG8_SB(b, h) + boff + n * 2048 + k * 1024); } while (0)
; #define PG8_WAIT_V(n) asm volatile("s_waitcnt vmcnt(" #n ")" ::: "memory")
; #define PG8_WAIT_L(n) asm volatile("s_waitcnt lgkmcnt(" #n ")" ::: "memory")
; #define PG8_BAR __builtin_amdgcn_s_barrier()
; #define PG8_SCHED __builtin_amdgcn_sched_barrier(0)
; template <class Epi, class Sched, bool ALIGN_EPI = true, bool SP2 = true, class Side = NoSide>
; __device__ __forceinline__ void gemm_phase(LAS unsigned char* lds, const Gemm g, const Sched& S, const Epi& E, const Side side = Side()) {
;     ...
;             const bool last = (t == nt - 2);
;             const char* a1 = cA + (size_t)(t + 1) * kstep;
;             const char* a2 = last ? nA : cA + (size_t)(t + 2) * kstep; const char* b2 = last ? nB : cB + (size_t)(t + 2) * kstep;
;             const char* a3 = a2 + kstep; const char* b3 = b2 + kstep;
;             const bool after_epi = Epi::LOADS && t == 0 && ui > 0;
;             if constexpr (SP2) {
;             PG8_LDB(B0, 0, 0); PG8_LDB(B1, 0, 1); PG8_SCHED; PG8_LDA(At, 0, 0); PG8_STAGE(PG8_SA(1, 1), a1 + hstepA, voffA);
;             if (!after_epi) PG8_WAIT_V(8);
;             PG8_WAIT_L(0); PG8_BAR; PG8_MMA(0, 0, At, B0); PG8_MMA(0, 1, At, B1); PG8_BAR; PG8_SCHED;
;             PG8_LDA(At, 0, 1); PG8_STAGE(PG8_SB(0, 0), b2, voffB); PG8_STAGE(PG8_SB(0, 1), b2 + hstepB, voffB); PG8_STAGE(PG8_SA(0, 0), a2, voffA);
;             if (!after_epi) PG8_WAIT_V(8);
.LBB0_1733:
	s_xor_b64 s[42:43], s[38:39], -1
	s_add_u32 s38, s30, s36
	s_addc_u32 s39, s31, s37
	s_add_u32 s38, s38, 0x100
	s_addc_u32 s39, s39, 0
	s_add_u32 s66, s63, s36
	s_addc_u32 s67, s64, s37
	s_waitcnt lgkmcnt(0)
	s_cmpk_eq_i32 s36, 0xf00
	s_cselect_b32 s41, s23, s39
	s_cselect_b32 s40, s61, s38
	s_cselect_b32 s39, s21, s67
	s_cselect_b32 s38, s62, s66
	s_barrier
	s_setprio 1
	s_waitcnt lgkmcnt(0)
	v_mfma_i32_16x16x64_i8 v[60:63], v[144:147], v[184:187], v[60:63]
	v_mfma_i32_16x16x64_i8 v[56:59], v[152:155], v[184:187], v[56:59]
	v_mfma_i32_16x16x64_i8 v[124:127], v[144:147], v[176:179], v[124:127]
	v_mfma_i32_16x16x64_i8 v[120:123], v[152:155], v[176:179], v[120:123]
	v_mfma_i32_16x16x64_i8 v[108:111], v[144:147], v[168:171], v[108:111]
	v_mfma_i32_16x16x64_i8 v[104:107], v[152:155], v[168:171], v[104:107]
	v_mfma_i32_16x16x64_i8 v[92:95], v[144:147], v[160:163], v[92:95]
	v_mfma_i32_16x16x64_i8 v[88:91], v[152:155], v[160:163], v[88:91]
	v_mfma_i32_16x16x64_i8 v[60:63], v[148:151], v[188:191], v[60:63]
	v_mfma_i32_16x16x64_i8 v[56:59], v[156:159], v[188:191], v[56:59]
	v_mfma_i32_16x16x64_i8 v[124:127], v[148:151], v[180:183], v[124:127]
	v_mfma_i32_16x16x64_i8 v[120:123], v[156:159], v[180:183], v[120:123]
	v_mfma_i32_16x16x64_i8 v[108:111], v[148:151], v[172:175], v[108:111]
	v_mfma_i32_16x16x64_i8 v[104:107], v[156:159], v[172:175], v[104:107]
	v_mfma_i32_16x16x64_i8 v[92:95], v[148:151], v[164:167], v[92:95]
	v_mfma_i32_16x16x64_i8 v[88:91], v[156:159], v[164:167], v[88:91]
	s_setprio 0
	s_setprio 1
	v_mfma_i32_16x16x64_i8 v[132:135], v[72:75], v[184:187], v[132:135]
	v_mfma_i32_16x16x64_i8 v[128:131], v[136:139], v[184:187], v[128:131]
	v_mfma_i32_16x16x64_i8 v[116:119], v[72:75], v[176:179], v[116:119]
	v_mfma_i32_16x16x64_i8 v[112:115], v[136:139], v[176:179], v[112:115]
	v_mfma_i32_16x16x64_i8 v[100:103], v[72:75], v[168:171], v[100:103]
	v_mfma_i32_16x16x64_i8 v[96:99], v[136:139], v[168:171], v[96:99]
	v_mfma_i32_16x16x64_i8 v[84:87], v[72:75], v[160:163], v[84:87]
	v_mfma_i32_16x16x64_i8 v[80:83], v[136:139], v[160:163], v[80:83]
	v_mfma_i32_16x16x64_i8 v[132:135], v[76:79], v[188:191], v[132:135]
	v_mfma_i32_16x16x64_i8 v[128:131], v[140:143], v[188:191], v[128:131]
	v_mfma_i32_16x16x64_i8 v[116:119], v[76:79], v[180:183], v[116:119]
	v_mfma_i32_16x16x64_i8 v[112:115], v[140:143], v[180:183], v[112:115]
	v_mfma_i32_16x16x64_i8 v[100:103], v[76:79], v[172:175], v[100:103]
	v_mfma_i32_16x16x64_i8 v[96:99], v[140:143], v[172:175], v[96:99]
	v_mfma_i32_16x16x64_i8 v[84:87], v[76:79], v[164:167], v[84:87]
	v_mfma_i32_16x16x64_i8 v[80:83], v[140:143], v[164:167], v[80:83]
	s_setprio 0
	s_barrier
	s_mov_b32 m0, s49
	v_lshl_add_u64 v[220:221], s[38:39], 0, v[196:197]
	s_add_u32 s66, s38, 0x80000
	global_load_lds_dwordx4 v[220:221], off
	v_lshl_add_u64 v[218:219], s[38:39], 0, v[200:201]
	s_mov_b32 m0, s50
	s_addc_u32 s67, s39, 0
	global_load_lds_dwordx4 v[218:219], off
	v_lshl_add_u64 v[214:215], s[66:67], 0, v[196:197]
	s_mov_b32 m0, s51
	v_lshl_add_u64 v[216:217], s[40:41], 0, v[198:199]
	global_load_lds_dwordx4 v[214:215], off
	v_lshl_add_u64 v[214:215], s[66:67], 0, v[200:201]
	s_mov_b32 m0, s52
	s_andn2_b64 vcc, exec, s[42:43]
	global_load_lds_dwordx4 v[214:215], off
	v_lshl_add_u64 v[214:215], s[40:41], 0, v[192:193]
	s_mov_b32 m0, s29
	s_nop 0
	global_load_lds_dwordx4 v[214:215], off
	s_mov_b32 m0, s53
	s_nop 0
	global_load_lds_dwordx4 v[216:217], off
	ds_read_b128 v[184:187], v226 offset:16384
	ds_read_b128 v[188:191], v226 offset:17408
	ds_read_b128 v[176:179], v226 offset:18432
	ds_read_b128 v[180:183], v226 offset:19456
	ds_read_b128 v[168:171], v226 offset:20480
	ds_read_b128 v[172:175], v226 offset:21504
	ds_read_b128 v[160:163], v226 offset:22528
	ds_read_b128 v[164:167], v226 offset:23552
	s_cbranch_vccnz .LBB0_1730
	s_waitcnt vmcnt(8)
	s_branch .LBB0_1730
